# loop-edge edit: the K-loop induction/compare SALU of the eight int8/fp8/fp6 GEMM main loops hoisted above the closing barrier into the last MFMA group (only the branch stays after the barrier)
# speedup vs baseline: 1.0211x; 1.0022x over previous
; #define PG8_STAGE(bufoff, gbase, voff) do { _Pragma("unroll") for (int _i = 0; _i < 2; ++_i) \
;         __builtin_amdgcn_global_load_lds((const unsigned*)((const char*)(gbase) + (voff)[_i]), (LAS unsigned*)(lds + (bufoff) + ldsw + _i * 8192), 16, 0, 0); } while (0)
; #define PG8_LDA(dst, b, h) do { _Pragma("unroll") for (int m = 0; m < 4; ++m) _Pragma("unroll") for (int k = 0; k < 2; ++k) dst[m][k] = *(const LAS bf16x8*)(lds + PG8_SA(b, h) + aoff + m * 2048 + k * 1024); } while (0)
; #define PG8_LDB(dst, b, h) do { _Pragma("unroll") for (int n = 0; n < 2; ++n) _Pragma("unroll") for (int k = 0; k < 2; ++k) dst[n][k] = *(const LAS bf16x8*)(lds + PG8_SB(b, h) + boff + n * 2048 + k * 1024); } while (0)
; #define PG8_MMA(ai, bj, At, Bt) do { __builtin_amdgcn_s_setprio(1); _Pragma("unroll") for (int m = 0; m < 4; ++m) _Pragma("unroll") for (int n = 0; n < 2; ++n) _Pragma("unroll") for (int k = 0; k < 2; ++k) \
;         acc[ai][bj][m][n] = __builtin_amdgcn_mfma_f32_16x16x32_bf16(Bt[n][k], At[m][k], acc[ai][bj][m][n], 0, 0, 0); __builtin_amdgcn_s_setprio(0); } while (0)
; #define PG8_WAIT_V(n) asm volatile("s_waitcnt vmcnt(" #n ")" ::: "memory")
; #define PG8_WAIT_L(n) asm volatile("s_waitcnt lgkmcnt(" #n ")" ::: "memory")
; #define PG8_BAR __builtin_amdgcn_s_barrier()
; #define PG8_SCHED __builtin_amdgcn_sched_barrier(0)
; #define PG8_STAGE(bufoff, gbase, voff) do { _Pragma("unroll") for (int _i = 0; _i < 2; ++_i) \
;         __builtin_amdgcn_global_load_lds((const unsigned*)((const char*)(gbase) + (voff)[_i]), (LAS unsigned*)(lds + (bufoff) + ldsw + _i * 8192), 16, 0, 0); } while (0)
; #define PG8_LDA(dst, b, h) do { _Pragma("unroll") for (int m = 0; m < 4; ++m) PG8_LD1(dst[m], PG8_SA(b, h) + aoff0 + m * 2048, PG8_SA(b, h) + aoff1 + m * 2048); } while (0)
; #define PG8_WAIT_V(n) asm volatile("s_waitcnt vmcnt(" #n ")" ::: "memory")
;     ...
;             PG8_LDB(B0, 0, 0); PG8_LDB(B1, 0, 1); PG8_SCHED; PG8_LDA(At, 0, 0); PG8_STAGE(PG8_SA(1, 1), a1 + hstepA, voffA);
;             PG8_WAIT_V(8); PG8_WAIT_L(0); PG8_BAR; PG8_MMA(0, 0, At, B0); PG8_MMA(0, 1, At, B1); PG8_BAR; PG8_SCHED;
;             PG8_LDA(At, 0, 1); PG8_STAGE(PG8_SB(0, 0), b2, voffB); PG8_STAGE(PG8_SB(0, 1), b2 + hstepB, voffB); PG8_STAGE(PG8_SA(0, 0), a2, voffA);
;             PG8_WAIT_V(8); PG8_WAIT_L(0); PG8_BAR; PG8_MMA(1, 0, At, B0); PG8_MMA(1, 1, At, B1); PG8_BAR; PG8_SCHED;
.LBB0_143:
	ds_read_b128 v[158:161], v187
	ds_read_b128 v[146:149], v188
	ds_read_b128 v[154:157], v195
	ds_read_b128 v[150:153], v196
	ds_read_b128 v[142:145], v189
	ds_read_b128 v[130:133], v190
	ds_read_b128 v[138:141], v197
	ds_read_b128 v[134:137], v198
	s_add_u32 s84, s82, 0x100
	s_addc_u32 s85, s83, 0
	s_cmp_eq_u32 vcc_lo, 12
	s_cselect_b32 s89, s45, s85
	s_cselect_b32 s88, s47, s84
	s_cselect_b32 s87, s75, s95
	s_cselect_b32 s86, s93, s94
	v_lshl_add_u64 v[230:231], s[82:83], 0, v[170:171]
	s_add_i32 m0, s0, 0xc000
	ds_read_b128 v[178:181], v204
	ds_read_b128 v[182:185], v204 offset:2048
	ds_read_b128 v[206:209], v205
	ds_read_b128 v[210:213], v205 offset:2048
	ds_read_b128 v[214:217], v204 offset:4096
	ds_read_b128 v[218:221], v204 offset:6144
	ds_read_b128 v[222:225], v205 offset:4096
	ds_read_b128 v[226:229], v205 offset:6144
	global_load_lds_dwordx4 v[230:231], off
	v_lshl_add_u64 v[230:231], s[82:83], 0, v[172:173]
	s_add_i32 m0, s0, 0xe000
	s_nop 0
	global_load_lds_dwordx4 v[230:231], off
	s_waitcnt vmcnt(8)
	s_waitcnt lgkmcnt(0)
	s_barrier
	s_setprio 1
	s_waitcnt lgkmcnt(0)
	v_mfma_i32_16x16x64_i8 v[126:129], v[158:161], v[178:181], v[126:129]
	v_mfma_i32_16x16x64_i8 v[122:125], v[154:157], v[178:181], v[122:125]
	v_mfma_i32_16x16x64_i8 v[118:121], v[158:161], v[182:185], v[118:121]
	v_mfma_i32_16x16x64_i8 v[114:117], v[154:157], v[182:185], v[114:117]
	v_mfma_i32_16x16x64_i8 v[110:113], v[158:161], v[214:217], v[110:113]
	v_mfma_i32_16x16x64_i8 v[106:109], v[154:157], v[214:217], v[106:109]
	v_mfma_i32_16x16x64_i8 v[102:105], v[158:161], v[218:221], v[102:105]
	v_mfma_i32_16x16x64_i8 v[98:101], v[154:157], v[218:221], v[98:101]
	s_nop 0
	v_mfma_i32_16x16x64_i8 v[126:129], v[146:149], v[206:209], v[126:129]
	v_mfma_i32_16x16x64_i8 v[122:125], v[150:153], v[206:209], v[122:125]
	v_mfma_i32_16x16x64_i8 v[118:121], v[146:149], v[210:213], v[118:121]
	v_mfma_i32_16x16x64_i8 v[114:117], v[150:153], v[210:213], v[114:117]
	v_mfma_i32_16x16x64_i8 v[110:113], v[146:149], v[222:225], v[110:113]
	v_mfma_i32_16x16x64_i8 v[106:109], v[150:153], v[222:225], v[106:109]
	v_mfma_i32_16x16x64_i8 v[102:105], v[146:149], v[226:229], v[102:105]
	v_mfma_i32_16x16x64_i8 v[98:101], v[150:153], v[226:229], v[98:101]
	s_setprio 0
	s_setprio 1
	v_mfma_i32_16x16x64_i8 v[94:97], v[142:145], v[178:181], v[94:97]
	v_mfma_i32_16x16x64_i8 v[90:93], v[138:141], v[178:181], v[90:93]
	v_mfma_i32_16x16x64_i8 v[86:89], v[142:145], v[182:185], v[86:89]
	v_mfma_i32_16x16x64_i8 v[82:85], v[138:141], v[182:185], v[82:85]
	v_mfma_i32_16x16x64_i8 v[78:81], v[142:145], v[214:217], v[78:81]
	v_mfma_i32_16x16x64_i8 v[74:77], v[138:141], v[214:217], v[74:77]
	v_mfma_i32_16x16x64_i8 v[70:73], v[142:145], v[218:221], v[70:73]
	v_mfma_i32_16x16x64_i8 v[66:69], v[138:141], v[218:221], v[66:69]
	s_nop 0
	v_mfma_i32_16x16x64_i8 v[94:97], v[130:133], v[206:209], v[94:97]
	v_mfma_i32_16x16x64_i8 v[90:93], v[134:137], v[206:209], v[90:93]
	v_mfma_i32_16x16x64_i8 v[86:89], v[130:133], v[210:213], v[86:89]
	v_mfma_i32_16x16x64_i8 v[82:85], v[134:137], v[210:213], v[82:85]
	v_mfma_i32_16x16x64_i8 v[78:81], v[130:133], v[222:225], v[78:81]
	v_mfma_i32_16x16x64_i8 v[74:77], v[134:137], v[222:225], v[74:77]
	v_mfma_i32_16x16x64_i8 v[70:73], v[130:133], v[226:229], v[70:73]
	v_mfma_i32_16x16x64_i8 v[66:69], v[134:137], v[226:229], v[66:69]
	s_setprio 0
	s_barrier
	s_mov_b32 m0, s1
	v_lshl_add_u64 v[178:179], s[86:87], 0, v[166:167]
	s_add_u32 s8, s86, 0x40000
	ds_read_b128 v[206:209], v204 offset:16384
	ds_read_b128 v[210:213], v204 offset:18432
	ds_read_b128 v[214:217], v205 offset:16384
	ds_read_b128 v[218:221], v205 offset:18432
	ds_read_b128 v[222:225], v204 offset:20480
	ds_read_b128 v[226:229], v204 offset:22528
	ds_read_b128 v[230:233], v205 offset:20480
	ds_read_b128 v[234:237], v205 offset:22528
	global_load_lds_dwordx4 v[178:179], off
	v_lshl_add_u64 v[180:181], s[86:87], 0, v[162:163]
	s_mov_b32 m0, s10
	s_addc_u32 s9, s87, 0
	global_load_lds_dwordx4 v[180:181], off
	v_lshl_add_u64 v[182:183], s[8:9], 0, v[166:167]
	s_mov_b32 m0, s11
	v_lshl_add_u64 v[184:185], s[88:89], 0, v[164:165]
	global_load_lds_dwordx4 v[182:183], off
	v_lshl_add_u64 v[182:183], s[8:9], 0, v[162:163]
	s_mov_b32 m0, s24
	s_nop 0
	global_load_lds_dwordx4 v[182:183], off
	v_lshl_add_u64 v[182:183], s[88:89], 0, v[168:169]
	s_mov_b32 m0, s0
	s_nop 0
	global_load_lds_dwordx4 v[182:183], off
	s_mov_b32 m0, s25
	s_nop 0
	global_load_lds_dwordx4 v[184:185], off
	s_waitcnt vmcnt(8)
	s_waitcnt lgkmcnt(0)
	s_barrier
; #define PG8_STAGE(bufoff, gbase, voff) do { _Pragma("unroll") for (int _i = 0; _i < 2; ++_i) \
;         __builtin_amdgcn_global_load_lds((const unsigned*)((const char*)(gbase) + (voff)[_i]), (LAS unsigned*)(lds + (bufoff) + ldsw + _i * 8192), 16, 0, 0); } while (0)
; #define PG8_LDA(dst, b, h) do { _Pragma("unroll") for (int m = 0; m < 4; ++m) _Pragma("unroll") for (int k = 0; k < 2; ++k) dst[m][k] = *(const LAS bf16x8*)(lds + PG8_SA(b, h) + aoff + m * 2048 + k * 1024); } while (0)
; #define PG8_LDB(dst, b, h) do { _Pragma("unroll") for (int n = 0; n < 2; ++n) _Pragma("unroll") for (int k = 0; k < 2; ++k) dst[n][k] = *(const LAS bf16x8*)(lds + PG8_SB(b, h) + boff + n * 2048 + k * 1024); } while (0)
; #define PG8_MMA(ai, bj, At, Bt) do { __builtin_amdgcn_s_setprio(1); _Pragma("unroll") for (int m = 0; m < 4; ++m) _Pragma("unroll") for (int n = 0; n < 2; ++n) _Pragma("unroll") for (int k = 0; k < 2; ++k) \
;         acc[ai][bj][m][n] = __builtin_amdgcn_mfma_f32_16x16x32_bf16(Bt[n][k], At[m][k], acc[ai][bj][m][n], 0, 0, 0); __builtin_amdgcn_s_setprio(0); } while (0)
; #define PG8_WAIT_V(n) asm volatile("s_waitcnt vmcnt(" #n ")" ::: "memory")
; #define PG8_WAIT_L(n) asm volatile("s_waitcnt lgkmcnt(" #n ")" ::: "memory")
; #define PG8_BAR __builtin_amdgcn_s_barrier()
; #define PG8_SCHED __builtin_amdgcn_sched_barrier(0)
; #define PG8_STAGE(bufoff, gbase, voff) do { _Pragma("unroll") for (int _i = 0; _i < 2; ++_i) \
;         __builtin_amdgcn_global_load_lds((const unsigned*)((const char*)(gbase) + (voff)[_i]), (LAS unsigned*)(lds + (bufoff) + ldsw + _i * 8192), 16, 0, 0); } while (0)
; #define PG8_LDA(dst, b, h) do { _Pragma("unroll") for (int m = 0; m < 4; ++m) PG8_LD1(dst[m], PG8_SA(b, h) + aoff0 + m * 2048, PG8_SA(b, h) + aoff1 + m * 2048); } while (0)
; #define PG8_WAIT_V(n) asm volatile("s_waitcnt vmcnt(" #n ")" ::: "memory")
;     ...
;             PG8_WAIT_V(8); PG8_WAIT_L(0); PG8_BAR; PG8_MMA(1, 0, At, B0); PG8_MMA(1, 1, At, B1); PG8_BAR; PG8_SCHED;
;             PG8_LDB(B0, 1, 0); PG8_LDB(B1, 1, 1); PG8_SCHED; PG8_LDA(At, 1, 0); PG8_STAGE(PG8_SA(0, 1), a2 + hstepA, voffA);
;             PG8_WAIT_V(8); PG8_WAIT_L(0); PG8_BAR; PG8_MMA(0, 0, At, B0); PG8_MMA(0, 1, At, B1); PG8_BAR; PG8_SCHED;
;             PG8_LDA(At, 1, 1); PG8_STAGE(PG8_SB(1, 0), b3, voffB); PG8_STAGE(PG8_SB(1, 1), b3 + hstepB, voffB); PG8_STAGE(PG8_SA(1, 0), a3, voffA);
	s_setprio 1
	s_waitcnt lgkmcnt(0)
	v_mfma_i32_16x16x64_i8 v[62:65], v[158:161], v[206:209], v[62:65]
	v_mfma_i32_16x16x64_i8 v[58:61], v[154:157], v[206:209], v[58:61]
	v_mfma_i32_16x16x64_i8 v[54:57], v[158:161], v[210:213], v[54:57]
	v_mfma_i32_16x16x64_i8 v[50:53], v[154:157], v[210:213], v[50:53]
	v_mfma_i32_16x16x64_i8 v[46:49], v[158:161], v[222:225], v[46:49]
	v_mfma_i32_16x16x64_i8 v[42:45], v[154:157], v[222:225], v[42:45]
	v_mfma_i32_16x16x64_i8 v[38:41], v[158:161], v[226:229], v[38:41]
	v_mfma_i32_16x16x64_i8 v[34:37], v[154:157], v[226:229], v[34:37]
	s_nop 0
	v_mfma_i32_16x16x64_i8 v[62:65], v[146:149], v[214:217], v[62:65]
	v_mfma_i32_16x16x64_i8 v[58:61], v[150:153], v[214:217], v[58:61]
	v_mfma_i32_16x16x64_i8 v[54:57], v[146:149], v[218:221], v[54:57]
	v_mfma_i32_16x16x64_i8 v[50:53], v[150:153], v[218:221], v[50:53]
	v_mfma_i32_16x16x64_i8 v[46:49], v[146:149], v[230:233], v[46:49]
	v_mfma_i32_16x16x64_i8 v[42:45], v[150:153], v[230:233], v[42:45]
	v_mfma_i32_16x16x64_i8 v[38:41], v[146:149], v[234:237], v[38:41]
	v_mfma_i32_16x16x64_i8 v[34:37], v[150:153], v[234:237], v[34:37]
	s_setprio 0
	s_setprio 1
	v_mfma_i32_16x16x64_i8 v[30:33], v[142:145], v[206:209], v[30:33]
	v_mfma_i32_16x16x64_i8 v[26:29], v[138:141], v[206:209], v[26:29]
	v_mfma_i32_16x16x64_i8 v[22:25], v[142:145], v[210:213], v[22:25]
	v_mfma_i32_16x16x64_i8 v[18:21], v[138:141], v[210:213], v[18:21]
	v_mfma_i32_16x16x64_i8 v[14:17], v[142:145], v[222:225], v[14:17]
	v_mfma_i32_16x16x64_i8 v[10:13], v[138:141], v[222:225], v[10:13]
	v_mfma_i32_16x16x64_i8 v[6:9], v[142:145], v[226:229], v[6:9]
	v_mfma_i32_16x16x64_i8 v[2:5], v[138:141], v[226:229], v[2:5]
	s_nop 0
	v_mfma_i32_16x16x64_i8 v[30:33], v[130:133], v[214:217], v[30:33]
	v_mfma_i32_16x16x64_i8 v[26:29], v[134:137], v[214:217], v[26:29]
	v_mfma_i32_16x16x64_i8 v[22:25], v[130:133], v[218:221], v[22:25]
	v_mfma_i32_16x16x64_i8 v[18:21], v[134:137], v[218:221], v[18:21]
	v_mfma_i32_16x16x64_i8 v[14:17], v[130:133], v[230:233], v[14:17]
	v_mfma_i32_16x16x64_i8 v[10:13], v[134:137], v[230:233], v[10:13]
	v_mfma_i32_16x16x64_i8 v[6:9], v[130:133], v[234:237], v[6:9]
	v_mfma_i32_16x16x64_i8 v[2:5], v[134:137], v[234:237], v[2:5]
	s_setprio 0
	s_barrier
	ds_read_b128 v[130:133], v191
	ds_read_b128 v[134:137], v192
	ds_read_b128 v[138:141], v199
	ds_read_b128 v[142:145], v200
	ds_read_b128 v[146:149], v193
	ds_read_b128 v[150:153], v194
	ds_read_b128 v[154:157], v201
	ds_read_b128 v[158:161], v202
	s_add_u32 s8, s88, 0x40000
	s_addc_u32 s9, s89, 0
	s_mov_b32 m0, s33
	v_lshl_add_u64 v[238:239], s[8:9], 0, v[168:169]
	ds_read_b128 v[206:209], v204 offset:32768
	ds_read_b128 v[210:213], v204 offset:34816
	ds_read_b128 v[214:217], v205 offset:32768
	ds_read_b128 v[218:221], v205 offset:34816
	ds_read_b128 v[222:225], v204 offset:36864
	ds_read_b128 v[226:229], v204 offset:38912
	ds_read_b128 v[230:233], v205 offset:36864
	ds_read_b128 v[234:237], v205 offset:38912
	global_load_lds_dwordx4 v[238:239], off
	v_lshl_add_u64 v[238:239], s[8:9], 0, v[164:165]
	s_mov_b32 m0, s43
	s_nop 0
	global_load_lds_dwordx4 v[238:239], off
	s_waitcnt vmcnt(8)
	s_waitcnt lgkmcnt(0)
	s_barrier
	s_setprio 1
	s_waitcnt lgkmcnt(0)
	v_mfma_i32_16x16x64_i8 v[126:129], v[130:133], v[206:209], v[126:129]
	v_mfma_i32_16x16x64_i8 v[122:125], v[138:141], v[206:209], v[122:125]
	v_mfma_i32_16x16x64_i8 v[118:121], v[130:133], v[210:213], v[118:121]
	v_mfma_i32_16x16x64_i8 v[114:117], v[138:141], v[210:213], v[114:117]
	v_mfma_i32_16x16x64_i8 v[110:113], v[130:133], v[222:225], v[110:113]
	v_mfma_i32_16x16x64_i8 v[106:109], v[138:141], v[222:225], v[106:109]
	v_mfma_i32_16x16x64_i8 v[102:105], v[130:133], v[226:229], v[102:105]
	v_mfma_i32_16x16x64_i8 v[98:101], v[138:141], v[226:229], v[98:101]
	s_nop 0
	v_mfma_i32_16x16x64_i8 v[126:129], v[134:137], v[214:217], v[126:129]
	v_mfma_i32_16x16x64_i8 v[122:125], v[142:145], v[214:217], v[122:125]
	v_mfma_i32_16x16x64_i8 v[118:121], v[134:137], v[218:221], v[118:121]
	v_mfma_i32_16x16x64_i8 v[114:117], v[142:145], v[218:221], v[114:117]
	v_mfma_i32_16x16x64_i8 v[110:113], v[134:137], v[230:233], v[110:113]
	v_mfma_i32_16x16x64_i8 v[106:109], v[142:145], v[230:233], v[106:109]
	v_mfma_i32_16x16x64_i8 v[102:105], v[134:137], v[234:237], v[102:105]
	v_mfma_i32_16x16x64_i8 v[98:101], v[142:145], v[234:237], v[98:101]
	s_setprio 0
	s_setprio 1
	v_mfma_i32_16x16x64_i8 v[94:97], v[146:149], v[206:209], v[94:97]
	v_mfma_i32_16x16x64_i8 v[90:93], v[154:157], v[206:209], v[90:93]
	v_mfma_i32_16x16x64_i8 v[86:89], v[146:149], v[210:213], v[86:89]
	v_mfma_i32_16x16x64_i8 v[82:85], v[154:157], v[210:213], v[82:85]
	v_mfma_i32_16x16x64_i8 v[78:81], v[146:149], v[222:225], v[78:81]
	v_mfma_i32_16x16x64_i8 v[74:77], v[154:157], v[222:225], v[74:77]
	v_mfma_i32_16x16x64_i8 v[70:73], v[146:149], v[226:229], v[70:73]
	v_mfma_i32_16x16x64_i8 v[66:69], v[154:157], v[226:229], v[66:69]
	s_nop 0
	v_mfma_i32_16x16x64_i8 v[94:97], v[150:153], v[214:217], v[94:97]
	v_mfma_i32_16x16x64_i8 v[90:93], v[158:161], v[214:217], v[90:93]
	v_mfma_i32_16x16x64_i8 v[86:89], v[150:153], v[218:221], v[86:89]
	v_mfma_i32_16x16x64_i8 v[82:85], v[158:161], v[218:221], v[82:85]
	v_mfma_i32_16x16x64_i8 v[78:81], v[150:153], v[230:233], v[78:81]
	v_mfma_i32_16x16x64_i8 v[74:77], v[158:161], v[230:233], v[74:77]
	v_mfma_i32_16x16x64_i8 v[70:73], v[150:153], v[234:237], v[70:73]
	v_mfma_i32_16x16x64_i8 v[66:69], v[158:161], v[234:237], v[66:69]
	s_setprio 0
	s_barrier
; #define PG8_STAGE(bufoff, gbase, voff) do { _Pragma("unroll") for (int _i = 0; _i < 2; ++_i) \
;         __builtin_amdgcn_global_load_lds((const unsigned*)((const char*)(gbase) + (voff)[_i]), (LAS unsigned*)(lds + (bufoff) + ldsw + _i * 8192), 16, 0, 0); } while (0)
; #define PG8_LDA(dst, b, h) do { _Pragma("unroll") for (int m = 0; m < 4; ++m) _Pragma("unroll") for (int k = 0; k < 2; ++k) dst[m][k] = *(const LAS bf16x8*)(lds + PG8_SA(b, h) + aoff + m * 2048 + k * 1024); } while (0)
; #define PG8_MMA(ai, bj, At, Bt) do { __builtin_amdgcn_s_setprio(1); _Pragma("unroll") for (int m = 0; m < 4; ++m) _Pragma("unroll") for (int n = 0; n < 2; ++n) _Pragma("unroll") for (int k = 0; k < 2; ++k) \
;         acc[ai][bj][m][n] = __builtin_amdgcn_mfma_f32_16x16x32_bf16(Bt[n][k], At[m][k], acc[ai][bj][m][n], 0, 0, 0); __builtin_amdgcn_s_setprio(0); } while (0)
; #define PG8_WAIT_V(n) asm volatile("s_waitcnt vmcnt(" #n ")" ::: "memory")
; #define PG8_WAIT_L(n) asm volatile("s_waitcnt lgkmcnt(" #n ")" ::: "memory")
; #define PG8_BAR __builtin_amdgcn_s_barrier()
; #define PG8_SCHED __builtin_amdgcn_sched_barrier(0)
; #define PG8_STAGE(bufoff, gbase, voff) do { _Pragma("unroll") for (int _i = 0; _i < 2; ++_i) \
;         __builtin_amdgcn_global_load_lds((const unsigned*)((const char*)(gbase) + (voff)[_i]), (LAS unsigned*)(lds + (bufoff) + ldsw + _i * 8192), 16, 0, 0); } while (0)
; #define PG8_LDA(dst, b, h) do { _Pragma("unroll") for (int m = 0; m < 4; ++m) PG8_LD1(dst[m], PG8_SA(b, h) + aoff0 + m * 2048, PG8_SA(b, h) + aoff1 + m * 2048); } while (0)
; #define PG8_WAIT_V(n) asm volatile("s_waitcnt vmcnt(" #n ")" ::: "memory")
; #define PG8_WAIT_L(n) asm volatile("s_waitcnt lgkmcnt(" #n ")" ::: "memory")
; #define PG8_BAR __builtin_amdgcn_s_barrier()
; #define PG8_SCHED __builtin_amdgcn_sched_barrier(0)
;     ...
;         for (int t = 0; t < nt; t += 2) {
;     ...
;             PG8_LDA(At, 1, 1); PG8_STAGE(PG8_SB(1, 0), b3, voffB); PG8_STAGE(PG8_SB(1, 1), b3 + hstepB, voffB); PG8_STAGE(PG8_SA(1, 0), a3, voffA);
;             PG8_WAIT_V(8); PG8_WAIT_L(0); PG8_BAR; PG8_MMA(1, 0, At, B0); PG8_MMA(1, 1, At, B1); PG8_BAR; PG8_SCHED;
	s_mov_b32 m0, s78
	v_lshl_add_u64 v[178:179], v[178:179], 0, s[22:23]
	s_add_u32 s8, s86, 0x40080
	ds_read_b128 v[206:209], v204 offset:49152
	ds_read_b128 v[210:213], v204 offset:51200
	ds_read_b128 v[214:217], v205 offset:49152
	ds_read_b128 v[218:221], v205 offset:51200
	ds_read_b128 v[222:225], v204 offset:53248
	ds_read_b128 v[226:229], v204 offset:55296
	ds_read_b128 v[230:233], v205 offset:53248
	ds_read_b128 v[234:237], v205 offset:55296
	global_load_lds_dwordx4 v[178:179], off
	v_lshl_add_u64 v[178:179], v[180:181], 0, s[22:23]
	s_mov_b32 m0, s79
	s_addc_u32 s9, s87, 0
	global_load_lds_dwordx4 v[178:179], off
	v_lshl_add_u64 v[178:179], s[8:9], 0, v[166:167]
	s_mov_b32 m0, s90
	s_nop 0
	global_load_lds_dwordx4 v[178:179], off
	v_lshl_add_u64 v[178:179], s[8:9], 0, v[162:163]
	s_mov_b32 m0, s91
	s_nop 0
	global_load_lds_dwordx4 v[178:179], off
	v_lshl_add_u64 v[178:179], v[182:183], 0, s[22:23]
	s_mov_b32 m0, s80
	s_nop 0
	global_load_lds_dwordx4 v[178:179], off
	v_lshl_add_u64 v[178:179], v[184:185], 0, s[22:23]
	s_mov_b32 m0, s81
	s_nop 0
	global_load_lds_dwordx4 v[178:179], off
	s_waitcnt vmcnt(8)
	s_waitcnt lgkmcnt(0)
	s_barrier
	s_setprio 1
	s_waitcnt lgkmcnt(0)
	v_mfma_i32_16x16x64_i8 v[62:65], v[130:133], v[206:209], v[62:65]
	v_mfma_i32_16x16x64_i8 v[58:61], v[138:141], v[206:209], v[58:61]
	v_mfma_i32_16x16x64_i8 v[54:57], v[130:133], v[210:213], v[54:57]
	v_mfma_i32_16x16x64_i8 v[50:53], v[138:141], v[210:213], v[50:53]
	v_mfma_i32_16x16x64_i8 v[46:49], v[130:133], v[222:225], v[46:49]
	v_mfma_i32_16x16x64_i8 v[42:45], v[138:141], v[222:225], v[42:45]
	v_mfma_i32_16x16x64_i8 v[38:41], v[130:133], v[226:229], v[38:41]
	v_mfma_i32_16x16x64_i8 v[34:37], v[138:141], v[226:229], v[34:37]
	s_nop 0
	v_mfma_i32_16x16x64_i8 v[62:65], v[134:137], v[214:217], v[62:65]
	v_mfma_i32_16x16x64_i8 v[58:61], v[142:145], v[214:217], v[58:61]
	v_mfma_i32_16x16x64_i8 v[54:57], v[134:137], v[218:221], v[54:57]
	v_mfma_i32_16x16x64_i8 v[50:53], v[142:145], v[218:221], v[50:53]
	v_mfma_i32_16x16x64_i8 v[46:49], v[134:137], v[230:233], v[46:49]
	v_mfma_i32_16x16x64_i8 v[42:45], v[142:145], v[230:233], v[42:45]
	v_mfma_i32_16x16x64_i8 v[38:41], v[134:137], v[234:237], v[38:41]
	v_mfma_i32_16x16x64_i8 v[34:37], v[142:145], v[234:237], v[34:37]
	s_setprio 0
	s_setprio 1
	v_mfma_i32_16x16x64_i8 v[30:33], v[146:149], v[206:209], v[30:33]
	v_mfma_i32_16x16x64_i8 v[26:29], v[154:157], v[206:209], v[26:29]
	v_mfma_i32_16x16x64_i8 v[22:25], v[146:149], v[210:213], v[22:25]
	v_mfma_i32_16x16x64_i8 v[18:21], v[154:157], v[210:213], v[18:21]
	v_mfma_i32_16x16x64_i8 v[14:17], v[146:149], v[222:225], v[14:17]
	v_mfma_i32_16x16x64_i8 v[10:13], v[154:157], v[222:225], v[10:13]
	v_mfma_i32_16x16x64_i8 v[6:9], v[146:149], v[226:229], v[6:9]
	v_mfma_i32_16x16x64_i8 v[2:5], v[154:157], v[226:229], v[2:5]
	s_nop 0
	v_mfma_i32_16x16x64_i8 v[30:33], v[150:153], v[214:217], v[30:33]
	v_mfma_i32_16x16x64_i8 v[26:29], v[158:161], v[214:217], v[26:29]
	v_mfma_i32_16x16x64_i8 v[22:25], v[150:153], v[218:221], v[22:25]
	v_mfma_i32_16x16x64_i8 v[18:21], v[158:161], v[218:221], v[18:21]
	s_add_i32 vcc_lo, vcc_lo, 2
	s_add_u32 s94, s94, 0x100
	s_addc_u32 s95, s95, 0
	s_cmp_gt_u32 vcc_lo, 13
	s_mov_b64 s[82:83], s[84:85]
	v_mfma_i32_16x16x64_i8 v[14:17], v[150:153], v[230:233], v[14:17]
	v_mfma_i32_16x16x64_i8 v[10:13], v[158:161], v[230:233], v[10:13]
	v_mfma_i32_16x16x64_i8 v[6:9], v[150:153], v[234:237], v[6:9]
	v_mfma_i32_16x16x64_i8 v[2:5], v[158:161], v[234:237], v[2:5]
	s_setprio 0
	s_barrier
	s_cbranch_scc0 .LBB0_143
	s_nop 15
	s_nop 15
	s_and_b64 vcc, exec, s[38:39]
	s_cbranch_vccz .LBB0_146
	s_barrier

; #define PG8_STAGE(bufoff, gbase, voff) do { _Pragma("unroll") for (int _i = 0; _i < 2; ++_i) \
;         __builtin_amdgcn_global_load_lds((const unsigned*)((const char*)(gbase) + (voff)[_i]), (LAS unsigned*)(lds + (bufoff) + ldsw + _i * 8192), 16, 0, 0); } while (0)
; #define PG8_LDA(dst, b, h) do { _Pragma("unroll") for (int m = 0; m < 4; ++m) _Pragma("unroll") for (int k = 0; k < 2; ++k) dst[m][k] = *(const LAS bf16x8*)(lds + PG8_SA(b, h) + aoff + m * 2048 + k * 1024); } while (0)
; #define PG8_LDB(dst, b, h) do { _Pragma("unroll") for (int n = 0; n < 2; ++n) _Pragma("unroll") for (int k = 0; k < 2; ++k) dst[n][k] = *(const LAS bf16x8*)(lds + PG8_SB(b, h) + boff + n * 2048 + k * 1024); } while (0)
; #define PG8_MMA(ai, bj, At, Bt) do { __builtin_amdgcn_s_setprio(1); _Pragma("unroll") for (int m = 0; m < 4; ++m) _Pragma("unroll") for (int n = 0; n < 2; ++n) _Pragma("unroll") for (int k = 0; k < 2; ++k) \
;         acc[ai][bj][m][n] = __builtin_amdgcn_mfma_f32_16x16x32_bf16(Bt[n][k], At[m][k], acc[ai][bj][m][n], 0, 0, 0); __builtin_amdgcn_s_setprio(0); } while (0)
; #define PG8_WAIT_V(n) asm volatile("s_waitcnt vmcnt(" #n ")" ::: "memory")
; #define PG8_WAIT_L(n) asm volatile("s_waitcnt lgkmcnt(" #n ")" ::: "memory")
; #define PG8_BAR __builtin_amdgcn_s_barrier()
; #define PG8_SCHED __builtin_amdgcn_sched_barrier(0)
; #define PG8_STAGE(bufoff, gbase, voff) do { _Pragma("unroll") for (int _i = 0; _i < 2; ++_i) \
;         __builtin_amdgcn_global_load_lds((const unsigned*)((const char*)(gbase) + (voff)[_i]), (LAS unsigned*)(lds + (bufoff) + ldsw + _i * 8192), 16, 0, 0); } while (0)
; #define PG8_LDA(dst, b, h) do { _Pragma("unroll") for (int m = 0; m < 4; ++m) PG8_LD1(dst[m], PG8_SA(b, h) + aoff0 + m * 2048, PG8_SA(b, h) + aoff1 + m * 2048); } while (0)
; #define PG8_WAIT_V(n) asm volatile("s_waitcnt vmcnt(" #n ")" ::: "memory")
;     ...
;             PG8_LDB(B0, 0, 0); PG8_LDB(B1, 0, 1); PG8_SCHED; PG8_LDA(At, 0, 0); PG8_STAGE(PG8_SA(1, 1), a1 + hstepA, voffA);
;             PG8_WAIT_V(8); PG8_WAIT_L(0); PG8_BAR; PG8_MMA(0, 0, At, B0); PG8_MMA(0, 1, At, B1); PG8_BAR; PG8_SCHED;
;             PG8_LDA(At, 0, 1); PG8_STAGE(PG8_SB(0, 0), b2, voffB); PG8_STAGE(PG8_SB(0, 1), b2 + hstepB, voffB); PG8_STAGE(PG8_SA(0, 0), a2, voffA);
;             PG8_WAIT_V(8); PG8_WAIT_L(0); PG8_BAR; PG8_MMA(1, 0, At, B0); PG8_MMA(1, 1, At, B1); PG8_BAR; PG8_SCHED;
.LBB0_594:
	ds_read_b128 v[158:161], v187
	ds_read_b128 v[146:149], v188
	ds_read_b128 v[154:157], v195
	ds_read_b128 v[150:153], v196
	ds_read_b128 v[142:145], v189
	ds_read_b128 v[130:133], v190
	ds_read_b128 v[138:141], v197
	ds_read_b128 v[134:137], v198
	s_add_u32 s58, s60, 0x100
	s_addc_u32 s59, s61, 0
	s_cmp_eq_u32 s92, 12
	s_cselect_b32 s65, s43, s59
	s_cselect_b32 s64, s45, s58
	s_cselect_b32 s63, s75, s91
	s_cselect_b32 s62, s89, s90
	v_lshl_add_u64 v[232:233], s[60:61], 0, v[170:171]
	s_add_i32 m0, s11, 0xc000
	ds_read_b128 v[178:181], v204
	ds_read_b128 v[182:185], v204 offset:2048
	ds_read_b128 v[208:211], v205
	ds_read_b128 v[212:215], v205 offset:2048
	ds_read_b128 v[216:219], v204 offset:4096
	ds_read_b128 v[220:223], v204 offset:6144
	ds_read_b128 v[224:227], v205 offset:4096
	ds_read_b128 v[228:231], v205 offset:6144
	global_load_lds_dwordx4 v[232:233], off
	v_lshl_add_u64 v[232:233], s[60:61], 0, v[172:173]
	s_add_i32 m0, s11, 0xe000
	s_nop 0
	global_load_lds_dwordx4 v[232:233], off
	s_waitcnt vmcnt(8)
	s_waitcnt lgkmcnt(0)
	s_barrier
	s_setprio 1
	s_waitcnt lgkmcnt(0)
	v_mfma_i32_16x16x64_i8 v[126:129], v[158:161], v[178:181], v[126:129]
	v_mfma_i32_16x16x64_i8 v[122:125], v[154:157], v[178:181], v[122:125]
	v_mfma_i32_16x16x64_i8 v[118:121], v[158:161], v[182:185], v[118:121]
	v_mfma_i32_16x16x64_i8 v[110:113], v[154:157], v[182:185], v[110:113]
	v_mfma_i32_16x16x64_i8 v[102:105], v[158:161], v[216:219], v[102:105]
	v_mfma_i32_16x16x64_i8 v[94:97], v[154:157], v[216:219], v[94:97]
	v_mfma_i32_16x16x64_i8 v[86:89], v[158:161], v[220:223], v[86:89]
	v_mfma_i32_16x16x64_i8 v[78:81], v[154:157], v[220:223], v[78:81]
	s_nop 0
	v_mfma_i32_16x16x64_i8 v[126:129], v[146:149], v[208:211], v[126:129]
	v_mfma_i32_16x16x64_i8 v[122:125], v[150:153], v[208:211], v[122:125]
	v_mfma_i32_16x16x64_i8 v[118:121], v[146:149], v[212:215], v[118:121]
	v_mfma_i32_16x16x64_i8 v[110:113], v[150:153], v[212:215], v[110:113]
	v_mfma_i32_16x16x64_i8 v[102:105], v[146:149], v[224:227], v[102:105]
	v_mfma_i32_16x16x64_i8 v[94:97], v[150:153], v[224:227], v[94:97]
	v_mfma_i32_16x16x64_i8 v[86:89], v[146:149], v[228:231], v[86:89]
	v_mfma_i32_16x16x64_i8 v[78:81], v[150:153], v[228:231], v[78:81]
	s_setprio 0
	s_setprio 1
	v_mfma_i32_16x16x64_i8 v[114:117], v[142:145], v[178:181], v[114:117]
	v_mfma_i32_16x16x64_i8 v[106:109], v[138:141], v[178:181], v[106:109]
	v_mfma_i32_16x16x64_i8 v[98:101], v[142:145], v[182:185], v[98:101]
	v_mfma_i32_16x16x64_i8 v[90:93], v[138:141], v[182:185], v[90:93]
	v_mfma_i32_16x16x64_i8 v[82:85], v[142:145], v[216:219], v[82:85]
	v_mfma_i32_16x16x64_i8 v[74:77], v[138:141], v[216:219], v[74:77]
	v_mfma_i32_16x16x64_i8 v[70:73], v[142:145], v[220:223], v[70:73]
	v_mfma_i32_16x16x64_i8 v[66:69], v[138:141], v[220:223], v[66:69]
	s_nop 0
	v_mfma_i32_16x16x64_i8 v[114:117], v[130:133], v[208:211], v[114:117]
	v_mfma_i32_16x16x64_i8 v[106:109], v[134:137], v[208:211], v[106:109]
	v_mfma_i32_16x16x64_i8 v[98:101], v[130:133], v[212:215], v[98:101]
	v_mfma_i32_16x16x64_i8 v[90:93], v[134:137], v[212:215], v[90:93]
	v_mfma_i32_16x16x64_i8 v[82:85], v[130:133], v[224:227], v[82:85]
	v_mfma_i32_16x16x64_i8 v[74:77], v[134:137], v[224:227], v[74:77]
	v_mfma_i32_16x16x64_i8 v[70:73], v[130:133], v[228:231], v[70:73]
	v_mfma_i32_16x16x64_i8 v[66:69], v[134:137], v[228:231], v[66:69]
	s_setprio 0
	s_barrier
	s_mov_b32 m0, s24
	v_lshl_add_u64 v[178:179], s[62:63], 0, v[166:167]
	s_add_u32 s8, s62, 0x40000
	ds_read_b128 v[208:211], v204 offset:16384
	ds_read_b128 v[212:215], v204 offset:18432
	ds_read_b128 v[216:219], v205 offset:16384
	ds_read_b128 v[220:223], v205 offset:18432
	ds_read_b128 v[224:227], v204 offset:20480
	ds_read_b128 v[228:231], v204 offset:22528
	ds_read_b128 v[232:235], v205 offset:20480
	ds_read_b128 v[236:239], v205 offset:22528
	global_load_lds_dwordx4 v[178:179], off
	v_lshl_add_u64 v[180:181], s[62:63], 0, v[162:163]
	s_mov_b32 m0, s25
	s_addc_u32 s9, s63, 0
	global_load_lds_dwordx4 v[180:181], off
	v_lshl_add_u64 v[182:183], s[8:9], 0, v[166:167]
	s_mov_b32 m0, s66
	v_lshl_add_u64 v[184:185], s[64:65], 0, v[164:165]
	global_load_lds_dwordx4 v[182:183], off
	v_lshl_add_u64 v[182:183], s[8:9], 0, v[162:163]
	s_mov_b32 m0, s67
	s_nop 0
	global_load_lds_dwordx4 v[182:183], off
	v_lshl_add_u64 v[182:183], s[64:65], 0, v[168:169]
	s_mov_b32 m0, s11
	s_nop 0
	global_load_lds_dwordx4 v[182:183], off
	s_mov_b32 m0, s0
	s_nop 0
	global_load_lds_dwordx4 v[184:185], off
	s_waitcnt vmcnt(8)
	s_waitcnt lgkmcnt(0)
	s_barrier
; #define PG8_STAGE(bufoff, gbase, voff) do { _Pragma("unroll") for (int _i = 0; _i < 2; ++_i) \
;         __builtin_amdgcn_global_load_lds((const unsigned*)((const char*)(gbase) + (voff)[_i]), (LAS unsigned*)(lds + (bufoff) + ldsw + _i * 8192), 16, 0, 0); } while (0)
; #define PG8_LDA(dst, b, h) do { _Pragma("unroll") for (int m = 0; m < 4; ++m) _Pragma("unroll") for (int k = 0; k < 2; ++k) dst[m][k] = *(const LAS bf16x8*)(lds + PG8_SA(b, h) + aoff + m * 2048 + k * 1024); } while (0)
; #define PG8_LDB(dst, b, h) do { _Pragma("unroll") for (int n = 0; n < 2; ++n) _Pragma("unroll") for (int k = 0; k < 2; ++k) dst[n][k] = *(const LAS bf16x8*)(lds + PG8_SB(b, h) + boff + n * 2048 + k * 1024); } while (0)
; #define PG8_MMA(ai, bj, At, Bt) do { __builtin_amdgcn_s_setprio(1); _Pragma("unroll") for (int m = 0; m < 4; ++m) _Pragma("unroll") for (int n = 0; n < 2; ++n) _Pragma("unroll") for (int k = 0; k < 2; ++k) \
;         acc[ai][bj][m][n] = __builtin_amdgcn_mfma_f32_16x16x32_bf16(Bt[n][k], At[m][k], acc[ai][bj][m][n], 0, 0, 0); __builtin_amdgcn_s_setprio(0); } while (0)
; #define PG8_WAIT_V(n) asm volatile("s_waitcnt vmcnt(" #n ")" ::: "memory")
; #define PG8_WAIT_L(n) asm volatile("s_waitcnt lgkmcnt(" #n ")" ::: "memory")
; #define PG8_BAR __builtin_amdgcn_s_barrier()
; #define PG8_SCHED __builtin_amdgcn_sched_barrier(0)
; #define PG8_STAGE(bufoff, gbase, voff) do { _Pragma("unroll") for (int _i = 0; _i < 2; ++_i) \
;         __builtin_amdgcn_global_load_lds((const unsigned*)((const char*)(gbase) + (voff)[_i]), (LAS unsigned*)(lds + (bufoff) + ldsw + _i * 8192), 16, 0, 0); } while (0)
; #define PG8_LDA(dst, b, h) do { _Pragma("unroll") for (int m = 0; m < 4; ++m) PG8_LD1(dst[m], PG8_SA(b, h) + aoff0 + m * 2048, PG8_SA(b, h) + aoff1 + m * 2048); } while (0)
; #define PG8_LDB(dst, b, h) do { _Pragma("unroll") for (int n = 0; n < 2; ++n) PG8_LD1(dst[n], PG8_SB(b, h) + boff0 + n * 2048, PG8_SB(b, h) + boff1 + n * 2048); } while (0)
; #define PG8_BAR __builtin_amdgcn_s_barrier()
;     ...
;             PG8_WAIT_V(8); PG8_WAIT_L(0); PG8_BAR; PG8_MMA(1, 0, At, B0); PG8_MMA(1, 1, At, B1); PG8_BAR; PG8_SCHED;
;             PG8_LDB(B0, 1, 0); PG8_LDB(B1, 1, 1); PG8_SCHED; PG8_LDA(At, 1, 0); PG8_STAGE(PG8_SA(0, 1), a2 + hstepA, voffA);
;             PG8_WAIT_V(8); PG8_WAIT_L(0); PG8_BAR; PG8_MMA(0, 0, At, B0); PG8_MMA(0, 1, At, B1); PG8_BAR; PG8_SCHED;
	s_setprio 1
	s_waitcnt lgkmcnt(0)
	v_mfma_i32_16x16x64_i8 v[62:65], v[158:161], v[208:211], v[62:65]
	v_mfma_i32_16x16x64_i8 v[58:61], v[154:157], v[208:211], v[58:61]
	v_mfma_i32_16x16x64_i8 v[54:57], v[158:161], v[212:215], v[54:57]
	v_mfma_i32_16x16x64_i8 v[46:49], v[154:157], v[212:215], v[46:49]
	v_mfma_i32_16x16x64_i8 v[38:41], v[158:161], v[224:227], v[38:41]
	v_mfma_i32_16x16x64_i8 v[30:33], v[154:157], v[224:227], v[30:33]
	v_mfma_i32_16x16x64_i8 v[22:25], v[158:161], v[228:231], v[22:25]
	v_mfma_i32_16x16x64_i8 v[14:17], v[154:157], v[228:231], v[14:17]
	s_nop 0
	v_mfma_i32_16x16x64_i8 v[62:65], v[146:149], v[216:219], v[62:65]
	v_mfma_i32_16x16x64_i8 v[58:61], v[150:153], v[216:219], v[58:61]
	v_mfma_i32_16x16x64_i8 v[54:57], v[146:149], v[220:223], v[54:57]
	v_mfma_i32_16x16x64_i8 v[46:49], v[150:153], v[220:223], v[46:49]
	v_mfma_i32_16x16x64_i8 v[38:41], v[146:149], v[232:235], v[38:41]
	v_mfma_i32_16x16x64_i8 v[30:33], v[150:153], v[232:235], v[30:33]
	v_mfma_i32_16x16x64_i8 v[22:25], v[146:149], v[236:239], v[22:25]
	v_mfma_i32_16x16x64_i8 v[14:17], v[150:153], v[236:239], v[14:17]
	s_setprio 0
	s_setprio 1
	v_mfma_i32_16x16x64_i8 v[50:53], v[142:145], v[208:211], v[50:53]
	v_mfma_i32_16x16x64_i8 v[42:45], v[138:141], v[208:211], v[42:45]
	v_mfma_i32_16x16x64_i8 v[34:37], v[142:145], v[212:215], v[34:37]
	v_mfma_i32_16x16x64_i8 v[26:29], v[138:141], v[212:215], v[26:29]
	v_mfma_i32_16x16x64_i8 v[18:21], v[142:145], v[224:227], v[18:21]
	v_mfma_i32_16x16x64_i8 v[10:13], v[138:141], v[224:227], v[10:13]
	v_mfma_i32_16x16x64_i8 v[6:9], v[142:145], v[228:231], v[6:9]
	v_mfma_i32_16x16x64_i8 v[2:5], v[138:141], v[228:231], v[2:5]
	s_nop 0
	v_mfma_i32_16x16x64_i8 v[50:53], v[130:133], v[216:219], v[50:53]
	v_mfma_i32_16x16x64_i8 v[42:45], v[134:137], v[216:219], v[42:45]
	v_mfma_i32_16x16x64_i8 v[34:37], v[130:133], v[220:223], v[34:37]
	v_mfma_i32_16x16x64_i8 v[26:29], v[134:137], v[220:223], v[26:29]
	v_mfma_i32_16x16x64_i8 v[18:21], v[130:133], v[232:235], v[18:21]
	v_mfma_i32_16x16x64_i8 v[10:13], v[134:137], v[232:235], v[10:13]
	v_mfma_i32_16x16x64_i8 v[6:9], v[130:133], v[236:239], v[6:9]
	v_mfma_i32_16x16x64_i8 v[2:5], v[134:137], v[236:239], v[2:5]
	s_setprio 0
	s_barrier
	ds_read_b128 v[130:133], v191
	ds_read_b128 v[134:137], v192
	ds_read_b128 v[138:141], v199
	ds_read_b128 v[142:145], v200
	ds_read_b128 v[146:149], v193
	ds_read_b128 v[150:153], v194
	ds_read_b128 v[154:157], v201
	ds_read_b128 v[158:161], v202
	s_add_u32 s8, s64, 0x40000
	s_addc_u32 s9, s65, 0
	s_mov_b32 m0, s78
	v_lshl_add_u64 v[240:241], s[8:9], 0, v[168:169]
	ds_read_b128 v[208:211], v204 offset:32768
	ds_read_b128 v[212:215], v204 offset:34816
	ds_read_b128 v[216:219], v205 offset:32768
	ds_read_b128 v[220:223], v205 offset:34816
	ds_read_b128 v[224:227], v204 offset:36864
	ds_read_b128 v[228:231], v204 offset:38912
	ds_read_b128 v[232:235], v205 offset:36864
	ds_read_b128 v[236:239], v205 offset:38912
	global_load_lds_dwordx4 v[240:241], off
	v_lshl_add_u64 v[240:241], s[8:9], 0, v[164:165]
	s_mov_b32 m0, s79
	s_nop 0
	global_load_lds_dwordx4 v[240:241], off
	s_waitcnt vmcnt(8)
	s_waitcnt lgkmcnt(0)
	s_barrier
	s_setprio 1
	s_waitcnt lgkmcnt(0)
	v_mfma_i32_16x16x64_i8 v[126:129], v[130:133], v[208:211], v[126:129]
	v_mfma_i32_16x16x64_i8 v[122:125], v[138:141], v[208:211], v[122:125]
	v_mfma_i32_16x16x64_i8 v[118:121], v[130:133], v[212:215], v[118:121]
	v_mfma_i32_16x16x64_i8 v[110:113], v[138:141], v[212:215], v[110:113]
	v_mfma_i32_16x16x64_i8 v[102:105], v[130:133], v[224:227], v[102:105]
	v_mfma_i32_16x16x64_i8 v[94:97], v[138:141], v[224:227], v[94:97]
	v_mfma_i32_16x16x64_i8 v[86:89], v[130:133], v[228:231], v[86:89]
	v_mfma_i32_16x16x64_i8 v[78:81], v[138:141], v[228:231], v[78:81]
	s_nop 0
	v_mfma_i32_16x16x64_i8 v[126:129], v[134:137], v[216:219], v[126:129]
	v_mfma_i32_16x16x64_i8 v[122:125], v[142:145], v[216:219], v[122:125]
	v_mfma_i32_16x16x64_i8 v[118:121], v[134:137], v[220:223], v[118:121]
	v_mfma_i32_16x16x64_i8 v[110:113], v[142:145], v[220:223], v[110:113]
	v_mfma_i32_16x16x64_i8 v[102:105], v[134:137], v[232:235], v[102:105]
	v_mfma_i32_16x16x64_i8 v[94:97], v[142:145], v[232:235], v[94:97]
	v_mfma_i32_16x16x64_i8 v[86:89], v[134:137], v[236:239], v[86:89]
	v_mfma_i32_16x16x64_i8 v[78:81], v[142:145], v[236:239], v[78:81]
	s_setprio 0
	s_setprio 1
	v_mfma_i32_16x16x64_i8 v[114:117], v[146:149], v[208:211], v[114:117]
	v_mfma_i32_16x16x64_i8 v[106:109], v[154:157], v[208:211], v[106:109]
	v_mfma_i32_16x16x64_i8 v[98:101], v[146:149], v[212:215], v[98:101]
	v_mfma_i32_16x16x64_i8 v[90:93], v[154:157], v[212:215], v[90:93]
	v_mfma_i32_16x16x64_i8 v[82:85], v[146:149], v[224:227], v[82:85]
	v_mfma_i32_16x16x64_i8 v[74:77], v[154:157], v[224:227], v[74:77]
	v_mfma_i32_16x16x64_i8 v[70:73], v[146:149], v[228:231], v[70:73]
	v_mfma_i32_16x16x64_i8 v[66:69], v[154:157], v[228:231], v[66:69]
	s_nop 0
	v_mfma_i32_16x16x64_i8 v[114:117], v[150:153], v[216:219], v[114:117]
	v_mfma_i32_16x16x64_i8 v[106:109], v[158:161], v[216:219], v[106:109]
	v_mfma_i32_16x16x64_i8 v[98:101], v[150:153], v[220:223], v[98:101]
	v_mfma_i32_16x16x64_i8 v[90:93], v[158:161], v[220:223], v[90:93]
	v_mfma_i32_16x16x64_i8 v[82:85], v[150:153], v[232:235], v[82:85]
	v_mfma_i32_16x16x64_i8 v[74:77], v[158:161], v[232:235], v[74:77]
	v_mfma_i32_16x16x64_i8 v[70:73], v[150:153], v[236:239], v[70:73]
	v_mfma_i32_16x16x64_i8 v[66:69], v[158:161], v[236:239], v[66:69]
	s_setprio 0
	s_barrier
; #define PG8_STAGE(bufoff, gbase, voff) do { _Pragma("unroll") for (int _i = 0; _i < 2; ++_i) \
;         __builtin_amdgcn_global_load_lds((const unsigned*)((const char*)(gbase) + (voff)[_i]), (LAS unsigned*)(lds + (bufoff) + ldsw + _i * 8192), 16, 0, 0); } while (0)
; #define PG8_LDA(dst, b, h) do { _Pragma("unroll") for (int m = 0; m < 4; ++m) _Pragma("unroll") for (int k = 0; k < 2; ++k) dst[m][k] = *(const LAS bf16x8*)(lds + PG8_SA(b, h) + aoff + m * 2048 + k * 1024); } while (0)
; #define PG8_MMA(ai, bj, At, Bt) do { __builtin_amdgcn_s_setprio(1); _Pragma("unroll") for (int m = 0; m < 4; ++m) _Pragma("unroll") for (int n = 0; n < 2; ++n) _Pragma("unroll") for (int k = 0; k < 2; ++k) \
;         acc[ai][bj][m][n] = __builtin_amdgcn_mfma_f32_16x16x32_bf16(Bt[n][k], At[m][k], acc[ai][bj][m][n], 0, 0, 0); __builtin_amdgcn_s_setprio(0); } while (0)
; #define PG8_WAIT_V(n) asm volatile("s_waitcnt vmcnt(" #n ")" ::: "memory")
; #define PG8_WAIT_L(n) asm volatile("s_waitcnt lgkmcnt(" #n ")" ::: "memory")
; #define PG8_BAR __builtin_amdgcn_s_barrier()
; #define PG8_SCHED __builtin_amdgcn_sched_barrier(0)
; #define PG8_STAGE(bufoff, gbase, voff) do { _Pragma("unroll") for (int _i = 0; _i < 2; ++_i) \
;         __builtin_amdgcn_global_load_lds((const unsigned*)((const char*)(gbase) + (voff)[_i]), (LAS unsigned*)(lds + (bufoff) + ldsw + _i * 8192), 16, 0, 0); } while (0)
; #define PG8_LDA(dst, b, h) do { _Pragma("unroll") for (int m = 0; m < 4; ++m) PG8_LD1(dst[m], PG8_SA(b, h) + aoff0 + m * 2048, PG8_SA(b, h) + aoff1 + m * 2048); } while (0)
; #define PG8_WAIT_V(n) asm volatile("s_waitcnt vmcnt(" #n ")" ::: "memory")
; #define PG8_WAIT_L(n) asm volatile("s_waitcnt lgkmcnt(" #n ")" ::: "memory")
; #define PG8_BAR __builtin_amdgcn_s_barrier()
; #define PG8_SCHED __builtin_amdgcn_sched_barrier(0)
;     ...
;             PG8_LDA(At, 1, 1); PG8_STAGE(PG8_SB(1, 0), b3, voffB); PG8_STAGE(PG8_SB(1, 1), b3 + hstepB, voffB); PG8_STAGE(PG8_SA(1, 0), a3, voffA);
;             PG8_WAIT_V(8); PG8_WAIT_L(0); PG8_BAR; PG8_MMA(1, 0, At, B0); PG8_MMA(1, 1, At, B1); PG8_BAR; PG8_SCHED;
;         }
;         asm volatile("s_nop 15\n\ts_nop 15" ::: "memory");
;         if (wr == 0) PG8_BAR;
	s_mov_b32 m0, s81
	v_lshl_add_u64 v[178:179], v[178:179], 0, s[38:39]
	s_add_u32 s8, s62, 0x40080
	ds_read_b128 v[208:211], v204 offset:49152
	ds_read_b128 v[212:215], v204 offset:51200
	ds_read_b128 v[216:219], v205 offset:49152
	ds_read_b128 v[220:223], v205 offset:51200
	ds_read_b128 v[224:227], v204 offset:53248
	ds_read_b128 v[228:231], v204 offset:55296
	ds_read_b128 v[232:235], v205 offset:53248
	ds_read_b128 v[236:239], v205 offset:55296
	global_load_lds_dwordx4 v[178:179], off
	v_lshl_add_u64 v[178:179], v[180:181], 0, s[38:39]
	s_mov_b32 m0, s82
	s_addc_u32 s9, s63, 0
	global_load_lds_dwordx4 v[178:179], off
	v_lshl_add_u64 v[178:179], s[8:9], 0, v[166:167]
	s_mov_b32 m0, s85
	s_nop 0
	global_load_lds_dwordx4 v[178:179], off
	v_lshl_add_u64 v[178:179], s[8:9], 0, v[162:163]
	s_mov_b32 m0, s86
	s_nop 0
	global_load_lds_dwordx4 v[178:179], off
	v_lshl_add_u64 v[178:179], v[182:183], 0, s[38:39]
	s_mov_b32 m0, s83
	s_nop 0
	global_load_lds_dwordx4 v[178:179], off
	v_lshl_add_u64 v[178:179], v[184:185], 0, s[38:39]
	s_mov_b32 m0, s84
	s_nop 0
	global_load_lds_dwordx4 v[178:179], off
	s_waitcnt vmcnt(8)
	s_waitcnt lgkmcnt(0)
	s_barrier
	s_setprio 1
	s_waitcnt lgkmcnt(0)
	v_mfma_i32_16x16x64_i8 v[62:65], v[130:133], v[208:211], v[62:65]
	v_mfma_i32_16x16x64_i8 v[58:61], v[138:141], v[208:211], v[58:61]
	v_mfma_i32_16x16x64_i8 v[54:57], v[130:133], v[212:215], v[54:57]
	v_mfma_i32_16x16x64_i8 v[46:49], v[138:141], v[212:215], v[46:49]
	v_mfma_i32_16x16x64_i8 v[38:41], v[130:133], v[224:227], v[38:41]
	v_mfma_i32_16x16x64_i8 v[30:33], v[138:141], v[224:227], v[30:33]
	v_mfma_i32_16x16x64_i8 v[22:25], v[130:133], v[228:231], v[22:25]
	v_mfma_i32_16x16x64_i8 v[14:17], v[138:141], v[228:231], v[14:17]
	s_nop 0
	v_mfma_i32_16x16x64_i8 v[62:65], v[134:137], v[216:219], v[62:65]
	v_mfma_i32_16x16x64_i8 v[58:61], v[142:145], v[216:219], v[58:61]
	v_mfma_i32_16x16x64_i8 v[54:57], v[134:137], v[220:223], v[54:57]
	v_mfma_i32_16x16x64_i8 v[46:49], v[142:145], v[220:223], v[46:49]
	v_mfma_i32_16x16x64_i8 v[38:41], v[134:137], v[232:235], v[38:41]
	v_mfma_i32_16x16x64_i8 v[30:33], v[142:145], v[232:235], v[30:33]
	v_mfma_i32_16x16x64_i8 v[22:25], v[134:137], v[236:239], v[22:25]
	v_mfma_i32_16x16x64_i8 v[14:17], v[142:145], v[236:239], v[14:17]
	s_setprio 0
	s_setprio 1
	v_mfma_i32_16x16x64_i8 v[50:53], v[146:149], v[208:211], v[50:53]
	v_mfma_i32_16x16x64_i8 v[42:45], v[154:157], v[208:211], v[42:45]
	v_mfma_i32_16x16x64_i8 v[34:37], v[146:149], v[212:215], v[34:37]
	v_mfma_i32_16x16x64_i8 v[26:29], v[154:157], v[212:215], v[26:29]
	v_mfma_i32_16x16x64_i8 v[18:21], v[146:149], v[224:227], v[18:21]
	v_mfma_i32_16x16x64_i8 v[10:13], v[154:157], v[224:227], v[10:13]
	v_mfma_i32_16x16x64_i8 v[6:9], v[146:149], v[228:231], v[6:9]
	v_mfma_i32_16x16x64_i8 v[2:5], v[154:157], v[228:231], v[2:5]
	s_nop 0
	v_mfma_i32_16x16x64_i8 v[50:53], v[150:153], v[216:219], v[50:53]
	v_mfma_i32_16x16x64_i8 v[42:45], v[158:161], v[216:219], v[42:45]
	v_mfma_i32_16x16x64_i8 v[34:37], v[150:153], v[220:223], v[34:37]
	v_mfma_i32_16x16x64_i8 v[26:29], v[158:161], v[220:223], v[26:29]
	s_add_i32 s92, s92, 2
	s_add_u32 s90, s90, 0x100
	s_addc_u32 s91, s91, 0
	s_cmp_gt_u32 s92, 13
	s_mov_b64 s[60:61], s[58:59]
	v_mfma_i32_16x16x64_i8 v[18:21], v[150:153], v[232:235], v[18:21]
	v_mfma_i32_16x16x64_i8 v[10:13], v[158:161], v[232:235], v[10:13]
	v_mfma_i32_16x16x64_i8 v[6:9], v[150:153], v[236:239], v[6:9]
	v_mfma_i32_16x16x64_i8 v[2:5], v[158:161], v[236:239], v[2:5]
	s_setprio 0
	s_barrier
	s_cbranch_scc0 .LBB0_594
	s_nop 15
	s_nop 15
	s_and_b64 vcc, exec, s[40:41]
	s_cbranch_vccz .LBB0_597
	s_barrier

; #define PG8_STAGE(bufoff, gbase, voff) do { _Pragma("unroll") for (int _i = 0; _i < 2; ++_i) \
;         __builtin_amdgcn_global_load_lds((const unsigned*)((const char*)(gbase) + (voff)[_i]), (LAS unsigned*)(lds + (bufoff) + ldsw + _i * 8192), 16, 0, 0); } while (0)
; #define PG8_LDA(dst, b, h) do { _Pragma("unroll") for (int m = 0; m < 4; ++m) _Pragma("unroll") for (int k = 0; k < 2; ++k) dst[m][k] = *(const LAS bf16x8*)(lds + PG8_SA(b, h) + aoff + m * 2048 + k * 1024); } while (0)
; #define PG8_LDB(dst, b, h) do { _Pragma("unroll") for (int n = 0; n < 2; ++n) _Pragma("unroll") for (int k = 0; k < 2; ++k) dst[n][k] = *(const LAS bf16x8*)(lds + PG8_SB(b, h) + boff + n * 2048 + k * 1024); } while (0)
; #define PG8_MMA(ai, bj, At, Bt) do { __builtin_amdgcn_s_setprio(1); _Pragma("unroll") for (int m = 0; m < 4; ++m) _Pragma("unroll") for (int n = 0; n < 2; ++n) _Pragma("unroll") for (int k = 0; k < 2; ++k) \
;         acc[ai][bj][m][n] = __builtin_amdgcn_mfma_f32_16x16x32_bf16(Bt[n][k], At[m][k], acc[ai][bj][m][n], 0, 0, 0); __builtin_amdgcn_s_setprio(0); } while (0)
; #define PG8_WAIT_V(n) asm volatile("s_waitcnt vmcnt(" #n ")" ::: "memory")
; #define PG8_WAIT_L(n) asm volatile("s_waitcnt lgkmcnt(" #n ")" ::: "memory")
; #define PG8_BAR __builtin_amdgcn_s_barrier()
; #define PG8_SCHED __builtin_amdgcn_sched_barrier(0)
; #define PG8_LDA(dst, b, h) do { _Pragma("unroll") for (int m = 0; m < 4; ++m) PG8_LD1(dst[m], PG8_SA(b, h) + aoff0 + m * 2048, PG8_SA(b, h) + aoff1 + m * 2048); } while (0)
;     ...
;             const bool last = (t == nt - 2);
;             const char* a1 = cA + (size_t)(t + 1) * kstep;
;             const char* a2 = last ? nA : cA + (size_t)(t + 2) * kstep; const char* b2 = last ? nB : cB + (size_t)(t + 2) * kstep;
;             const char* a3 = a2 + kstep; const char* b3 = b2 + kstep;
;             if (last && has_next) S.a_ready(nxt);
;             PG8_LDB(B0, 0, 0); PG8_LDB(B1, 0, 1); PG8_SCHED; PG8_LDA(At, 0, 0); PG8_STAGE(PG8_SA(1, 1), a1 + hstepA, voffA);
;             PG8_WAIT_V(8); PG8_WAIT_L(0); PG8_BAR; PG8_MMA(0, 0, At, B0); PG8_MMA(0, 1, At, B1); PG8_BAR; PG8_SCHED;
;             PG8_LDA(At, 0, 1); PG8_STAGE(PG8_SB(0, 0), b2, voffB); PG8_STAGE(PG8_SB(0, 1), b2 + hstepB, voffB); PG8_STAGE(PG8_SA(0, 0), a2, voffA);
;             PG8_WAIT_V(8); PG8_WAIT_L(0); PG8_BAR; PG8_MMA(1, 0, At, B0); PG8_MMA(1, 1, At, B1); PG8_BAR; PG8_SCHED;
.LBB0_667:
	ds_read_b128 v[158:161], v217
	ds_read_b128 v[146:149], v218
	ds_read_b128 v[154:157], v225
	ds_read_b128 v[150:153], v226
	ds_read_b128 v[142:145], v219
	ds_read_b128 v[130:133], v220
	ds_read_b128 v[138:141], v227
	ds_read_b128 v[134:137], v228
	s_add_u32 s56, s54, 0x100
	s_addc_u32 s57, s55, 0
	s_cmp_eq_u32 s88, 52
	s_cselect_b32 s61, s82, s57
	s_cselect_b32 s60, s83, s56
	s_cselect_b32 s59, s84, s87
	s_cselect_b32 s58, s85, s86
	v_lshl_add_u64 v[206:207], s[54:55], 0, v[166:167]
	s_add_i32 m0, s0, 0xc000
	ds_read_b128 v[174:177], v234
	ds_read_b128 v[178:181], v234 offset:2048
	ds_read_b128 v[182:185], v235
	ds_read_b128 v[186:189], v235 offset:2048
	ds_read_b128 v[190:193], v234 offset:4096
	ds_read_b128 v[194:197], v234 offset:6144
	ds_read_b128 v[198:201], v235 offset:4096
	ds_read_b128 v[202:205], v235 offset:6144
	global_load_lds_dwordx4 v[206:207], off
	v_lshl_add_u64 v[206:207], s[54:55], 0, v[168:169]
	s_add_i32 m0, s0, 0xe000
	s_nop 0
	global_load_lds_dwordx4 v[206:207], off
	s_waitcnt vmcnt(8)
	s_waitcnt lgkmcnt(0)
	s_barrier
	s_setprio 1
	s_waitcnt lgkmcnt(0)
	v_mfma_i32_16x16x64_i8 v[126:129], v[158:161], v[174:177], v[126:129]
	v_mfma_i32_16x16x64_i8 v[122:125], v[154:157], v[174:177], v[122:125]
	v_mfma_i32_16x16x64_i8 v[118:121], v[158:161], v[178:181], v[118:121]
	v_mfma_i32_16x16x64_i8 v[114:117], v[154:157], v[178:181], v[114:117]
	v_mfma_i32_16x16x64_i8 v[110:113], v[158:161], v[190:193], v[110:113]
	v_mfma_i32_16x16x64_i8 v[106:109], v[154:157], v[190:193], v[106:109]
	v_mfma_i32_16x16x64_i8 v[102:105], v[158:161], v[194:197], v[102:105]
	v_mfma_i32_16x16x64_i8 v[98:101], v[154:157], v[194:197], v[98:101]
	s_nop 0
	v_mfma_i32_16x16x64_i8 v[126:129], v[146:149], v[182:185], v[126:129]
	v_mfma_i32_16x16x64_i8 v[122:125], v[150:153], v[182:185], v[122:125]
	v_mfma_i32_16x16x64_i8 v[118:121], v[146:149], v[186:189], v[118:121]
	v_mfma_i32_16x16x64_i8 v[114:117], v[150:153], v[186:189], v[114:117]
	v_mfma_i32_16x16x64_i8 v[110:113], v[146:149], v[198:201], v[110:113]
	v_mfma_i32_16x16x64_i8 v[106:109], v[150:153], v[198:201], v[106:109]
	v_mfma_i32_16x16x64_i8 v[102:105], v[146:149], v[202:205], v[102:105]
	v_mfma_i32_16x16x64_i8 v[98:101], v[150:153], v[202:205], v[98:101]
	s_setprio 0
	s_setprio 1
	v_mfma_i32_16x16x64_i8 v[94:97], v[142:145], v[174:177], v[94:97]
	v_mfma_i32_16x16x64_i8 v[90:93], v[138:141], v[174:177], v[90:93]
	v_mfma_i32_16x16x64_i8 v[86:89], v[142:145], v[178:181], v[86:89]
	v_mfma_i32_16x16x64_i8 v[82:85], v[138:141], v[178:181], v[82:85]
	v_mfma_i32_16x16x64_i8 v[78:81], v[142:145], v[190:193], v[78:81]
	v_mfma_i32_16x16x64_i8 v[74:77], v[138:141], v[190:193], v[74:77]
	v_mfma_i32_16x16x64_i8 v[70:73], v[142:145], v[194:197], v[70:73]
	v_mfma_i32_16x16x64_i8 v[66:69], v[138:141], v[194:197], v[66:69]
	s_nop 0
	v_mfma_i32_16x16x64_i8 v[94:97], v[130:133], v[182:185], v[94:97]
	v_mfma_i32_16x16x64_i8 v[90:93], v[134:137], v[182:185], v[90:93]
	v_mfma_i32_16x16x64_i8 v[86:89], v[130:133], v[186:189], v[86:89]
	v_mfma_i32_16x16x64_i8 v[82:85], v[134:137], v[186:189], v[82:85]
	v_mfma_i32_16x16x64_i8 v[78:81], v[130:133], v[198:201], v[78:81]
	v_mfma_i32_16x16x64_i8 v[74:77], v[134:137], v[198:201], v[74:77]
	v_mfma_i32_16x16x64_i8 v[70:73], v[130:133], v[202:205], v[70:73]
	v_mfma_i32_16x16x64_i8 v[66:69], v[134:137], v[202:205], v[66:69]
	s_setprio 0
	s_barrier
	s_mov_b32 m0, s1
	v_lshl_add_u64 v[174:175], s[58:59], 0, v[164:165]
	s_add_u32 s8, s58, 0xe0000
	ds_read_b128 v[182:185], v234 offset:16384
	ds_read_b128 v[186:189], v234 offset:18432
	ds_read_b128 v[190:193], v235 offset:16384
	ds_read_b128 v[194:197], v235 offset:18432
	ds_read_b128 v[198:201], v234 offset:20480
	ds_read_b128 v[202:205], v234 offset:22528
	ds_read_b128 v[206:209], v235 offset:20480
	ds_read_b128 v[210:213], v235 offset:22528
	global_load_lds_dwordx4 v[174:175], off
	v_lshl_add_u64 v[176:177], s[58:59], 0, v[162:163]
	s_mov_b32 m0, s10
	s_addc_u32 s9, s59, 0
	global_load_lds_dwordx4 v[176:177], off
	v_lshl_add_u64 v[178:179], s[8:9], 0, v[164:165]
	s_mov_b32 m0, s11
	v_lshl_add_u64 v[180:181], s[60:61], 0, v[162:163]
	global_load_lds_dwordx4 v[178:179], off
	v_lshl_add_u64 v[178:179], s[8:9], 0, v[162:163]
	s_mov_b32 m0, s24
	s_nop 0
	global_load_lds_dwordx4 v[178:179], off
	v_lshl_add_u64 v[178:179], s[60:61], 0, v[164:165]
	s_mov_b32 m0, s0
	s_nop 0
	global_load_lds_dwordx4 v[178:179], off
	s_mov_b32 m0, s25
	s_nop 0
	global_load_lds_dwordx4 v[180:181], off
	s_waitcnt vmcnt(8)
	s_waitcnt lgkmcnt(0)
	s_barrier
	s_setprio 1
	s_waitcnt lgkmcnt(0)
	v_mfma_i32_16x16x64_i8 v[62:65], v[158:161], v[182:185], v[62:65]
	v_mfma_i32_16x16x64_i8 v[58:61], v[154:157], v[182:185], v[58:61]
	v_mfma_i32_16x16x64_i8 v[54:57], v[158:161], v[186:189], v[54:57]
	v_mfma_i32_16x16x64_i8 v[50:53], v[154:157], v[186:189], v[50:53]
	v_mfma_i32_16x16x64_i8 v[46:49], v[158:161], v[198:201], v[46:49]
	v_mfma_i32_16x16x64_i8 v[42:45], v[154:157], v[198:201], v[42:45]
	v_mfma_i32_16x16x64_i8 v[38:41], v[158:161], v[202:205], v[38:41]
	v_mfma_i32_16x16x64_i8 v[34:37], v[154:157], v[202:205], v[34:37]
	s_nop 0
	v_mfma_i32_16x16x64_i8 v[62:65], v[146:149], v[190:193], v[62:65]
	v_mfma_i32_16x16x64_i8 v[58:61], v[150:153], v[190:193], v[58:61]
	v_mfma_i32_16x16x64_i8 v[54:57], v[146:149], v[194:197], v[54:57]
	v_mfma_i32_16x16x64_i8 v[50:53], v[150:153], v[194:197], v[50:53]
	v_mfma_i32_16x16x64_i8 v[46:49], v[146:149], v[206:209], v[46:49]
	v_mfma_i32_16x16x64_i8 v[42:45], v[150:153], v[206:209], v[42:45]
	v_mfma_i32_16x16x64_i8 v[38:41], v[146:149], v[210:213], v[38:41]
	v_mfma_i32_16x16x64_i8 v[34:37], v[150:153], v[210:213], v[34:37]
	s_setprio 0
	s_setprio 1
	v_mfma_i32_16x16x64_i8 v[30:33], v[142:145], v[182:185], v[30:33]
	v_mfma_i32_16x16x64_i8 v[26:29], v[138:141], v[182:185], v[26:29]
	v_mfma_i32_16x16x64_i8 v[22:25], v[142:145], v[186:189], v[22:25]
	v_mfma_i32_16x16x64_i8 v[18:21], v[138:141], v[186:189], v[18:21]
	v_mfma_i32_16x16x64_i8 v[14:17], v[142:145], v[198:201], v[14:17]
	v_mfma_i32_16x16x64_i8 v[10:13], v[138:141], v[198:201], v[10:13]
	v_mfma_i32_16x16x64_i8 v[6:9], v[142:145], v[202:205], v[6:9]
	v_mfma_i32_16x16x64_i8 v[2:5], v[138:141], v[202:205], v[2:5]
	s_nop 0
	v_mfma_i32_16x16x64_i8 v[30:33], v[130:133], v[190:193], v[30:33]
	v_mfma_i32_16x16x64_i8 v[26:29], v[134:137], v[190:193], v[26:29]
	v_mfma_i32_16x16x64_i8 v[22:25], v[130:133], v[194:197], v[22:25]
	v_mfma_i32_16x16x64_i8 v[18:21], v[134:137], v[194:197], v[18:21]
	v_mfma_i32_16x16x64_i8 v[14:17], v[130:133], v[206:209], v[14:17]
	v_mfma_i32_16x16x64_i8 v[10:13], v[134:137], v[206:209], v[10:13]
	v_mfma_i32_16x16x64_i8 v[6:9], v[130:133], v[210:213], v[6:9]
	v_mfma_i32_16x16x64_i8 v[2:5], v[134:137], v[210:213], v[2:5]
	s_setprio 0
	s_barrier
; #define PG8_STAGE(bufoff, gbase, voff) do { _Pragma("unroll") for (int _i = 0; _i < 2; ++_i) \
;         __builtin_amdgcn_global_load_lds((const unsigned*)((const char*)(gbase) + (voff)[_i]), (LAS unsigned*)(lds + (bufoff) + ldsw + _i * 8192), 16, 0, 0); } while (0)
; #define PG8_LDA(dst, b, h) do { _Pragma("unroll") for (int m = 0; m < 4; ++m) _Pragma("unroll") for (int k = 0; k < 2; ++k) dst[m][k] = *(const LAS bf16x8*)(lds + PG8_SA(b, h) + aoff + m * 2048 + k * 1024); } while (0)
; #define PG8_LDB(dst, b, h) do { _Pragma("unroll") for (int n = 0; n < 2; ++n) _Pragma("unroll") for (int k = 0; k < 2; ++k) dst[n][k] = *(const LAS bf16x8*)(lds + PG8_SB(b, h) + boff + n * 2048 + k * 1024); } while (0)
; #define PG8_MMA(ai, bj, At, Bt) do { __builtin_amdgcn_s_setprio(1); _Pragma("unroll") for (int m = 0; m < 4; ++m) _Pragma("unroll") for (int n = 0; n < 2; ++n) _Pragma("unroll") for (int k = 0; k < 2; ++k) \
;         acc[ai][bj][m][n] = __builtin_amdgcn_mfma_f32_16x16x32_bf16(Bt[n][k], At[m][k], acc[ai][bj][m][n], 0, 0, 0); __builtin_amdgcn_s_setprio(0); } while (0)
; #define PG8_WAIT_V(n) asm volatile("s_waitcnt vmcnt(" #n ")" ::: "memory")
; #define PG8_WAIT_L(n) asm volatile("s_waitcnt lgkmcnt(" #n ")" ::: "memory")
; #define PG8_BAR __builtin_amdgcn_s_barrier()
; #define PG8_SCHED __builtin_amdgcn_sched_barrier(0)
; #define PG8_STAGE(bufoff, gbase, voff) do { _Pragma("unroll") for (int _i = 0; _i < 2; ++_i) \
;         __builtin_amdgcn_global_load_lds((const unsigned*)((const char*)(gbase) + (voff)[_i]), (LAS unsigned*)(lds + (bufoff) + ldsw + _i * 8192), 16, 0, 0); } while (0)
; #define PG8_WAIT_V(n) asm volatile("s_waitcnt vmcnt(" #n ")" ::: "memory")
; #define PG8_WAIT_L(n) asm volatile("s_waitcnt lgkmcnt(" #n ")" ::: "memory")
;     ...
;             PG8_LDB(B0, 1, 0); PG8_LDB(B1, 1, 1); PG8_SCHED; PG8_LDA(At, 1, 0); PG8_STAGE(PG8_SA(0, 1), a2 + hstepA, voffA);
;             PG8_WAIT_V(8); PG8_WAIT_L(0); PG8_BAR; PG8_MMA(0, 0, At, B0); PG8_MMA(0, 1, At, B1); PG8_BAR; PG8_SCHED;
;             PG8_LDA(At, 1, 1); PG8_STAGE(PG8_SB(1, 0), b3, voffB); PG8_STAGE(PG8_SB(1, 1), b3 + hstepB, voffB); PG8_STAGE(PG8_SA(1, 0), a3, voffA);
;             PG8_WAIT_V(8); PG8_WAIT_L(0); PG8_BAR; PG8_MMA(1, 0, At, B0); PG8_MMA(1, 1, At, B1); PG8_BAR; PG8_SCHED;
;         }
;         asm volatile("s_nop 15\n\ts_nop 15" ::: "memory");
;         if (wr == 0) PG8_BAR;
	ds_read_b128 v[130:133], v221
	ds_read_b128 v[134:137], v222
	ds_read_b128 v[138:141], v229
	ds_read_b128 v[142:145], v230
	ds_read_b128 v[146:149], v223
	ds_read_b128 v[150:153], v224
	ds_read_b128 v[154:157], v231
	ds_read_b128 v[158:161], v232
	s_add_u32 s8, s60, 0xe0000
	s_addc_u32 s9, s61, 0
	s_mov_b32 m0, s33
	v_lshl_add_u64 v[214:215], s[8:9], 0, v[164:165]
	ds_read_b128 v[182:185], v234 offset:32768
	ds_read_b128 v[186:189], v234 offset:34816
	ds_read_b128 v[190:193], v235 offset:32768
	ds_read_b128 v[194:197], v235 offset:34816
	ds_read_b128 v[198:201], v234 offset:36864
	ds_read_b128 v[202:205], v234 offset:38912
	ds_read_b128 v[206:209], v235 offset:36864
	ds_read_b128 v[210:213], v235 offset:38912
	global_load_lds_dwordx4 v[214:215], off
	v_lshl_add_u64 v[214:215], s[8:9], 0, v[162:163]
	s_mov_b32 m0, s43
	s_nop 0
	global_load_lds_dwordx4 v[214:215], off
	s_waitcnt vmcnt(8)
	s_waitcnt lgkmcnt(0)
	s_barrier
	s_setprio 1
	s_waitcnt lgkmcnt(0)
	v_mfma_i32_16x16x64_i8 v[126:129], v[130:133], v[182:185], v[126:129]
	v_mfma_i32_16x16x64_i8 v[122:125], v[138:141], v[182:185], v[122:125]
	v_mfma_i32_16x16x64_i8 v[118:121], v[130:133], v[186:189], v[118:121]
	v_mfma_i32_16x16x64_i8 v[114:117], v[138:141], v[186:189], v[114:117]
	v_mfma_i32_16x16x64_i8 v[110:113], v[130:133], v[198:201], v[110:113]
	v_mfma_i32_16x16x64_i8 v[106:109], v[138:141], v[198:201], v[106:109]
	v_mfma_i32_16x16x64_i8 v[102:105], v[130:133], v[202:205], v[102:105]
	v_mfma_i32_16x16x64_i8 v[98:101], v[138:141], v[202:205], v[98:101]
	s_nop 0
	v_mfma_i32_16x16x64_i8 v[126:129], v[134:137], v[190:193], v[126:129]
	v_mfma_i32_16x16x64_i8 v[122:125], v[142:145], v[190:193], v[122:125]
	v_mfma_i32_16x16x64_i8 v[118:121], v[134:137], v[194:197], v[118:121]
	v_mfma_i32_16x16x64_i8 v[114:117], v[142:145], v[194:197], v[114:117]
	v_mfma_i32_16x16x64_i8 v[110:113], v[134:137], v[206:209], v[110:113]
	v_mfma_i32_16x16x64_i8 v[106:109], v[142:145], v[206:209], v[106:109]
	v_mfma_i32_16x16x64_i8 v[102:105], v[134:137], v[210:213], v[102:105]
	v_mfma_i32_16x16x64_i8 v[98:101], v[142:145], v[210:213], v[98:101]
	s_setprio 0
	s_setprio 1
	v_mfma_i32_16x16x64_i8 v[94:97], v[146:149], v[182:185], v[94:97]
	v_mfma_i32_16x16x64_i8 v[90:93], v[154:157], v[182:185], v[90:93]
	v_mfma_i32_16x16x64_i8 v[86:89], v[146:149], v[186:189], v[86:89]
	v_mfma_i32_16x16x64_i8 v[82:85], v[154:157], v[186:189], v[82:85]
	v_mfma_i32_16x16x64_i8 v[78:81], v[146:149], v[198:201], v[78:81]
	v_mfma_i32_16x16x64_i8 v[74:77], v[154:157], v[198:201], v[74:77]
	v_mfma_i32_16x16x64_i8 v[70:73], v[146:149], v[202:205], v[70:73]
	v_mfma_i32_16x16x64_i8 v[66:69], v[154:157], v[202:205], v[66:69]
	s_nop 0
	v_mfma_i32_16x16x64_i8 v[94:97], v[150:153], v[190:193], v[94:97]
	v_mfma_i32_16x16x64_i8 v[90:93], v[158:161], v[190:193], v[90:93]
	v_mfma_i32_16x16x64_i8 v[86:89], v[150:153], v[194:197], v[86:89]
	v_mfma_i32_16x16x64_i8 v[82:85], v[158:161], v[194:197], v[82:85]
	v_mfma_i32_16x16x64_i8 v[78:81], v[150:153], v[206:209], v[78:81]
	v_mfma_i32_16x16x64_i8 v[74:77], v[158:161], v[206:209], v[74:77]
	v_mfma_i32_16x16x64_i8 v[70:73], v[150:153], v[210:213], v[70:73]
	v_mfma_i32_16x16x64_i8 v[66:69], v[158:161], v[210:213], v[66:69]
	s_setprio 0
	s_barrier
	s_mov_b32 m0, s63
	v_lshl_add_u64 v[174:175], v[174:175], 0, s[38:39]
	s_add_u32 s8, s58, 0xe0080
	ds_read_b128 v[182:185], v234 offset:49152
	ds_read_b128 v[186:189], v234 offset:51200
	ds_read_b128 v[190:193], v235 offset:49152
	ds_read_b128 v[194:197], v235 offset:51200
	ds_read_b128 v[198:201], v234 offset:53248
	ds_read_b128 v[202:205], v234 offset:55296
	ds_read_b128 v[206:209], v235 offset:53248
	ds_read_b128 v[210:213], v235 offset:55296
	global_load_lds_dwordx4 v[174:175], off
	v_lshl_add_u64 v[174:175], v[176:177], 0, s[38:39]
	s_mov_b32 m0, s64
	s_addc_u32 s9, s59, 0
	global_load_lds_dwordx4 v[174:175], off
	v_lshl_add_u64 v[174:175], s[8:9], 0, v[164:165]
	s_mov_b32 m0, s67
	s_nop 0
	global_load_lds_dwordx4 v[174:175], off
	v_lshl_add_u64 v[174:175], s[8:9], 0, v[162:163]
	s_mov_b32 m0, s75
	s_nop 0
	global_load_lds_dwordx4 v[174:175], off
	v_lshl_add_u64 v[174:175], v[178:179], 0, s[38:39]
	s_mov_b32 m0, s65
	s_nop 0
	global_load_lds_dwordx4 v[174:175], off
	v_lshl_add_u64 v[174:175], v[180:181], 0, s[38:39]
	s_mov_b32 m0, s66
	s_nop 0
	global_load_lds_dwordx4 v[174:175], off
	s_waitcnt vmcnt(8)
	s_waitcnt lgkmcnt(0)
	s_barrier
	s_setprio 1
	s_waitcnt lgkmcnt(0)
	v_mfma_i32_16x16x64_i8 v[62:65], v[130:133], v[182:185], v[62:65]
	v_mfma_i32_16x16x64_i8 v[58:61], v[138:141], v[182:185], v[58:61]
	v_mfma_i32_16x16x64_i8 v[54:57], v[130:133], v[186:189], v[54:57]
	v_mfma_i32_16x16x64_i8 v[50:53], v[138:141], v[186:189], v[50:53]
	v_mfma_i32_16x16x64_i8 v[46:49], v[130:133], v[198:201], v[46:49]
	v_mfma_i32_16x16x64_i8 v[42:45], v[138:141], v[198:201], v[42:45]
	v_mfma_i32_16x16x64_i8 v[38:41], v[130:133], v[202:205], v[38:41]
	v_mfma_i32_16x16x64_i8 v[34:37], v[138:141], v[202:205], v[34:37]
	s_nop 0
	v_mfma_i32_16x16x64_i8 v[62:65], v[134:137], v[190:193], v[62:65]
	v_mfma_i32_16x16x64_i8 v[58:61], v[142:145], v[190:193], v[58:61]
	v_mfma_i32_16x16x64_i8 v[54:57], v[134:137], v[194:197], v[54:57]
	v_mfma_i32_16x16x64_i8 v[50:53], v[142:145], v[194:197], v[50:53]
	v_mfma_i32_16x16x64_i8 v[46:49], v[134:137], v[206:209], v[46:49]
	v_mfma_i32_16x16x64_i8 v[42:45], v[142:145], v[206:209], v[42:45]
	v_mfma_i32_16x16x64_i8 v[38:41], v[134:137], v[210:213], v[38:41]
	v_mfma_i32_16x16x64_i8 v[34:37], v[142:145], v[210:213], v[34:37]
	s_setprio 0
	s_setprio 1
	v_mfma_i32_16x16x64_i8 v[30:33], v[146:149], v[182:185], v[30:33]
	v_mfma_i32_16x16x64_i8 v[26:29], v[154:157], v[182:185], v[26:29]
	v_mfma_i32_16x16x64_i8 v[22:25], v[146:149], v[186:189], v[22:25]
	v_mfma_i32_16x16x64_i8 v[18:21], v[154:157], v[186:189], v[18:21]
	v_mfma_i32_16x16x64_i8 v[14:17], v[146:149], v[198:201], v[14:17]
	v_mfma_i32_16x16x64_i8 v[10:13], v[154:157], v[198:201], v[10:13]
	v_mfma_i32_16x16x64_i8 v[6:9], v[146:149], v[202:205], v[6:9]
	v_mfma_i32_16x16x64_i8 v[2:5], v[154:157], v[202:205], v[2:5]
	s_nop 0
	v_mfma_i32_16x16x64_i8 v[30:33], v[150:153], v[190:193], v[30:33]
	v_mfma_i32_16x16x64_i8 v[26:29], v[158:161], v[190:193], v[26:29]
	v_mfma_i32_16x16x64_i8 v[22:25], v[150:153], v[194:197], v[22:25]
	v_mfma_i32_16x16x64_i8 v[18:21], v[158:161], v[194:197], v[18:21]
	s_add_i32 s88, s88, 2
	s_add_u32 s86, s86, 0x100
	s_addc_u32 s87, s87, 0
	s_cmp_gt_u32 s88, 53
	s_mov_b64 s[54:55], s[56:57]
	v_mfma_i32_16x16x64_i8 v[14:17], v[150:153], v[206:209], v[14:17]
	v_mfma_i32_16x16x64_i8 v[10:13], v[158:161], v[206:209], v[10:13]
	v_mfma_i32_16x16x64_i8 v[6:9], v[150:153], v[210:213], v[6:9]
	v_mfma_i32_16x16x64_i8 v[2:5], v[158:161], v[210:213], v[2:5]
	s_setprio 0
	s_barrier
	s_cbranch_scc0 .LBB0_667
	s_nop 15
	s_nop 15
	s_and_b64 vcc, exec, s[40:41]
	s_cbranch_vccz .LBB0_670
	s_barrier

; #define PG8_STAGE(bufoff, gbase, voff) do { _Pragma("unroll") for (int _i = 0; _i < 2; ++_i) \
;         __builtin_amdgcn_global_load_lds((const unsigned*)((const char*)(gbase) + (voff)[_i]), (LAS unsigned*)(lds + (bufoff) + ldsw + _i * 8192), 16, 0, 0); } while (0)
; #define PG8_LDA(dst, b, h) do { _Pragma("unroll") for (int m = 0; m < 4; ++m) _Pragma("unroll") for (int k = 0; k < 2; ++k) dst[m][k] = *(const LAS bf16x8*)(lds + PG8_SA(b, h) + aoff + m * 2048 + k * 1024); } while (0)
; #define PG8_LDB(dst, b, h) do { _Pragma("unroll") for (int n = 0; n < 2; ++n) _Pragma("unroll") for (int k = 0; k < 2; ++k) dst[n][k] = *(const LAS bf16x8*)(lds + PG8_SB(b, h) + boff + n * 2048 + k * 1024); } while (0)
; #define PG8_MMA(ai, bj, At, Bt) do { __builtin_amdgcn_s_setprio(1); _Pragma("unroll") for (int m = 0; m < 4; ++m) _Pragma("unroll") for (int n = 0; n < 2; ++n) _Pragma("unroll") for (int k = 0; k < 2; ++k) \
;         acc[ai][bj][m][n] = __builtin_amdgcn_mfma_f32_16x16x32_bf16(Bt[n][k], At[m][k], acc[ai][bj][m][n], 0, 0, 0); __builtin_amdgcn_s_setprio(0); } while (0)
; #define PG8_WAIT_V(n) asm volatile("s_waitcnt vmcnt(" #n ")" ::: "memory")
; #define PG8_WAIT_L(n) asm volatile("s_waitcnt lgkmcnt(" #n ")" ::: "memory")
; #define PG8_BAR __builtin_amdgcn_s_barrier()
; #define PG8_SCHED __builtin_amdgcn_sched_barrier(0)
; #define PG8_LDA(dst, b, h) do { _Pragma("unroll") for (int m = 0; m < 4; ++m) PG8_LD1(dst[m], PG8_SA(b, h) + aoff0 + m * 2048, PG8_SA(b, h) + aoff1 + m * 2048); } while (0)
;     ...
;             const bool last = (t == nt - 2);
;             const char* a1 = cA + (size_t)(t + 1) * kstep;
;             const char* a2 = last ? nA : cA + (size_t)(t + 2) * kstep; const char* b2 = last ? nB : cB + (size_t)(t + 2) * kstep;
;             const char* a3 = a2 + kstep; const char* b3 = b2 + kstep;
;             if (last && has_next) S.a_ready(nxt);
;             PG8_LDB(B0, 0, 0); PG8_LDB(B1, 0, 1); PG8_SCHED; PG8_LDA(At, 0, 0); PG8_STAGE(PG8_SA(1, 1), a1 + hstepA, voffA);
;             PG8_WAIT_V(8); PG8_WAIT_L(0); PG8_BAR; PG8_MMA(0, 0, At, B0); PG8_MMA(0, 1, At, B1); PG8_BAR; PG8_SCHED;
;             PG8_LDA(At, 0, 1); PG8_STAGE(PG8_SB(0, 0), b2, voffB); PG8_STAGE(PG8_SB(0, 1), b2 + hstepB, voffB); PG8_STAGE(PG8_SA(0, 0), a2, voffA);
;             PG8_WAIT_V(8); PG8_WAIT_L(0); PG8_BAR; PG8_MMA(1, 0, At, B0); PG8_MMA(1, 1, At, B1); PG8_BAR; PG8_SCHED;
.LBB0_796:
	ds_read_b128 v[158:161], v187
	ds_read_b128 v[146:149], v188
	ds_read_b128 v[154:157], v195
	ds_read_b128 v[150:153], v196
	ds_read_b128 v[142:145], v189
	ds_read_b128 v[130:133], v190
	ds_read_b128 v[138:141], v197
	ds_read_b128 v[134:137], v198
	s_add_u32 s60, s58, 0x100
	s_addc_u32 s61, s59, 0
	s_cmp_eq_u32 s87, 12
	s_cselect_b32 s65, s45, s61
	s_cselect_b32 s64, s47, s60
	s_cselect_b32 s63, s83, s86
	s_cselect_b32 s62, s84, s85
	v_lshl_add_u64 v[230:231], s[58:59], 0, v[170:171]
	s_add_i32 m0, s0, 0xc000
	ds_read_b128 v[178:181], v204
	ds_read_b128 v[182:185], v204 offset:2048
	ds_read_b128 v[206:209], v205
	ds_read_b128 v[210:213], v205 offset:2048
	ds_read_b128 v[214:217], v204 offset:4096
	ds_read_b128 v[218:221], v204 offset:6144
	ds_read_b128 v[222:225], v205 offset:4096
	ds_read_b128 v[226:229], v205 offset:6144
	global_load_lds_dwordx4 v[230:231], off
	v_lshl_add_u64 v[230:231], s[58:59], 0, v[172:173]
	s_add_i32 m0, s0, 0xe000
	s_nop 0
	global_load_lds_dwordx4 v[230:231], off
	s_waitcnt vmcnt(8)
	s_waitcnt lgkmcnt(0)
	s_barrier
	s_setprio 1
	s_waitcnt lgkmcnt(0)
	v_mfma_i32_16x16x64_i8 v[126:129], v[158:161], v[178:181], v[126:129]
	v_mfma_i32_16x16x64_i8 v[122:125], v[154:157], v[178:181], v[122:125]
	v_mfma_i32_16x16x64_i8 v[118:121], v[158:161], v[182:185], v[118:121]
	v_mfma_i32_16x16x64_i8 v[114:117], v[154:157], v[182:185], v[114:117]
	v_mfma_i32_16x16x64_i8 v[110:113], v[158:161], v[214:217], v[110:113]
	v_mfma_i32_16x16x64_i8 v[106:109], v[154:157], v[214:217], v[106:109]
	v_mfma_i32_16x16x64_i8 v[102:105], v[158:161], v[218:221], v[102:105]
	v_mfma_i32_16x16x64_i8 v[98:101], v[154:157], v[218:221], v[98:101]
	s_nop 0
	v_mfma_i32_16x16x64_i8 v[126:129], v[146:149], v[206:209], v[126:129]
	v_mfma_i32_16x16x64_i8 v[122:125], v[150:153], v[206:209], v[122:125]
	v_mfma_i32_16x16x64_i8 v[118:121], v[146:149], v[210:213], v[118:121]
	v_mfma_i32_16x16x64_i8 v[114:117], v[150:153], v[210:213], v[114:117]
	v_mfma_i32_16x16x64_i8 v[110:113], v[146:149], v[222:225], v[110:113]
	v_mfma_i32_16x16x64_i8 v[106:109], v[150:153], v[222:225], v[106:109]
	v_mfma_i32_16x16x64_i8 v[102:105], v[146:149], v[226:229], v[102:105]
	v_mfma_i32_16x16x64_i8 v[98:101], v[150:153], v[226:229], v[98:101]
	s_setprio 0
	s_setprio 1
	v_mfma_i32_16x16x64_i8 v[94:97], v[142:145], v[178:181], v[94:97]
	v_mfma_i32_16x16x64_i8 v[90:93], v[138:141], v[178:181], v[90:93]
	v_mfma_i32_16x16x64_i8 v[86:89], v[142:145], v[182:185], v[86:89]
	v_mfma_i32_16x16x64_i8 v[82:85], v[138:141], v[182:185], v[82:85]
	v_mfma_i32_16x16x64_i8 v[78:81], v[142:145], v[214:217], v[78:81]
	v_mfma_i32_16x16x64_i8 v[74:77], v[138:141], v[214:217], v[74:77]
	v_mfma_i32_16x16x64_i8 v[70:73], v[142:145], v[218:221], v[70:73]
	v_mfma_i32_16x16x64_i8 v[66:69], v[138:141], v[218:221], v[66:69]
	s_nop 0
	v_mfma_i32_16x16x64_i8 v[94:97], v[130:133], v[206:209], v[94:97]
	v_mfma_i32_16x16x64_i8 v[90:93], v[134:137], v[206:209], v[90:93]
	v_mfma_i32_16x16x64_i8 v[86:89], v[130:133], v[210:213], v[86:89]
	v_mfma_i32_16x16x64_i8 v[82:85], v[134:137], v[210:213], v[82:85]
	v_mfma_i32_16x16x64_i8 v[78:81], v[130:133], v[222:225], v[78:81]
	v_mfma_i32_16x16x64_i8 v[74:77], v[134:137], v[222:225], v[74:77]
	v_mfma_i32_16x16x64_i8 v[70:73], v[130:133], v[226:229], v[70:73]
	v_mfma_i32_16x16x64_i8 v[66:69], v[134:137], v[226:229], v[66:69]
	s_setprio 0
	s_barrier
	s_mov_b32 m0, s1
	v_lshl_add_u64 v[178:179], s[62:63], 0, v[166:167]
	s_add_u32 s8, s62, 0x40000
	ds_read_b128 v[206:209], v204 offset:16384
	ds_read_b128 v[210:213], v204 offset:18432
	ds_read_b128 v[214:217], v205 offset:16384
	ds_read_b128 v[218:221], v205 offset:18432
	ds_read_b128 v[222:225], v204 offset:20480
	ds_read_b128 v[226:229], v204 offset:22528
	ds_read_b128 v[230:233], v205 offset:20480
	ds_read_b128 v[234:237], v205 offset:22528
	global_load_lds_dwordx4 v[178:179], off
	v_lshl_add_u64 v[180:181], s[62:63], 0, v[162:163]
	s_mov_b32 m0, s10
	s_addc_u32 s9, s63, 0
	global_load_lds_dwordx4 v[180:181], off
	v_lshl_add_u64 v[182:183], s[8:9], 0, v[166:167]
	s_mov_b32 m0, s11
	v_lshl_add_u64 v[184:185], s[64:65], 0, v[164:165]
	global_load_lds_dwordx4 v[182:183], off
	v_lshl_add_u64 v[182:183], s[8:9], 0, v[162:163]
	s_mov_b32 m0, s24
	s_nop 0
	global_load_lds_dwordx4 v[182:183], off
	v_lshl_add_u64 v[182:183], s[64:65], 0, v[168:169]
	s_mov_b32 m0, s0
	s_nop 0
	global_load_lds_dwordx4 v[182:183], off
	s_mov_b32 m0, s25
	s_nop 0
	global_load_lds_dwordx4 v[184:185], off
	s_waitcnt vmcnt(8)
	s_waitcnt lgkmcnt(0)
	s_barrier
	s_setprio 1
	s_waitcnt lgkmcnt(0)
	v_mfma_i32_16x16x64_i8 v[62:65], v[158:161], v[206:209], v[62:65]
	v_mfma_i32_16x16x64_i8 v[58:61], v[154:157], v[206:209], v[58:61]
	v_mfma_i32_16x16x64_i8 v[54:57], v[158:161], v[210:213], v[54:57]
	v_mfma_i32_16x16x64_i8 v[50:53], v[154:157], v[210:213], v[50:53]
	v_mfma_i32_16x16x64_i8 v[46:49], v[158:161], v[222:225], v[46:49]
	v_mfma_i32_16x16x64_i8 v[42:45], v[154:157], v[222:225], v[42:45]
	v_mfma_i32_16x16x64_i8 v[38:41], v[158:161], v[226:229], v[38:41]
	v_mfma_i32_16x16x64_i8 v[34:37], v[154:157], v[226:229], v[34:37]
	s_nop 0
	v_mfma_i32_16x16x64_i8 v[62:65], v[146:149], v[214:217], v[62:65]
	v_mfma_i32_16x16x64_i8 v[58:61], v[150:153], v[214:217], v[58:61]
	v_mfma_i32_16x16x64_i8 v[54:57], v[146:149], v[218:221], v[54:57]
	v_mfma_i32_16x16x64_i8 v[50:53], v[150:153], v[218:221], v[50:53]
	v_mfma_i32_16x16x64_i8 v[46:49], v[146:149], v[230:233], v[46:49]
	v_mfma_i32_16x16x64_i8 v[42:45], v[150:153], v[230:233], v[42:45]
	v_mfma_i32_16x16x64_i8 v[38:41], v[146:149], v[234:237], v[38:41]
	v_mfma_i32_16x16x64_i8 v[34:37], v[150:153], v[234:237], v[34:37]
	s_setprio 0
	s_setprio 1
	v_mfma_i32_16x16x64_i8 v[30:33], v[142:145], v[206:209], v[30:33]
	v_mfma_i32_16x16x64_i8 v[26:29], v[138:141], v[206:209], v[26:29]
	v_mfma_i32_16x16x64_i8 v[22:25], v[142:145], v[210:213], v[22:25]
	v_mfma_i32_16x16x64_i8 v[18:21], v[138:141], v[210:213], v[18:21]
	v_mfma_i32_16x16x64_i8 v[14:17], v[142:145], v[222:225], v[14:17]
	v_mfma_i32_16x16x64_i8 v[10:13], v[138:141], v[222:225], v[10:13]
	v_mfma_i32_16x16x64_i8 v[6:9], v[142:145], v[226:229], v[6:9]
	v_mfma_i32_16x16x64_i8 v[2:5], v[138:141], v[226:229], v[2:5]
	s_nop 0
	v_mfma_i32_16x16x64_i8 v[30:33], v[130:133], v[214:217], v[30:33]
	v_mfma_i32_16x16x64_i8 v[26:29], v[134:137], v[214:217], v[26:29]
	v_mfma_i32_16x16x64_i8 v[22:25], v[130:133], v[218:221], v[22:25]
	v_mfma_i32_16x16x64_i8 v[18:21], v[134:137], v[218:221], v[18:21]
	v_mfma_i32_16x16x64_i8 v[14:17], v[130:133], v[230:233], v[14:17]
	v_mfma_i32_16x16x64_i8 v[10:13], v[134:137], v[230:233], v[10:13]
	v_mfma_i32_16x16x64_i8 v[6:9], v[130:133], v[234:237], v[6:9]
	v_mfma_i32_16x16x64_i8 v[2:5], v[134:137], v[234:237], v[2:5]
	s_setprio 0
	s_barrier
; #define PG8_STAGE(bufoff, gbase, voff) do { _Pragma("unroll") for (int _i = 0; _i < 2; ++_i) \
;         __builtin_amdgcn_global_load_lds((const unsigned*)((const char*)(gbase) + (voff)[_i]), (LAS unsigned*)(lds + (bufoff) + ldsw + _i * 8192), 16, 0, 0); } while (0)
; #define PG8_LDA(dst, b, h) do { _Pragma("unroll") for (int m = 0; m < 4; ++m) _Pragma("unroll") for (int k = 0; k < 2; ++k) dst[m][k] = *(const LAS bf16x8*)(lds + PG8_SA(b, h) + aoff + m * 2048 + k * 1024); } while (0)
; #define PG8_LDB(dst, b, h) do { _Pragma("unroll") for (int n = 0; n < 2; ++n) _Pragma("unroll") for (int k = 0; k < 2; ++k) dst[n][k] = *(const LAS bf16x8*)(lds + PG8_SB(b, h) + boff + n * 2048 + k * 1024); } while (0)
; #define PG8_MMA(ai, bj, At, Bt) do { __builtin_amdgcn_s_setprio(1); _Pragma("unroll") for (int m = 0; m < 4; ++m) _Pragma("unroll") for (int n = 0; n < 2; ++n) _Pragma("unroll") for (int k = 0; k < 2; ++k) \
;         acc[ai][bj][m][n] = __builtin_amdgcn_mfma_f32_16x16x32_bf16(Bt[n][k], At[m][k], acc[ai][bj][m][n], 0, 0, 0); __builtin_amdgcn_s_setprio(0); } while (0)
; #define PG8_WAIT_V(n) asm volatile("s_waitcnt vmcnt(" #n ")" ::: "memory")
; #define PG8_WAIT_L(n) asm volatile("s_waitcnt lgkmcnt(" #n ")" ::: "memory")
; #define PG8_BAR __builtin_amdgcn_s_barrier()
; #define PG8_SCHED __builtin_amdgcn_sched_barrier(0)
; #define PG8_STAGE(bufoff, gbase, voff) do { _Pragma("unroll") for (int _i = 0; _i < 2; ++_i) \
;         __builtin_amdgcn_global_load_lds((const unsigned*)((const char*)(gbase) + (voff)[_i]), (LAS unsigned*)(lds + (bufoff) + ldsw + _i * 8192), 16, 0, 0); } while (0)
; #define PG8_WAIT_V(n) asm volatile("s_waitcnt vmcnt(" #n ")" ::: "memory")
; #define PG8_WAIT_L(n) asm volatile("s_waitcnt lgkmcnt(" #n ")" ::: "memory")
;     ...
;             PG8_LDB(B0, 1, 0); PG8_LDB(B1, 1, 1); PG8_SCHED; PG8_LDA(At, 1, 0); PG8_STAGE(PG8_SA(0, 1), a2 + hstepA, voffA);
;             PG8_WAIT_V(8); PG8_WAIT_L(0); PG8_BAR; PG8_MMA(0, 0, At, B0); PG8_MMA(0, 1, At, B1); PG8_BAR; PG8_SCHED;
;             PG8_LDA(At, 1, 1); PG8_STAGE(PG8_SB(1, 0), b3, voffB); PG8_STAGE(PG8_SB(1, 1), b3 + hstepB, voffB); PG8_STAGE(PG8_SA(1, 0), a3, voffA);
;             PG8_WAIT_V(8); PG8_WAIT_L(0); PG8_BAR; PG8_MMA(1, 0, At, B0); PG8_MMA(1, 1, At, B1); PG8_BAR; PG8_SCHED;
;         }
;         asm volatile("s_nop 15\n\ts_nop 15" ::: "memory");
;         if (wr == 0) PG8_BAR;
	ds_read_b128 v[130:133], v191
	ds_read_b128 v[134:137], v192
	ds_read_b128 v[138:141], v199
	ds_read_b128 v[142:145], v200
	ds_read_b128 v[146:149], v193
	ds_read_b128 v[150:153], v194
	ds_read_b128 v[154:157], v201
	ds_read_b128 v[158:161], v202
	s_add_u32 s8, s64, 0x40000
	s_addc_u32 s9, s65, 0
	s_mov_b32 m0, s33
	v_lshl_add_u64 v[238:239], s[8:9], 0, v[168:169]
	ds_read_b128 v[206:209], v204 offset:32768
	ds_read_b128 v[210:213], v204 offset:34816
	ds_read_b128 v[214:217], v205 offset:32768
	ds_read_b128 v[218:221], v205 offset:34816
	ds_read_b128 v[222:225], v204 offset:36864
	ds_read_b128 v[226:229], v204 offset:38912
	ds_read_b128 v[230:233], v205 offset:36864
	ds_read_b128 v[234:237], v205 offset:38912
	global_load_lds_dwordx4 v[238:239], off
	v_lshl_add_u64 v[238:239], s[8:9], 0, v[164:165]
	s_mov_b32 m0, s43
	s_nop 0
	global_load_lds_dwordx4 v[238:239], off
	s_waitcnt vmcnt(8)
	s_waitcnt lgkmcnt(0)
	s_barrier
	s_setprio 1
	s_waitcnt lgkmcnt(0)
	v_mfma_i32_16x16x64_i8 v[126:129], v[130:133], v[206:209], v[126:129]
	v_mfma_i32_16x16x64_i8 v[122:125], v[138:141], v[206:209], v[122:125]
	v_mfma_i32_16x16x64_i8 v[118:121], v[130:133], v[210:213], v[118:121]
	v_mfma_i32_16x16x64_i8 v[114:117], v[138:141], v[210:213], v[114:117]
	v_mfma_i32_16x16x64_i8 v[110:113], v[130:133], v[222:225], v[110:113]
	v_mfma_i32_16x16x64_i8 v[106:109], v[138:141], v[222:225], v[106:109]
	v_mfma_i32_16x16x64_i8 v[102:105], v[130:133], v[226:229], v[102:105]
	v_mfma_i32_16x16x64_i8 v[98:101], v[138:141], v[226:229], v[98:101]
	s_nop 0
	v_mfma_i32_16x16x64_i8 v[126:129], v[134:137], v[214:217], v[126:129]
	v_mfma_i32_16x16x64_i8 v[122:125], v[142:145], v[214:217], v[122:125]
	v_mfma_i32_16x16x64_i8 v[118:121], v[134:137], v[218:221], v[118:121]
	v_mfma_i32_16x16x64_i8 v[114:117], v[142:145], v[218:221], v[114:117]
	v_mfma_i32_16x16x64_i8 v[110:113], v[134:137], v[230:233], v[110:113]
	v_mfma_i32_16x16x64_i8 v[106:109], v[142:145], v[230:233], v[106:109]
	v_mfma_i32_16x16x64_i8 v[102:105], v[134:137], v[234:237], v[102:105]
	v_mfma_i32_16x16x64_i8 v[98:101], v[142:145], v[234:237], v[98:101]
	s_setprio 0
	s_setprio 1
	v_mfma_i32_16x16x64_i8 v[94:97], v[146:149], v[206:209], v[94:97]
	v_mfma_i32_16x16x64_i8 v[90:93], v[154:157], v[206:209], v[90:93]
	v_mfma_i32_16x16x64_i8 v[86:89], v[146:149], v[210:213], v[86:89]
	v_mfma_i32_16x16x64_i8 v[82:85], v[154:157], v[210:213], v[82:85]
	v_mfma_i32_16x16x64_i8 v[78:81], v[146:149], v[222:225], v[78:81]
	v_mfma_i32_16x16x64_i8 v[74:77], v[154:157], v[222:225], v[74:77]
	v_mfma_i32_16x16x64_i8 v[70:73], v[146:149], v[226:229], v[70:73]
	v_mfma_i32_16x16x64_i8 v[66:69], v[154:157], v[226:229], v[66:69]
	s_nop 0
	v_mfma_i32_16x16x64_i8 v[94:97], v[150:153], v[214:217], v[94:97]
	v_mfma_i32_16x16x64_i8 v[90:93], v[158:161], v[214:217], v[90:93]
	v_mfma_i32_16x16x64_i8 v[86:89], v[150:153], v[218:221], v[86:89]
	v_mfma_i32_16x16x64_i8 v[82:85], v[158:161], v[218:221], v[82:85]
	v_mfma_i32_16x16x64_i8 v[78:81], v[150:153], v[230:233], v[78:81]
	v_mfma_i32_16x16x64_i8 v[74:77], v[158:161], v[230:233], v[74:77]
	v_mfma_i32_16x16x64_i8 v[70:73], v[150:153], v[234:237], v[70:73]
	v_mfma_i32_16x16x64_i8 v[66:69], v[158:161], v[234:237], v[66:69]
	s_setprio 0
	s_barrier
	s_mov_b32 m0, s66
	v_lshl_add_u64 v[178:179], v[178:179], 0, s[38:39]
	s_add_u32 s8, s62, 0x40080
	ds_read_b128 v[206:209], v204 offset:49152
	ds_read_b128 v[210:213], v204 offset:51200
	ds_read_b128 v[214:217], v205 offset:49152
	ds_read_b128 v[218:221], v205 offset:51200
	ds_read_b128 v[222:225], v204 offset:53248
	ds_read_b128 v[226:229], v204 offset:55296
	ds_read_b128 v[230:233], v205 offset:53248
	ds_read_b128 v[234:237], v205 offset:55296
	global_load_lds_dwordx4 v[178:179], off
	v_lshl_add_u64 v[178:179], v[180:181], 0, s[38:39]
	s_mov_b32 m0, s67
	s_addc_u32 s9, s63, 0
	global_load_lds_dwordx4 v[178:179], off
	v_lshl_add_u64 v[178:179], s[8:9], 0, v[166:167]
	s_mov_b32 m0, s79
	s_nop 0
	global_load_lds_dwordx4 v[178:179], off
	v_lshl_add_u64 v[178:179], s[8:9], 0, v[162:163]
	s_mov_b32 m0, s80
	s_nop 0
	global_load_lds_dwordx4 v[178:179], off
	v_lshl_add_u64 v[178:179], v[182:183], 0, s[38:39]
	s_mov_b32 m0, s75
	s_nop 0
	global_load_lds_dwordx4 v[178:179], off
	v_lshl_add_u64 v[178:179], v[184:185], 0, s[38:39]
	s_mov_b32 m0, s78
	s_nop 0
	global_load_lds_dwordx4 v[178:179], off
	s_waitcnt vmcnt(8)
	s_waitcnt lgkmcnt(0)
	s_barrier
	s_setprio 1
	s_waitcnt lgkmcnt(0)
	v_mfma_i32_16x16x64_i8 v[62:65], v[130:133], v[206:209], v[62:65]
	v_mfma_i32_16x16x64_i8 v[58:61], v[138:141], v[206:209], v[58:61]
	v_mfma_i32_16x16x64_i8 v[54:57], v[130:133], v[210:213], v[54:57]
	v_mfma_i32_16x16x64_i8 v[50:53], v[138:141], v[210:213], v[50:53]
	v_mfma_i32_16x16x64_i8 v[46:49], v[130:133], v[222:225], v[46:49]
	v_mfma_i32_16x16x64_i8 v[42:45], v[138:141], v[222:225], v[42:45]
	v_mfma_i32_16x16x64_i8 v[38:41], v[130:133], v[226:229], v[38:41]
	v_mfma_i32_16x16x64_i8 v[34:37], v[138:141], v[226:229], v[34:37]
	s_nop 0
	v_mfma_i32_16x16x64_i8 v[62:65], v[134:137], v[214:217], v[62:65]
	v_mfma_i32_16x16x64_i8 v[58:61], v[142:145], v[214:217], v[58:61]
	v_mfma_i32_16x16x64_i8 v[54:57], v[134:137], v[218:221], v[54:57]
	v_mfma_i32_16x16x64_i8 v[50:53], v[142:145], v[218:221], v[50:53]
	v_mfma_i32_16x16x64_i8 v[46:49], v[134:137], v[230:233], v[46:49]
	v_mfma_i32_16x16x64_i8 v[42:45], v[142:145], v[230:233], v[42:45]
	v_mfma_i32_16x16x64_i8 v[38:41], v[134:137], v[234:237], v[38:41]
	v_mfma_i32_16x16x64_i8 v[34:37], v[142:145], v[234:237], v[34:37]
	s_setprio 0
	s_setprio 1
	v_mfma_i32_16x16x64_i8 v[30:33], v[146:149], v[206:209], v[30:33]
	v_mfma_i32_16x16x64_i8 v[26:29], v[154:157], v[206:209], v[26:29]
	v_mfma_i32_16x16x64_i8 v[22:25], v[146:149], v[210:213], v[22:25]
	v_mfma_i32_16x16x64_i8 v[18:21], v[154:157], v[210:213], v[18:21]
	v_mfma_i32_16x16x64_i8 v[14:17], v[146:149], v[222:225], v[14:17]
	v_mfma_i32_16x16x64_i8 v[10:13], v[154:157], v[222:225], v[10:13]
	v_mfma_i32_16x16x64_i8 v[6:9], v[146:149], v[226:229], v[6:9]
	v_mfma_i32_16x16x64_i8 v[2:5], v[154:157], v[226:229], v[2:5]
	s_nop 0
	v_mfma_i32_16x16x64_i8 v[30:33], v[150:153], v[214:217], v[30:33]
	v_mfma_i32_16x16x64_i8 v[26:29], v[158:161], v[214:217], v[26:29]
	v_mfma_i32_16x16x64_i8 v[22:25], v[150:153], v[218:221], v[22:25]
	v_mfma_i32_16x16x64_i8 v[18:21], v[158:161], v[218:221], v[18:21]
	s_add_i32 s87, s87, 2
	s_add_u32 s85, s85, 0x100
	s_addc_u32 s86, s86, 0
	s_cmp_gt_u32 s87, 13
	s_mov_b64 s[58:59], s[60:61]
	v_mfma_i32_16x16x64_i8 v[14:17], v[150:153], v[230:233], v[14:17]
	v_mfma_i32_16x16x64_i8 v[10:13], v[158:161], v[230:233], v[10:13]
	v_mfma_i32_16x16x64_i8 v[6:9], v[150:153], v[234:237], v[6:9]
	v_mfma_i32_16x16x64_i8 v[2:5], v[158:161], v[234:237], v[2:5]
	s_setprio 0
	s_barrier
	s_cbranch_scc0 .LBB0_796
	s_nop 15
	s_nop 15
	s_and_b64 vcc, exec, s[40:41]
	s_cbranch_vccz .LBB0_799
	s_barrier

; #define PG8_STAGE(bufoff, gbase, voff) do { _Pragma("unroll") for (int _i = 0; _i < 2; ++_i) \
;         __builtin_amdgcn_global_load_lds((const unsigned*)((const char*)(gbase) + (voff)[_i]), (LAS unsigned*)(lds + (bufoff) + ldsw + _i * 8192), 16, 0, 0); } while (0)
; #define PG8_LDA(dst, b, h) do { _Pragma("unroll") for (int m = 0; m < 4; ++m) _Pragma("unroll") for (int k = 0; k < 2; ++k) dst[m][k] = *(const LAS bf16x8*)(lds + PG8_SA(b, h) + aoff + m * 2048 + k * 1024); } while (0)
; #define PG8_LDB(dst, b, h) do { _Pragma("unroll") for (int n = 0; n < 2; ++n) _Pragma("unroll") for (int k = 0; k < 2; ++k) dst[n][k] = *(const LAS bf16x8*)(lds + PG8_SB(b, h) + boff + n * 2048 + k * 1024); } while (0)
; #define PG8_MMA(ai, bj, At, Bt) do { __builtin_amdgcn_s_setprio(1); _Pragma("unroll") for (int m = 0; m < 4; ++m) _Pragma("unroll") for (int n = 0; n < 2; ++n) _Pragma("unroll") for (int k = 0; k < 2; ++k) \
;         acc[ai][bj][m][n] = __builtin_amdgcn_mfma_f32_16x16x32_bf16(Bt[n][k], At[m][k], acc[ai][bj][m][n], 0, 0, 0); __builtin_amdgcn_s_setprio(0); } while (0)
; #define PG8_WAIT_V(n) asm volatile("s_waitcnt vmcnt(" #n ")" ::: "memory")
; #define PG8_WAIT_L(n) asm volatile("s_waitcnt lgkmcnt(" #n ")" ::: "memory")
; #define PG8_BAR __builtin_amdgcn_s_barrier()
; #define PG8_SCHED __builtin_amdgcn_sched_barrier(0)
; #define PG8_LDA(dst, b, h) do { _Pragma("unroll") for (int m = 0; m < 4; ++m) PG8_LD1(dst[m], PG8_SA(b, h) + aoff0 + m * 2048, PG8_SA(b, h) + aoff1 + m * 2048); } while (0)
;     ...
;             const bool last = (t == nt - 2);
;             const char* a1 = cA + (size_t)(t + 1) * kstep;
;             const char* a2 = last ? nA : cA + (size_t)(t + 2) * kstep; const char* b2 = last ? nB : cB + (size_t)(t + 2) * kstep;
;             const char* a3 = a2 + kstep; const char* b3 = b2 + kstep;
;             if (last && has_next) S.a_ready(nxt);
;             PG8_LDB(B0, 0, 0); PG8_LDB(B1, 0, 1); PG8_SCHED; PG8_LDA(At, 0, 0); PG8_STAGE(PG8_SA(1, 1), a1 + hstepA, voffA);
;             PG8_WAIT_V(8); PG8_WAIT_L(0); PG8_BAR; PG8_MMA(0, 0, At, B0); PG8_MMA(0, 1, At, B1); PG8_BAR; PG8_SCHED;
;             PG8_LDA(At, 0, 1); PG8_STAGE(PG8_SB(0, 0), b2, voffB); PG8_STAGE(PG8_SB(0, 1), b2 + hstepB, voffB); PG8_STAGE(PG8_SA(0, 0), a2, voffA);
;             PG8_WAIT_V(8); PG8_WAIT_L(0); PG8_BAR; PG8_MMA(1, 0, At, B0); PG8_MMA(1, 1, At, B1); PG8_BAR; PG8_SCHED;
.LBB0_1121:
	ds_read_b128 v[18:21], v183
	ds_read_b128 v[22:25], v184
	ds_read_b128 v[26:29], v191
	ds_read_b128 v[30:33], v192
	ds_read_b128 v[2:5], v185
	ds_read_b128 v[6:9], v186
	ds_read_b128 v[10:13], v193
	ds_read_b128 v[14:17], v194
	s_add_u32 s56, s54, 0x100
	s_addc_u32 s57, s55, 0
	s_cmp_eq_u32 s83, 12
	s_cselect_b32 s61, s41, s57
	s_cselect_b32 s60, s43, s56
	s_cselect_b32 s59, s79, s82
	s_cselect_b32 s58, s80, s81
	v_lshl_add_u64 v[226:227], s[54:55], 0, v[166:167]
	s_add_i32 m0, s15, 0xc000
	ds_read_b128 v[174:177], v200
	ds_read_b128 v[202:205], v200 offset:2048
	ds_read_b128 v[178:181], v201
	ds_read_b128 v[206:209], v201 offset:2048
	ds_read_b128 v[210:213], v200 offset:4096
	ds_read_b128 v[218:221], v200 offset:6144
	ds_read_b128 v[214:217], v201 offset:4096
	ds_read_b128 v[222:225], v201 offset:6144
	global_load_lds_dwordx4 v[226:227], off
	v_lshl_add_u64 v[226:227], s[54:55], 0, v[168:169]
	s_add_i32 m0, s15, 0xe000
	s_nop 0
	global_load_lds_dwordx4 v[226:227], off
	s_waitcnt vmcnt(8)
	s_waitcnt lgkmcnt(0)
	s_barrier
	s_setprio 1
	s_waitcnt lgkmcnt(0)
	v_mfma_f32_16x16x128_f8f6f4 v[158:161], v[18:25], v[174:181], v[158:161]
	v_mfma_f32_16x16x128_f8f6f4 v[154:157], v[26:33], v[174:181], v[154:157]
	v_mfma_f32_16x16x128_f8f6f4 v[150:153], v[18:25], v[202:209], v[150:153]
	v_mfma_f32_16x16x128_f8f6f4 v[146:149], v[26:33], v[202:209], v[146:149]
	v_mfma_f32_16x16x128_f8f6f4 v[126:129], v[18:25], v[210:217], v[126:129]
	v_mfma_f32_16x16x128_f8f6f4 v[122:125], v[26:33], v[210:217], v[122:125]
	v_mfma_f32_16x16x128_f8f6f4 v[118:121], v[18:25], v[218:225], v[118:121]
	v_mfma_f32_16x16x128_f8f6f4 v[114:117], v[26:33], v[218:225], v[114:117]
	s_setprio 0
	s_setprio 1
	v_mfma_f32_16x16x128_f8f6f4 v[142:145], v[2:9], v[174:181], v[142:145]
	v_mfma_f32_16x16x128_f8f6f4 v[138:141], v[10:17], v[174:181], v[138:141]
	v_mfma_f32_16x16x128_f8f6f4 v[134:137], v[2:9], v[202:209], v[134:137]
	v_mfma_f32_16x16x128_f8f6f4 v[130:133], v[10:17], v[202:209], v[130:133]
	v_mfma_f32_16x16x128_f8f6f4 v[110:113], v[2:9], v[210:217], v[110:113]
	v_mfma_f32_16x16x128_f8f6f4 v[106:109], v[10:17], v[210:217], v[106:109]
	v_mfma_f32_16x16x128_f8f6f4 v[102:105], v[2:9], v[218:225], v[102:105]
	v_mfma_f32_16x16x128_f8f6f4 v[98:101], v[10:17], v[218:225], v[98:101]
	s_setprio 0
	s_barrier
	s_mov_b32 m0, s24
	v_lshl_add_u64 v[174:175], s[58:59], 0, v[164:165]
	s_add_u32 s18, s58, 0x40000
	ds_read_b128 v[202:205], v200 offset:16384
	ds_read_b128 v[210:213], v200 offset:18432
	ds_read_b128 v[206:209], v201 offset:16384
	ds_read_b128 v[214:217], v201 offset:18432
	ds_read_b128 v[218:221], v200 offset:20480
	ds_read_b128 v[226:229], v200 offset:22528
	ds_read_b128 v[222:225], v201 offset:20480
	ds_read_b128 v[230:233], v201 offset:22528
	global_load_lds_dwordx4 v[174:175], off
	v_lshl_add_u64 v[176:177], s[58:59], 0, v[162:163]
	s_mov_b32 m0, s25
	s_addc_u32 s19, s59, 0
	global_load_lds_dwordx4 v[176:177], off
	v_lshl_add_u64 v[178:179], s[18:19], 0, v[164:165]
	s_mov_b32 m0, s33
	v_lshl_add_u64 v[180:181], s[60:61], 0, v[162:163]
	global_load_lds_dwordx4 v[178:179], off
	v_lshl_add_u64 v[178:179], s[18:19], 0, v[162:163]
	s_mov_b32 m0, s35
	s_nop 0
	global_load_lds_dwordx4 v[178:179], off
	v_lshl_add_u64 v[178:179], s[60:61], 0, v[164:165]
	s_mov_b32 m0, s15
	s_nop 0
	global_load_lds_dwordx4 v[178:179], off
	s_mov_b32 m0, s62
	s_nop 0
	global_load_lds_dwordx4 v[180:181], off
	s_waitcnt vmcnt(8)
	s_waitcnt lgkmcnt(0)
	s_barrier
	s_setprio 1
	s_waitcnt lgkmcnt(0)
	v_mfma_f32_16x16x128_f8f6f4 v[94:97], v[18:25], v[202:209], v[94:97]
	v_mfma_f32_16x16x128_f8f6f4 v[90:93], v[26:33], v[202:209], v[90:93]
	v_mfma_f32_16x16x128_f8f6f4 v[86:89], v[18:25], v[210:217], v[86:89]
	v_mfma_f32_16x16x128_f8f6f4 v[78:81], v[26:33], v[210:217], v[78:81]
	v_mfma_f32_16x16x128_f8f6f4 v[70:73], v[18:25], v[218:225], v[70:73]
	v_mfma_f32_16x16x128_f8f6f4 v[62:65], v[26:33], v[218:225], v[62:65]
	v_mfma_f32_16x16x128_f8f6f4 v[54:57], v[18:25], v[226:233], v[54:57]
	v_mfma_f32_16x16x128_f8f6f4 v[46:49], v[26:33], v[226:233], v[46:49]
	s_setprio 0
	s_setprio 1
	v_mfma_f32_16x16x128_f8f6f4 v[82:85], v[2:9], v[202:209], v[82:85]
	v_mfma_f32_16x16x128_f8f6f4 v[74:77], v[10:17], v[202:209], v[74:77]
	v_mfma_f32_16x16x128_f8f6f4 v[66:69], v[2:9], v[210:217], v[66:69]
	v_mfma_f32_16x16x128_f8f6f4 v[58:61], v[10:17], v[210:217], v[58:61]
	v_mfma_f32_16x16x128_f8f6f4 v[50:53], v[2:9], v[218:225], v[50:53]
	v_mfma_f32_16x16x128_f8f6f4 v[42:45], v[10:17], v[218:225], v[42:45]
	v_mfma_f32_16x16x128_f8f6f4 v[38:41], v[2:9], v[226:233], v[38:41]
	v_mfma_f32_16x16x128_f8f6f4 v[34:37], v[10:17], v[226:233], v[34:37]
	s_setprio 0
	s_barrier
; #define PG8_STAGE(bufoff, gbase, voff) do { _Pragma("unroll") for (int _i = 0; _i < 2; ++_i) \
;         __builtin_amdgcn_global_load_lds((const unsigned*)((const char*)(gbase) + (voff)[_i]), (LAS unsigned*)(lds + (bufoff) + ldsw + _i * 8192), 16, 0, 0); } while (0)
; #define PG8_LDA(dst, b, h) do { _Pragma("unroll") for (int m = 0; m < 4; ++m) _Pragma("unroll") for (int k = 0; k < 2; ++k) dst[m][k] = *(const LAS bf16x8*)(lds + PG8_SA(b, h) + aoff + m * 2048 + k * 1024); } while (0)
; #define PG8_LDB(dst, b, h) do { _Pragma("unroll") for (int n = 0; n < 2; ++n) _Pragma("unroll") for (int k = 0; k < 2; ++k) dst[n][k] = *(const LAS bf16x8*)(lds + PG8_SB(b, h) + boff + n * 2048 + k * 1024); } while (0)
; #define PG8_MMA(ai, bj, At, Bt) do { __builtin_amdgcn_s_setprio(1); _Pragma("unroll") for (int m = 0; m < 4; ++m) _Pragma("unroll") for (int n = 0; n < 2; ++n) _Pragma("unroll") for (int k = 0; k < 2; ++k) \
;         acc[ai][bj][m][n] = __builtin_amdgcn_mfma_f32_16x16x32_bf16(Bt[n][k], At[m][k], acc[ai][bj][m][n], 0, 0, 0); __builtin_amdgcn_s_setprio(0); } while (0)
; #define PG8_WAIT_V(n) asm volatile("s_waitcnt vmcnt(" #n ")" ::: "memory")
; #define PG8_WAIT_L(n) asm volatile("s_waitcnt lgkmcnt(" #n ")" ::: "memory")
; #define PG8_BAR __builtin_amdgcn_s_barrier()
; #define PG8_SCHED __builtin_amdgcn_sched_barrier(0)
; #define PG8_STAGE(bufoff, gbase, voff) do { _Pragma("unroll") for (int _i = 0; _i < 2; ++_i) \
;         __builtin_amdgcn_global_load_lds((const unsigned*)((const char*)(gbase) + (voff)[_i]), (LAS unsigned*)(lds + (bufoff) + ldsw + _i * 8192), 16, 0, 0); } while (0)
; #define PG8_WAIT_V(n) asm volatile("s_waitcnt vmcnt(" #n ")" ::: "memory")
; #define PG8_WAIT_L(n) asm volatile("s_waitcnt lgkmcnt(" #n ")" ::: "memory")
;     ...
;             PG8_LDB(B0, 1, 0); PG8_LDB(B1, 1, 1); PG8_SCHED; PG8_LDA(At, 1, 0); PG8_STAGE(PG8_SA(0, 1), a2 + hstepA, voffA);
;             PG8_WAIT_V(8); PG8_WAIT_L(0); PG8_BAR; PG8_MMA(0, 0, At, B0); PG8_MMA(0, 1, At, B1); PG8_BAR; PG8_SCHED;
;             PG8_LDA(At, 1, 1); PG8_STAGE(PG8_SB(1, 0), b3, voffB); PG8_STAGE(PG8_SB(1, 1), b3 + hstepB, voffB); PG8_STAGE(PG8_SA(1, 0), a3, voffA);
;             PG8_WAIT_V(8); PG8_WAIT_L(0); PG8_BAR; PG8_MMA(1, 0, At, B0); PG8_MMA(1, 1, At, B1); PG8_BAR; PG8_SCHED;
;         }
;         asm volatile("s_nop 15\n\ts_nop 15" ::: "memory");
;         if (wr == 0) PG8_BAR;
	ds_read_b128 v[2:5], v187
	ds_read_b128 v[6:9], v188
	ds_read_b128 v[10:13], v195
	ds_read_b128 v[14:17], v196
	ds_read_b128 v[18:21], v189
	ds_read_b128 v[22:25], v190
	ds_read_b128 v[26:29], v197
	ds_read_b128 v[30:33], v198
	s_add_u32 s18, s60, 0x40000
	s_addc_u32 s19, s61, 0
	s_mov_b32 m0, s63
	v_lshl_add_u64 v[234:235], s[18:19], 0, v[164:165]
	ds_read_b128 v[202:205], v200 offset:32768
	ds_read_b128 v[210:213], v200 offset:34816
	ds_read_b128 v[206:209], v201 offset:32768
	ds_read_b128 v[214:217], v201 offset:34816
	ds_read_b128 v[218:221], v200 offset:36864
	ds_read_b128 v[226:229], v200 offset:38912
	ds_read_b128 v[222:225], v201 offset:36864
	ds_read_b128 v[230:233], v201 offset:38912
	global_load_lds_dwordx4 v[234:235], off
	v_lshl_add_u64 v[234:235], s[18:19], 0, v[162:163]
	s_mov_b32 m0, s64
	s_nop 0
	global_load_lds_dwordx4 v[234:235], off
	s_waitcnt vmcnt(8)
	s_waitcnt lgkmcnt(0)
	s_barrier
	s_setprio 1
	s_waitcnt lgkmcnt(0)
	v_mfma_f32_16x16x128_f8f6f4 v[158:161], v[2:9], v[202:209], v[158:161]
	v_mfma_f32_16x16x128_f8f6f4 v[154:157], v[10:17], v[202:209], v[154:157]
	v_mfma_f32_16x16x128_f8f6f4 v[150:153], v[2:9], v[210:217], v[150:153]
	v_mfma_f32_16x16x128_f8f6f4 v[146:149], v[10:17], v[210:217], v[146:149]
	v_mfma_f32_16x16x128_f8f6f4 v[126:129], v[2:9], v[218:225], v[126:129]
	v_mfma_f32_16x16x128_f8f6f4 v[122:125], v[10:17], v[218:225], v[122:125]
	v_mfma_f32_16x16x128_f8f6f4 v[118:121], v[2:9], v[226:233], v[118:121]
	v_mfma_f32_16x16x128_f8f6f4 v[114:117], v[10:17], v[226:233], v[114:117]
	s_setprio 0
	s_setprio 1
	v_mfma_f32_16x16x128_f8f6f4 v[142:145], v[18:25], v[202:209], v[142:145]
	v_mfma_f32_16x16x128_f8f6f4 v[138:141], v[26:33], v[202:209], v[138:141]
	v_mfma_f32_16x16x128_f8f6f4 v[134:137], v[18:25], v[210:217], v[134:137]
	v_mfma_f32_16x16x128_f8f6f4 v[130:133], v[26:33], v[210:217], v[130:133]
	v_mfma_f32_16x16x128_f8f6f4 v[110:113], v[18:25], v[218:225], v[110:113]
	v_mfma_f32_16x16x128_f8f6f4 v[106:109], v[26:33], v[218:225], v[106:109]
	v_mfma_f32_16x16x128_f8f6f4 v[102:105], v[18:25], v[226:233], v[102:105]
	v_mfma_f32_16x16x128_f8f6f4 v[98:101], v[26:33], v[226:233], v[98:101]
	s_setprio 0
	s_barrier
	s_mov_b32 m0, s66
	v_lshl_add_u64 v[174:175], v[174:175], 0, s[10:11]
	s_add_u32 s18, s58, 0x40080
	ds_read_b128 v[202:205], v200 offset:49152
	ds_read_b128 v[210:213], v200 offset:51200
	ds_read_b128 v[206:209], v201 offset:49152
	ds_read_b128 v[214:217], v201 offset:51200
	ds_read_b128 v[218:221], v200 offset:53248
	ds_read_b128 v[226:229], v200 offset:55296
	ds_read_b128 v[222:225], v201 offset:53248
	ds_read_b128 v[230:233], v201 offset:55296
	global_load_lds_dwordx4 v[174:175], off
	v_lshl_add_u64 v[174:175], v[176:177], 0, s[10:11]
	s_mov_b32 m0, s67
	s_addc_u32 s19, s59, 0
	global_load_lds_dwordx4 v[174:175], off
	v_lshl_add_u64 v[174:175], s[18:19], 0, v[164:165]
	s_mov_b32 m0, s75
	s_nop 0
	global_load_lds_dwordx4 v[174:175], off
	v_lshl_add_u64 v[174:175], s[18:19], 0, v[162:163]
	s_mov_b32 m0, s78
	s_nop 0
	global_load_lds_dwordx4 v[174:175], off
	v_lshl_add_u64 v[174:175], v[178:179], 0, s[10:11]
	s_mov_b32 m0, s73
	s_nop 0
	global_load_lds_dwordx4 v[174:175], off
	v_lshl_add_u64 v[174:175], v[180:181], 0, s[10:11]
	s_mov_b32 m0, s74
	s_nop 0
	global_load_lds_dwordx4 v[174:175], off
	s_waitcnt vmcnt(8)
	s_waitcnt lgkmcnt(0)
	s_barrier
	s_setprio 1
	s_waitcnt lgkmcnt(0)
	v_mfma_f32_16x16x128_f8f6f4 v[94:97], v[2:9], v[202:209], v[94:97]
	v_mfma_f32_16x16x128_f8f6f4 v[90:93], v[10:17], v[202:209], v[90:93]
	v_mfma_f32_16x16x128_f8f6f4 v[86:89], v[2:9], v[210:217], v[86:89]
	v_mfma_f32_16x16x128_f8f6f4 v[78:81], v[10:17], v[210:217], v[78:81]
	v_mfma_f32_16x16x128_f8f6f4 v[70:73], v[2:9], v[218:225], v[70:73]
	v_mfma_f32_16x16x128_f8f6f4 v[62:65], v[10:17], v[218:225], v[62:65]
	v_mfma_f32_16x16x128_f8f6f4 v[54:57], v[2:9], v[226:233], v[54:57]
	v_mfma_f32_16x16x128_f8f6f4 v[46:49], v[10:17], v[226:233], v[46:49]
	s_setprio 0
	s_setprio 1
	v_mfma_f32_16x16x128_f8f6f4 v[82:85], v[18:25], v[202:209], v[82:85]
	v_mfma_f32_16x16x128_f8f6f4 v[74:77], v[26:33], v[202:209], v[74:77]
	v_mfma_f32_16x16x128_f8f6f4 v[66:69], v[18:25], v[210:217], v[66:69]
	v_mfma_f32_16x16x128_f8f6f4 v[58:61], v[26:33], v[210:217], v[58:61]
	s_add_i32 s83, s83, 2
	s_add_u32 s81, s81, 0x100
	s_addc_u32 s82, s82, 0
	s_cmp_gt_u32 s83, 13
	s_mov_b64 s[54:55], s[56:57]
	v_mfma_f32_16x16x128_f8f6f4 v[50:53], v[18:25], v[218:225], v[50:53]
	v_mfma_f32_16x16x128_f8f6f4 v[42:45], v[26:33], v[218:225], v[42:45]
	v_mfma_f32_16x16x128_f8f6f4 v[38:41], v[18:25], v[226:233], v[38:41]
	v_mfma_f32_16x16x128_f8f6f4 v[34:37], v[26:33], v[226:233], v[34:37]
	s_setprio 0
	s_barrier
	s_cbranch_scc0 .LBB0_1121
	s_nop 15
	s_nop 15
	s_and_b64 vcc, exec, s[12:13]
	s_cbranch_vccz .LBB0_1124
	s_barrier

; #define PG8_STAGE(bufoff, gbase, voff) do { _Pragma("unroll") for (int _i = 0; _i < 2; ++_i) \
;         __builtin_amdgcn_global_load_lds((const unsigned*)((const char*)(gbase) + (voff)[_i]), (LAS unsigned*)(lds + (bufoff) + ldsw + _i * 8192), 16, 0, 0); } while (0)
; #define PG8_LDA(dst, b, h) do { _Pragma("unroll") for (int m = 0; m < 4; ++m) _Pragma("unroll") for (int k = 0; k < 2; ++k) dst[m][k] = *(const LAS bf16x8*)(lds + PG8_SA(b, h) + aoff + m * 2048 + k * 1024); } while (0)
; #define PG8_LDB(dst, b, h) do { _Pragma("unroll") for (int n = 0; n < 2; ++n) _Pragma("unroll") for (int k = 0; k < 2; ++k) dst[n][k] = *(const LAS bf16x8*)(lds + PG8_SB(b, h) + boff + n * 2048 + k * 1024); } while (0)
; #define PG8_MMA(ai, bj, At, Bt) do { __builtin_amdgcn_s_setprio(1); _Pragma("unroll") for (int m = 0; m < 4; ++m) _Pragma("unroll") for (int n = 0; n < 2; ++n) _Pragma("unroll") for (int k = 0; k < 2; ++k) \
;         acc[ai][bj][m][n] = __builtin_amdgcn_mfma_f32_16x16x32_bf16(Bt[n][k], At[m][k], acc[ai][bj][m][n], 0, 0, 0); __builtin_amdgcn_s_setprio(0); } while (0)
; #define PG8_WAIT_V(n) asm volatile("s_waitcnt vmcnt(" #n ")" ::: "memory")
; #define PG8_WAIT_L(n) asm volatile("s_waitcnt lgkmcnt(" #n ")" ::: "memory")
; #define PG8_BAR __builtin_amdgcn_s_barrier()
; #define PG8_SCHED __builtin_amdgcn_sched_barrier(0)
; #define PG8_LDA(dst, b, h) do { _Pragma("unroll") for (int m = 0; m < 4; ++m) PG8_LD1(dst[m], PG8_SA(b, h) + aoff0 + m * 2048, PG8_SA(b, h) + aoff1 + m * 2048); } while (0)
;     ...
;             const bool last = (t == nt - 2);
;             const char* a1 = cA + (size_t)(t + 1) * kstep;
;             const char* a2 = last ? nA : cA + (size_t)(t + 2) * kstep; const char* b2 = last ? nB : cB + (size_t)(t + 2) * kstep;
;             const char* a3 = a2 + kstep; const char* b3 = b2 + kstep;
;             if (last && has_next) S.a_ready(nxt);
;             PG8_LDB(B0, 0, 0); PG8_LDB(B1, 0, 1); PG8_SCHED; PG8_LDA(At, 0, 0); PG8_STAGE(PG8_SA(1, 1), a1 + hstepA, voffA);
;             PG8_WAIT_V(8); PG8_WAIT_L(0); PG8_BAR; PG8_MMA(0, 0, At, B0); PG8_MMA(0, 1, At, B1); PG8_BAR; PG8_SCHED;
;             PG8_LDA(At, 0, 1); PG8_STAGE(PG8_SB(0, 0), b2, voffB); PG8_STAGE(PG8_SB(0, 1), b2 + hstepB, voffB); PG8_STAGE(PG8_SA(0, 0), a2, voffA);
;             PG8_WAIT_V(8); PG8_WAIT_L(0); PG8_BAR; PG8_MMA(1, 0, At, B0); PG8_MMA(1, 1, At, B1); PG8_BAR; PG8_SCHED;
.LBB0_1409:
	ds_read_b128 v[14:17], v176
	ds_read_b64 v[18:19], v177
	ds_read_b128 v[20:23], v190
	ds_read_b64 v[24:25], v191
	ds_read_b128 v[2:5], v178
	ds_read_b64 v[6:7], v179
	ds_read_b128 v[8:11], v192
	ds_read_b64 v[12:13], v193
	s_add_u32 s46, s44, 0x100
	s_addc_u32 s47, s45, 0
	s_cmp_eq_u32 s80, 12
	s_cselect_b32 s51, s21, s47
	s_cselect_b32 s50, s73, s46
	s_cselect_b32 s49, s74, s79
	s_cselect_b32 s48, s75, s78
	ds_read_b64 v[212:213], v200
	ds_read_b64 v[172:173], v200 offset:2048
	ds_read_b64 v[218:219], v200 offset:4096
	ds_read_b64 v[206:207], v200 offset:6144
	v_lshl_add_u64 v[174:175], s[44:45], 0, v[164:165]
	s_add_i32 m0, s35, 0xc000
	ds_read_b128 v[208:211], v199
	ds_read_b128 v[168:171], v199 offset:2048
	ds_read_b128 v[214:217], v199 offset:4096
	ds_read_b128 v[202:205], v199 offset:6144
	global_load_lds_dwordx4 v[174:175], off
	v_lshl_add_u64 v[174:175], s[44:45], 0, v[166:167]
	s_add_i32 m0, s35, 0xe000
	s_nop 0
	global_load_lds_dwordx4 v[174:175], off
	s_waitcnt vmcnt(8)
	s_waitcnt lgkmcnt(0)
	s_barrier
	s_setprio 1
	s_waitcnt lgkmcnt(0)
	v_mfma_f32_16x16x128_f8f6f4 v[150:153], v[14:19], v[208:213], v[150:153] cbsz:2 blgp:2
	v_mfma_f32_16x16x128_f8f6f4 v[142:145], v[20:25], v[208:213], v[142:145] cbsz:2 blgp:2
	v_mfma_f32_16x16x128_f8f6f4 v[134:137], v[14:19], v[168:173], v[134:137] cbsz:2 blgp:2
	v_mfma_f32_16x16x128_f8f6f4 v[126:129], v[20:25], v[168:173], v[126:129] cbsz:2 blgp:2
	v_mfma_f32_16x16x128_f8f6f4 v[118:121], v[14:19], v[214:219], v[118:121] cbsz:2 blgp:2
	v_mfma_f32_16x16x128_f8f6f4 v[110:113], v[20:25], v[214:219], v[110:113] cbsz:2 blgp:2
	v_mfma_f32_16x16x128_f8f6f4 v[102:105], v[14:19], v[202:207], v[102:105] cbsz:2 blgp:2
	v_mfma_f32_16x16x128_f8f6f4 v[94:97], v[20:25], v[202:207], v[94:97] cbsz:2 blgp:2
	s_setprio 0
	s_setprio 1
	v_mfma_f32_16x16x128_f8f6f4 v[146:149], v[2:7], v[208:213], v[146:149] cbsz:2 blgp:2
	v_mfma_f32_16x16x128_f8f6f4 v[138:141], v[8:13], v[208:213], v[138:141] cbsz:2 blgp:2
	v_mfma_f32_16x16x128_f8f6f4 v[130:133], v[2:7], v[168:173], v[130:133] cbsz:2 blgp:2
	v_mfma_f32_16x16x128_f8f6f4 v[122:125], v[8:13], v[168:173], v[122:125] cbsz:2 blgp:2
	v_mfma_f32_16x16x128_f8f6f4 v[114:117], v[2:7], v[214:219], v[114:117] cbsz:2 blgp:2
	v_mfma_f32_16x16x128_f8f6f4 v[106:109], v[8:13], v[214:219], v[106:109] cbsz:2 blgp:2
	v_mfma_f32_16x16x128_f8f6f4 v[98:101], v[2:7], v[202:207], v[98:101] cbsz:2 blgp:2
	v_mfma_f32_16x16x128_f8f6f4 v[86:89], v[8:13], v[202:207], v[86:89] cbsz:2 blgp:2
	s_setprio 0
	s_barrier
	ds_read_b64 v[218:219], v200 offset:16384
	ds_read_b64 v[206:207], v200 offset:18432
	ds_read_b64 v[224:225], v200 offset:20480
	ds_read_b64 v[212:213], v200 offset:22528
	s_mov_b32 m0, s43
	v_lshl_add_u64 v[168:169], s[48:49], 0, v[160:161]
	s_add_u32 s44, s48, 0x40000
	ds_read_b128 v[214:217], v199 offset:16384
	ds_read_b128 v[202:205], v199 offset:18432
	ds_read_b128 v[220:223], v199 offset:20480
	ds_read_b128 v[208:211], v199 offset:22528
	global_load_lds_dwordx4 v[168:169], off
	v_lshl_add_u64 v[170:171], s[48:49], 0, v[156:157]
	s_mov_b32 m0, s52
	s_addc_u32 s45, s49, 0
	global_load_lds_dwordx4 v[170:171], off
	v_lshl_add_u64 v[172:173], s[44:45], 0, v[160:161]
	s_mov_b32 m0, s53
	v_lshl_add_u64 v[174:175], s[50:51], 0, v[158:159]
	global_load_lds_dwordx4 v[172:173], off
	v_lshl_add_u64 v[172:173], s[44:45], 0, v[156:157]
	s_mov_b32 m0, s54
	s_nop 0
	global_load_lds_dwordx4 v[172:173], off
	v_lshl_add_u64 v[172:173], s[50:51], 0, v[162:163]
	s_mov_b32 m0, s35
	s_nop 0
	global_load_lds_dwordx4 v[172:173], off
	s_mov_b32 m0, s55
	s_nop 0
	global_load_lds_dwordx4 v[174:175], off
	s_waitcnt vmcnt(8)
	s_waitcnt lgkmcnt(0)
	s_barrier
	s_setprio 1
	s_waitcnt lgkmcnt(0)
	v_mfma_f32_16x16x128_f8f6f4 v[78:81], v[14:19], v[214:219], v[78:81] cbsz:2 blgp:2
	v_mfma_f32_16x16x128_f8f6f4 v[70:73], v[20:25], v[214:219], v[70:73] cbsz:2 blgp:2
	v_mfma_f32_16x16x128_f8f6f4 v[58:61], v[14:19], v[202:207], v[58:61] cbsz:2 blgp:2
	v_mfma_f32_16x16x128_f8f6f4 v[50:53], v[20:25], v[202:207], v[50:53] cbsz:2 blgp:2
	v_mfma_f32_16x16x128_f8f6f4 v[42:45], v[14:19], v[220:225], v[42:45] cbsz:2 blgp:2
	v_mfma_f32_16x16x128_f8f6f4 v[34:37], v[20:25], v[220:225], v[34:37] cbsz:2 blgp:2
	v_mfma_f32_16x16x128_f8f6f4 v[30:33], v[14:19], v[208:213], v[30:33] cbsz:2 blgp:2
	v_mfma_f32_16x16x128_f8f6f4 v[26:29], v[20:25], v[208:213], v[26:29] cbsz:2 blgp:2
	s_setprio 0
	s_setprio 1
	v_mfma_f32_16x16x128_f8f6f4 v[90:93], v[2:7], v[214:219], v[90:93] cbsz:2 blgp:2
	v_mfma_f32_16x16x128_f8f6f4 v[82:85], v[8:13], v[214:219], v[82:85] cbsz:2 blgp:2
	v_mfma_f32_16x16x128_f8f6f4 v[74:77], v[2:7], v[202:207], v[74:77] cbsz:2 blgp:2
	v_mfma_f32_16x16x128_f8f6f4 v[66:69], v[8:13], v[202:207], v[66:69] cbsz:2 blgp:2
	v_mfma_f32_16x16x128_f8f6f4 v[62:65], v[2:7], v[220:225], v[62:65] cbsz:2 blgp:2
	v_mfma_f32_16x16x128_f8f6f4 v[54:57], v[8:13], v[220:225], v[54:57] cbsz:2 blgp:2
	v_mfma_f32_16x16x128_f8f6f4 v[46:49], v[2:7], v[208:213], v[46:49] cbsz:2 blgp:2
	v_mfma_f32_16x16x128_f8f6f4 v[38:41], v[8:13], v[208:213], v[38:41] cbsz:2 blgp:2
	s_setprio 0
	s_barrier
; #define PG8_STAGE(bufoff, gbase, voff) do { _Pragma("unroll") for (int _i = 0; _i < 2; ++_i) \
;         __builtin_amdgcn_global_load_lds((const unsigned*)((const char*)(gbase) + (voff)[_i]), (LAS unsigned*)(lds + (bufoff) + ldsw + _i * 8192), 16, 0, 0); } while (0)
; #define PG8_LDA(dst, b, h) do { _Pragma("unroll") for (int m = 0; m < 4; ++m) _Pragma("unroll") for (int k = 0; k < 2; ++k) dst[m][k] = *(const LAS bf16x8*)(lds + PG8_SA(b, h) + aoff + m * 2048 + k * 1024); } while (0)
; #define PG8_LDB(dst, b, h) do { _Pragma("unroll") for (int n = 0; n < 2; ++n) _Pragma("unroll") for (int k = 0; k < 2; ++k) dst[n][k] = *(const LAS bf16x8*)(lds + PG8_SB(b, h) + boff + n * 2048 + k * 1024); } while (0)
; #define PG8_MMA(ai, bj, At, Bt) do { __builtin_amdgcn_s_setprio(1); _Pragma("unroll") for (int m = 0; m < 4; ++m) _Pragma("unroll") for (int n = 0; n < 2; ++n) _Pragma("unroll") for (int k = 0; k < 2; ++k) \
;         acc[ai][bj][m][n] = __builtin_amdgcn_mfma_f32_16x16x32_bf16(Bt[n][k], At[m][k], acc[ai][bj][m][n], 0, 0, 0); __builtin_amdgcn_s_setprio(0); } while (0)
; #define PG8_WAIT_V(n) asm volatile("s_waitcnt vmcnt(" #n ")" ::: "memory")
; #define PG8_WAIT_L(n) asm volatile("s_waitcnt lgkmcnt(" #n ")" ::: "memory")
; #define PG8_BAR __builtin_amdgcn_s_barrier()
; #define PG8_SCHED __builtin_amdgcn_sched_barrier(0)
; #define PG8_STAGE(bufoff, gbase, voff) do { _Pragma("unroll") for (int _i = 0; _i < 2; ++_i) \
;         __builtin_amdgcn_global_load_lds((const unsigned*)((const char*)(gbase) + (voff)[_i]), (LAS unsigned*)(lds + (bufoff) + ldsw + _i * 8192), 16, 0, 0); } while (0)
; #define PG8_WAIT_V(n) asm volatile("s_waitcnt vmcnt(" #n ")" ::: "memory")
; #define PG8_WAIT_L(n) asm volatile("s_waitcnt lgkmcnt(" #n ")" ::: "memory")
;     ...
;             PG8_LDB(B0, 1, 0); PG8_LDB(B1, 1, 1); PG8_SCHED; PG8_LDA(At, 1, 0); PG8_STAGE(PG8_SA(0, 1), a2 + hstepA, voffA);
;             PG8_WAIT_V(8); PG8_WAIT_L(0); PG8_BAR; PG8_MMA(0, 0, At, B0); PG8_MMA(0, 1, At, B1); PG8_BAR; PG8_SCHED;
;             PG8_LDA(At, 1, 1); PG8_STAGE(PG8_SB(1, 0), b3, voffB); PG8_STAGE(PG8_SB(1, 1), b3 + hstepB, voffB); PG8_STAGE(PG8_SA(1, 0), a3, voffA);
;             PG8_WAIT_V(8); PG8_WAIT_L(0); PG8_BAR; PG8_MMA(1, 0, At, B0); PG8_MMA(1, 1, At, B1); PG8_BAR; PG8_SCHED;
;         }
;         asm volatile("s_nop 15\n\ts_nop 15" ::: "memory");
;         if (wr == 0) PG8_BAR;
	ds_read_b128 v[2:5], v180
	ds_read_b64 v[6:7], v181
	ds_read_b128 v[8:11], v194
	ds_read_b64 v[12:13], v195
	ds_read_b128 v[14:17], v182
	ds_read_b64 v[18:19], v183
	ds_read_b128 v[20:23], v196
	ds_read_b64 v[24:25], v197
	ds_read_b64 v[218:219], v200 offset:32768
	ds_read_b64 v[206:207], v200 offset:34816
	ds_read_b64 v[224:225], v200 offset:36864
	ds_read_b64 v[212:213], v200 offset:38912
	s_add_u32 s44, s50, 0x40000
	s_addc_u32 s45, s51, 0
	s_mov_b32 m0, s56
	v_lshl_add_u64 v[226:227], s[44:45], 0, v[162:163]
	ds_read_b128 v[214:217], v199 offset:32768
	ds_read_b128 v[202:205], v199 offset:34816
	ds_read_b128 v[220:223], v199 offset:36864
	ds_read_b128 v[208:211], v199 offset:38912
	global_load_lds_dwordx4 v[226:227], off
	v_lshl_add_u64 v[226:227], s[44:45], 0, v[158:159]
	s_mov_b32 m0, s57
	s_nop 0
	global_load_lds_dwordx4 v[226:227], off
	s_waitcnt vmcnt(8)
	s_waitcnt lgkmcnt(0)
	s_barrier
	s_setprio 1
	s_waitcnt lgkmcnt(0)
	v_mfma_f32_16x16x128_f8f6f4 v[150:153], v[2:7], v[214:219], v[150:153] cbsz:2 blgp:2
	v_mfma_f32_16x16x128_f8f6f4 v[142:145], v[8:13], v[214:219], v[142:145] cbsz:2 blgp:2
	v_mfma_f32_16x16x128_f8f6f4 v[134:137], v[2:7], v[202:207], v[134:137] cbsz:2 blgp:2
	v_mfma_f32_16x16x128_f8f6f4 v[126:129], v[8:13], v[202:207], v[126:129] cbsz:2 blgp:2
	v_mfma_f32_16x16x128_f8f6f4 v[118:121], v[2:7], v[220:225], v[118:121] cbsz:2 blgp:2
	v_mfma_f32_16x16x128_f8f6f4 v[110:113], v[8:13], v[220:225], v[110:113] cbsz:2 blgp:2
	v_mfma_f32_16x16x128_f8f6f4 v[102:105], v[2:7], v[208:213], v[102:105] cbsz:2 blgp:2
	v_mfma_f32_16x16x128_f8f6f4 v[94:97], v[8:13], v[208:213], v[94:97] cbsz:2 blgp:2
	s_setprio 0
	s_setprio 1
	v_mfma_f32_16x16x128_f8f6f4 v[146:149], v[14:19], v[214:219], v[146:149] cbsz:2 blgp:2
	v_mfma_f32_16x16x128_f8f6f4 v[138:141], v[20:25], v[214:219], v[138:141] cbsz:2 blgp:2
	v_mfma_f32_16x16x128_f8f6f4 v[130:133], v[14:19], v[202:207], v[130:133] cbsz:2 blgp:2
	v_mfma_f32_16x16x128_f8f6f4 v[122:125], v[20:25], v[202:207], v[122:125] cbsz:2 blgp:2
	v_mfma_f32_16x16x128_f8f6f4 v[114:117], v[14:19], v[220:225], v[114:117] cbsz:2 blgp:2
	v_mfma_f32_16x16x128_f8f6f4 v[106:109], v[20:25], v[220:225], v[106:109] cbsz:2 blgp:2
	v_mfma_f32_16x16x128_f8f6f4 v[98:101], v[14:19], v[208:213], v[98:101] cbsz:2 blgp:2
	v_mfma_f32_16x16x128_f8f6f4 v[86:89], v[20:25], v[208:213], v[86:89] cbsz:2 blgp:2
	s_setprio 0
	s_barrier
	ds_read_b64 v[218:219], v200 offset:49152
	ds_read_b64 v[206:207], v200 offset:51200
	ds_read_b64 v[224:225], v200 offset:53248
	ds_read_b64 v[212:213], v200 offset:55296
	s_mov_b32 m0, s58
	v_lshl_add_u64 v[168:169], v[168:169], 0, s[16:17]
	s_add_u32 s44, s48, 0x40080
	ds_read_b128 v[214:217], v199 offset:49152
	ds_read_b128 v[202:205], v199 offset:51200
	ds_read_b128 v[220:223], v199 offset:53248
	ds_read_b128 v[208:211], v199 offset:55296
	global_load_lds_dwordx4 v[168:169], off
	v_lshl_add_u64 v[168:169], v[170:171], 0, s[16:17]
	s_mov_b32 m0, s59
	s_addc_u32 s45, s49, 0
	global_load_lds_dwordx4 v[168:169], off
	v_lshl_add_u64 v[168:169], s[44:45], 0, v[160:161]
	s_mov_b32 m0, s62
	s_nop 0
	global_load_lds_dwordx4 v[168:169], off
	v_lshl_add_u64 v[168:169], s[44:45], 0, v[156:157]
	s_mov_b32 m0, s63
	s_nop 0
	global_load_lds_dwordx4 v[168:169], off
	v_lshl_add_u64 v[168:169], v[172:173], 0, s[16:17]
	s_mov_b32 m0, s60
	s_nop 0
	global_load_lds_dwordx4 v[168:169], off
	v_lshl_add_u64 v[168:169], v[174:175], 0, s[16:17]
	s_mov_b32 m0, s61
	s_nop 0
	global_load_lds_dwordx4 v[168:169], off
	s_waitcnt vmcnt(8)
	s_waitcnt lgkmcnt(0)
	s_barrier
	s_setprio 1
	s_waitcnt lgkmcnt(0)
	v_mfma_f32_16x16x128_f8f6f4 v[78:81], v[2:7], v[214:219], v[78:81] cbsz:2 blgp:2
	v_mfma_f32_16x16x128_f8f6f4 v[70:73], v[8:13], v[214:219], v[70:73] cbsz:2 blgp:2
	v_mfma_f32_16x16x128_f8f6f4 v[58:61], v[2:7], v[202:207], v[58:61] cbsz:2 blgp:2
	v_mfma_f32_16x16x128_f8f6f4 v[50:53], v[8:13], v[202:207], v[50:53] cbsz:2 blgp:2
	v_mfma_f32_16x16x128_f8f6f4 v[42:45], v[2:7], v[220:225], v[42:45] cbsz:2 blgp:2
	v_mfma_f32_16x16x128_f8f6f4 v[34:37], v[8:13], v[220:225], v[34:37] cbsz:2 blgp:2
	v_mfma_f32_16x16x128_f8f6f4 v[30:33], v[2:7], v[208:213], v[30:33] cbsz:2 blgp:2
	v_mfma_f32_16x16x128_f8f6f4 v[26:29], v[8:13], v[208:213], v[26:29] cbsz:2 blgp:2
	s_setprio 0
	s_setprio 1
	v_mfma_f32_16x16x128_f8f6f4 v[90:93], v[14:19], v[214:219], v[90:93] cbsz:2 blgp:2
	v_mfma_f32_16x16x128_f8f6f4 v[82:85], v[20:25], v[214:219], v[82:85] cbsz:2 blgp:2
	v_mfma_f32_16x16x128_f8f6f4 v[74:77], v[14:19], v[202:207], v[74:77] cbsz:2 blgp:2
	v_mfma_f32_16x16x128_f8f6f4 v[66:69], v[20:25], v[202:207], v[66:69] cbsz:2 blgp:2
	s_add_i32 s80, s80, 2
	s_add_u32 s78, s78, 0x100
	s_addc_u32 s79, s79, 0
	s_cmp_gt_u32 s80, 13
	s_mov_b64 s[44:45], s[46:47]
	v_mfma_f32_16x16x128_f8f6f4 v[62:65], v[14:19], v[220:225], v[62:65] cbsz:2 blgp:2
	v_mfma_f32_16x16x128_f8f6f4 v[54:57], v[20:25], v[220:225], v[54:57] cbsz:2 blgp:2
	v_mfma_f32_16x16x128_f8f6f4 v[46:49], v[14:19], v[208:213], v[46:49] cbsz:2 blgp:2
	v_mfma_f32_16x16x128_f8f6f4 v[38:41], v[20:25], v[208:213], v[38:41] cbsz:2 blgp:2
	s_setprio 0
	s_barrier
	s_cbranch_scc0 .LBB0_1409
	s_nop 15
	s_nop 15
	s_and_b64 vcc, exec, s[18:19]
	s_cbranch_vccz .LBB0_1412
	s_barrier

; #define PG8_STAGE(bufoff, gbase, voff) do { _Pragma("unroll") for (int _i = 0; _i < 2; ++_i) \
;         __builtin_amdgcn_global_load_lds((const unsigned*)((const char*)(gbase) + (voff)[_i]), (LAS unsigned*)(lds + (bufoff) + ldsw + _i * 8192), 16, 0, 0); } while (0)
; #define PG8_LDA(dst, b, h) do { _Pragma("unroll") for (int m = 0; m < 4; ++m) _Pragma("unroll") for (int k = 0; k < 2; ++k) dst[m][k] = *(const LAS bf16x8*)(lds + PG8_SA(b, h) + aoff + m * 2048 + k * 1024); } while (0)
; #define PG8_LDB(dst, b, h) do { _Pragma("unroll") for (int n = 0; n < 2; ++n) _Pragma("unroll") for (int k = 0; k < 2; ++k) dst[n][k] = *(const LAS bf16x8*)(lds + PG8_SB(b, h) + boff + n * 2048 + k * 1024); } while (0)
; #define PG8_MMA(ai, bj, At, Bt) do { __builtin_amdgcn_s_setprio(1); _Pragma("unroll") for (int m = 0; m < 4; ++m) _Pragma("unroll") for (int n = 0; n < 2; ++n) _Pragma("unroll") for (int k = 0; k < 2; ++k) \
;         acc[ai][bj][m][n] = __builtin_amdgcn_mfma_f32_16x16x32_bf16(Bt[n][k], At[m][k], acc[ai][bj][m][n], 0, 0, 0); __builtin_amdgcn_s_setprio(0); } while (0)
; #define PG8_WAIT_V(n) asm volatile("s_waitcnt vmcnt(" #n ")" ::: "memory")
; #define PG8_WAIT_L(n) asm volatile("s_waitcnt lgkmcnt(" #n ")" ::: "memory")
; #define PG8_BAR __builtin_amdgcn_s_barrier()
; #define PG8_SCHED __builtin_amdgcn_sched_barrier(0)
; #define PG8_LDA(dst, b, h) do { _Pragma("unroll") for (int m = 0; m < 4; ++m) PG8_LD1(dst[m], PG8_SA(b, h) + aoff0 + m * 2048, PG8_SA(b, h) + aoff1 + m * 2048); } while (0)
;     ...
;             const bool last = (t == nt - 2);
;             const char* a1 = cA + (size_t)(t + 1) * kstep;
;             const char* a2 = last ? nA : cA + (size_t)(t + 2) * kstep; const char* b2 = last ? nB : cB + (size_t)(t + 2) * kstep;
;             const char* a3 = a2 + kstep; const char* b3 = b2 + kstep;
;             if (last && has_next) S.a_ready(nxt);
;             PG8_LDB(B0, 0, 0); PG8_LDB(B1, 0, 1); PG8_SCHED; PG8_LDA(At, 0, 0); PG8_STAGE(PG8_SA(1, 1), a1 + hstepA, voffA);
;             PG8_WAIT_V(8); PG8_WAIT_L(0); PG8_BAR; PG8_MMA(0, 0, At, B0); PG8_MMA(0, 1, At, B1); PG8_BAR; PG8_SCHED;
;             PG8_LDA(At, 0, 1); PG8_STAGE(PG8_SB(0, 0), b2, voffB); PG8_STAGE(PG8_SB(0, 1), b2 + hstepB, voffB); PG8_STAGE(PG8_SA(0, 0), a2, voffA);
;             PG8_WAIT_V(8); PG8_WAIT_L(0); PG8_BAR; PG8_MMA(1, 0, At, B0); PG8_MMA(1, 1, At, B1); PG8_BAR; PG8_SCHED;
.LBB0_1480:
	ds_read_b128 v[18:21], v190
	ds_read_b128 v[22:25], v191
	ds_read_b128 v[26:29], v198
	ds_read_b128 v[30:33], v199
	ds_read_b128 v[2:5], v192
	ds_read_b128 v[6:9], v193
	ds_read_b128 v[10:13], v200
	ds_read_b128 v[14:17], v201
	s_add_u32 s48, s46, 0x100
	s_addc_u32 s49, s47, 0
	s_cmp_eq_u32 s86, 52
	s_cselect_b32 s53, s80, s49
	s_cselect_b32 s52, s81, s48
	s_cselect_b32 s51, s82, s85
	s_cselect_b32 s50, s83, s84
	v_lshl_add_u64 v[234:235], s[46:47], 0, v[170:171]
	s_add_i32 m0, s0, 0xc000
	ds_read_b128 v[176:179], v207
	ds_read_b128 v[210:213], v207 offset:2048
	ds_read_b128 v[180:183], v208
	ds_read_b128 v[214:217], v208 offset:2048
	ds_read_b128 v[218:221], v207 offset:4096
	ds_read_b128 v[226:229], v207 offset:6144
	ds_read_b128 v[222:225], v208 offset:4096
	ds_read_b128 v[230:233], v208 offset:6144
	global_load_lds_dwordx4 v[234:235], off
	v_lshl_add_u64 v[234:235], s[46:47], 0, v[172:173]
	s_add_i32 m0, s0, 0xe000
	s_nop 0
	global_load_lds_dwordx4 v[234:235], off
	s_waitcnt vmcnt(8)
	s_waitcnt lgkmcnt(0)
	s_barrier
	s_setprio 1
	s_waitcnt lgkmcnt(0)
	v_mfma_f32_16x16x128_f8f6f4 v[158:161], v[18:25], v[176:183], v[158:161]
	v_mfma_f32_16x16x128_f8f6f4 v[154:157], v[26:33], v[176:183], v[154:157]
	v_mfma_f32_16x16x128_f8f6f4 v[146:149], v[18:25], v[210:217], v[146:149]
	v_mfma_f32_16x16x128_f8f6f4 v[138:141], v[26:33], v[210:217], v[138:141]
	v_mfma_f32_16x16x128_f8f6f4 v[130:133], v[18:25], v[218:225], v[130:133]
	v_mfma_f32_16x16x128_f8f6f4 v[122:125], v[26:33], v[218:225], v[122:125]
	v_mfma_f32_16x16x128_f8f6f4 v[114:117], v[18:25], v[226:233], v[114:117]
	v_mfma_f32_16x16x128_f8f6f4 v[106:109], v[26:33], v[226:233], v[106:109]
	s_setprio 0
	s_setprio 1
	v_mfma_f32_16x16x128_f8f6f4 v[150:153], v[2:9], v[176:183], v[150:153]
	v_mfma_f32_16x16x128_f8f6f4 v[142:145], v[10:17], v[176:183], v[142:145]
	v_mfma_f32_16x16x128_f8f6f4 v[134:137], v[2:9], v[210:217], v[134:137]
	v_mfma_f32_16x16x128_f8f6f4 v[126:129], v[10:17], v[210:217], v[126:129]
	v_mfma_f32_16x16x128_f8f6f4 v[118:121], v[2:9], v[218:225], v[118:121]
	v_mfma_f32_16x16x128_f8f6f4 v[110:113], v[10:17], v[218:225], v[110:113]
	v_mfma_f32_16x16x128_f8f6f4 v[102:105], v[2:9], v[226:233], v[102:105]
	v_mfma_f32_16x16x128_f8f6f4 v[98:101], v[10:17], v[226:233], v[98:101]
	s_setprio 0
	s_barrier
	s_mov_b32 m0, s1
	v_lshl_add_u64 v[176:177], s[50:51], 0, v[166:167]
	s_add_u32 s46, s50, 0xe0000
	ds_read_b128 v[210:213], v207 offset:16384
	ds_read_b128 v[218:221], v207 offset:18432
	ds_read_b128 v[214:217], v208 offset:16384
	ds_read_b128 v[222:225], v208 offset:18432
	ds_read_b128 v[226:229], v207 offset:20480
	ds_read_b128 v[234:237], v207 offset:22528
	ds_read_b128 v[230:233], v208 offset:20480
	ds_read_b128 v[238:241], v208 offset:22528
	global_load_lds_dwordx4 v[176:177], off
	v_lshl_add_u64 v[178:179], s[50:51], 0, v[162:163]
	s_mov_b32 m0, s33
	s_addc_u32 s47, s51, 0
	global_load_lds_dwordx4 v[178:179], off
	v_lshl_add_u64 v[180:181], s[46:47], 0, v[166:167]
	s_mov_b32 m0, s35
	v_lshl_add_u64 v[182:183], s[52:53], 0, v[164:165]
	global_load_lds_dwordx4 v[180:181], off
	v_lshl_add_u64 v[180:181], s[46:47], 0, v[162:163]
	s_mov_b32 m0, s54
	s_nop 0
	global_load_lds_dwordx4 v[180:181], off
	v_lshl_add_u64 v[180:181], s[52:53], 0, v[168:169]
	s_mov_b32 m0, s0
	s_nop 0
	global_load_lds_dwordx4 v[180:181], off
	s_mov_b32 m0, s55
	s_nop 0
	global_load_lds_dwordx4 v[182:183], off
	s_waitcnt vmcnt(8)
	s_waitcnt lgkmcnt(0)
	s_barrier
	s_setprio 1
	s_waitcnt lgkmcnt(0)
	v_mfma_f32_16x16x128_f8f6f4 v[94:97], v[18:25], v[210:217], v[94:97]
	v_mfma_f32_16x16x128_f8f6f4 v[90:93], v[26:33], v[210:217], v[90:93]
	v_mfma_f32_16x16x128_f8f6f4 v[82:85], v[18:25], v[218:225], v[82:85]
	v_mfma_f32_16x16x128_f8f6f4 v[74:77], v[26:33], v[218:225], v[74:77]
	v_mfma_f32_16x16x128_f8f6f4 v[66:69], v[18:25], v[226:233], v[66:69]
	v_mfma_f32_16x16x128_f8f6f4 v[58:61], v[26:33], v[226:233], v[58:61]
	v_mfma_f32_16x16x128_f8f6f4 v[50:53], v[18:25], v[234:241], v[50:53]
	v_mfma_f32_16x16x128_f8f6f4 v[42:45], v[26:33], v[234:241], v[42:45]
	s_setprio 0
	s_setprio 1
	v_mfma_f32_16x16x128_f8f6f4 v[86:89], v[2:9], v[210:217], v[86:89]
	v_mfma_f32_16x16x128_f8f6f4 v[78:81], v[10:17], v[210:217], v[78:81]
	v_mfma_f32_16x16x128_f8f6f4 v[70:73], v[2:9], v[218:225], v[70:73]
	v_mfma_f32_16x16x128_f8f6f4 v[62:65], v[10:17], v[218:225], v[62:65]
	v_mfma_f32_16x16x128_f8f6f4 v[54:57], v[2:9], v[226:233], v[54:57]
	v_mfma_f32_16x16x128_f8f6f4 v[46:49], v[10:17], v[226:233], v[46:49]
	v_mfma_f32_16x16x128_f8f6f4 v[38:41], v[2:9], v[234:241], v[38:41]
	v_mfma_f32_16x16x128_f8f6f4 v[34:37], v[10:17], v[234:241], v[34:37]
	s_setprio 0
	s_barrier
; #define PG8_STAGE(bufoff, gbase, voff) do { _Pragma("unroll") for (int _i = 0; _i < 2; ++_i) \
;         __builtin_amdgcn_global_load_lds((const unsigned*)((const char*)(gbase) + (voff)[_i]), (LAS unsigned*)(lds + (bufoff) + ldsw + _i * 8192), 16, 0, 0); } while (0)
; #define PG8_LDA(dst, b, h) do { _Pragma("unroll") for (int m = 0; m < 4; ++m) _Pragma("unroll") for (int k = 0; k < 2; ++k) dst[m][k] = *(const LAS bf16x8*)(lds + PG8_SA(b, h) + aoff + m * 2048 + k * 1024); } while (0)
; #define PG8_LDB(dst, b, h) do { _Pragma("unroll") for (int n = 0; n < 2; ++n) _Pragma("unroll") for (int k = 0; k < 2; ++k) dst[n][k] = *(const LAS bf16x8*)(lds + PG8_SB(b, h) + boff + n * 2048 + k * 1024); } while (0)
; #define PG8_MMA(ai, bj, At, Bt) do { __builtin_amdgcn_s_setprio(1); _Pragma("unroll") for (int m = 0; m < 4; ++m) _Pragma("unroll") for (int n = 0; n < 2; ++n) _Pragma("unroll") for (int k = 0; k < 2; ++k) \
;         acc[ai][bj][m][n] = __builtin_amdgcn_mfma_f32_16x16x32_bf16(Bt[n][k], At[m][k], acc[ai][bj][m][n], 0, 0, 0); __builtin_amdgcn_s_setprio(0); } while (0)
; #define PG8_WAIT_V(n) asm volatile("s_waitcnt vmcnt(" #n ")" ::: "memory")
; #define PG8_WAIT_L(n) asm volatile("s_waitcnt lgkmcnt(" #n ")" ::: "memory")
; #define PG8_BAR __builtin_amdgcn_s_barrier()
; #define PG8_SCHED __builtin_amdgcn_sched_barrier(0)
; #define PG8_STAGE(bufoff, gbase, voff) do { _Pragma("unroll") for (int _i = 0; _i < 2; ++_i) \
;         __builtin_amdgcn_global_load_lds((const unsigned*)((const char*)(gbase) + (voff)[_i]), (LAS unsigned*)(lds + (bufoff) + ldsw + _i * 8192), 16, 0, 0); } while (0)
; #define PG8_WAIT_V(n) asm volatile("s_waitcnt vmcnt(" #n ")" ::: "memory")
; #define PG8_WAIT_L(n) asm volatile("s_waitcnt lgkmcnt(" #n ")" ::: "memory")
;     ...
;             PG8_LDB(B0, 1, 0); PG8_LDB(B1, 1, 1); PG8_SCHED; PG8_LDA(At, 1, 0); PG8_STAGE(PG8_SA(0, 1), a2 + hstepA, voffA);
;             PG8_WAIT_V(8); PG8_WAIT_L(0); PG8_BAR; PG8_MMA(0, 0, At, B0); PG8_MMA(0, 1, At, B1); PG8_BAR; PG8_SCHED;
;             PG8_LDA(At, 1, 1); PG8_STAGE(PG8_SB(1, 0), b3, voffB); PG8_STAGE(PG8_SB(1, 1), b3 + hstepB, voffB); PG8_STAGE(PG8_SA(1, 0), a3, voffA);
;             PG8_WAIT_V(8); PG8_WAIT_L(0); PG8_BAR; PG8_MMA(1, 0, At, B0); PG8_MMA(1, 1, At, B1); PG8_BAR; PG8_SCHED;
;         }
;         asm volatile("s_nop 15\n\ts_nop 15" ::: "memory");
;         if (wr == 0) PG8_BAR;
	ds_read_b128 v[2:5], v194
	ds_read_b128 v[6:9], v195
	ds_read_b128 v[10:13], v202
	ds_read_b128 v[14:17], v203
	ds_read_b128 v[18:21], v196
	ds_read_b128 v[22:25], v197
	ds_read_b128 v[26:29], v204
	ds_read_b128 v[30:33], v205
	s_add_u32 s46, s52, 0xe0000
	s_addc_u32 s47, s53, 0
	s_mov_b32 m0, s56
	v_lshl_add_u64 v[242:243], s[46:47], 0, v[168:169]
	ds_read_b128 v[210:213], v207 offset:32768
	ds_read_b128 v[218:221], v207 offset:34816
	ds_read_b128 v[214:217], v208 offset:32768
	ds_read_b128 v[222:225], v208 offset:34816
	ds_read_b128 v[226:229], v207 offset:36864
	ds_read_b128 v[234:237], v207 offset:38912
	ds_read_b128 v[230:233], v208 offset:36864
	ds_read_b128 v[238:241], v208 offset:38912
	global_load_lds_dwordx4 v[242:243], off
	v_lshl_add_u64 v[242:243], s[46:47], 0, v[164:165]
	s_mov_b32 m0, s57
	s_nop 0
	global_load_lds_dwordx4 v[242:243], off
	s_waitcnt vmcnt(8)
	s_waitcnt lgkmcnt(0)
	s_barrier
	s_setprio 1
	s_waitcnt lgkmcnt(0)
	v_mfma_f32_16x16x128_f8f6f4 v[158:161], v[2:9], v[210:217], v[158:161]
	v_mfma_f32_16x16x128_f8f6f4 v[154:157], v[10:17], v[210:217], v[154:157]
	v_mfma_f32_16x16x128_f8f6f4 v[146:149], v[2:9], v[218:225], v[146:149]
	v_mfma_f32_16x16x128_f8f6f4 v[138:141], v[10:17], v[218:225], v[138:141]
	v_mfma_f32_16x16x128_f8f6f4 v[130:133], v[2:9], v[226:233], v[130:133]
	v_mfma_f32_16x16x128_f8f6f4 v[122:125], v[10:17], v[226:233], v[122:125]
	v_mfma_f32_16x16x128_f8f6f4 v[114:117], v[2:9], v[234:241], v[114:117]
	v_mfma_f32_16x16x128_f8f6f4 v[106:109], v[10:17], v[234:241], v[106:109]
	s_setprio 0
	s_setprio 1
	v_mfma_f32_16x16x128_f8f6f4 v[150:153], v[18:25], v[210:217], v[150:153]
	v_mfma_f32_16x16x128_f8f6f4 v[142:145], v[26:33], v[210:217], v[142:145]
	v_mfma_f32_16x16x128_f8f6f4 v[134:137], v[18:25], v[218:225], v[134:137]
	v_mfma_f32_16x16x128_f8f6f4 v[126:129], v[26:33], v[218:225], v[126:129]
	v_mfma_f32_16x16x128_f8f6f4 v[118:121], v[18:25], v[226:233], v[118:121]
	v_mfma_f32_16x16x128_f8f6f4 v[110:113], v[26:33], v[226:233], v[110:113]
	v_mfma_f32_16x16x128_f8f6f4 v[102:105], v[18:25], v[234:241], v[102:105]
	v_mfma_f32_16x16x128_f8f6f4 v[98:101], v[26:33], v[234:241], v[98:101]
	s_setprio 0
	s_barrier
	s_mov_b32 m0, s58
	v_lshl_add_u64 v[176:177], v[176:177], 0, s[14:15]
	s_add_u32 s46, s50, 0xe0080
	ds_read_b128 v[210:213], v207 offset:49152
	ds_read_b128 v[218:221], v207 offset:51200
	ds_read_b128 v[214:217], v208 offset:49152
	ds_read_b128 v[222:225], v208 offset:51200
	ds_read_b128 v[226:229], v207 offset:53248
	ds_read_b128 v[234:237], v207 offset:55296
	ds_read_b128 v[230:233], v208 offset:53248
	ds_read_b128 v[238:241], v208 offset:55296
	global_load_lds_dwordx4 v[176:177], off
	v_lshl_add_u64 v[176:177], v[178:179], 0, s[14:15]
	s_mov_b32 m0, s59
	s_addc_u32 s47, s51, 0
	global_load_lds_dwordx4 v[176:177], off
	v_lshl_add_u64 v[176:177], s[46:47], 0, v[166:167]
	s_mov_b32 m0, s62
	s_nop 0
	global_load_lds_dwordx4 v[176:177], off
	v_lshl_add_u64 v[176:177], s[46:47], 0, v[162:163]
	s_mov_b32 m0, s63
	s_nop 0
	global_load_lds_dwordx4 v[176:177], off
	v_lshl_add_u64 v[176:177], v[180:181], 0, s[14:15]
	s_mov_b32 m0, s60
	s_nop 0
	global_load_lds_dwordx4 v[176:177], off
	v_lshl_add_u64 v[176:177], v[182:183], 0, s[14:15]
	s_mov_b32 m0, s61
	s_nop 0
	global_load_lds_dwordx4 v[176:177], off
	s_waitcnt vmcnt(8)
	s_waitcnt lgkmcnt(0)
	s_barrier
	s_setprio 1
	s_waitcnt lgkmcnt(0)
	v_mfma_f32_16x16x128_f8f6f4 v[94:97], v[2:9], v[210:217], v[94:97]
	v_mfma_f32_16x16x128_f8f6f4 v[90:93], v[10:17], v[210:217], v[90:93]
	v_mfma_f32_16x16x128_f8f6f4 v[82:85], v[2:9], v[218:225], v[82:85]
	v_mfma_f32_16x16x128_f8f6f4 v[74:77], v[10:17], v[218:225], v[74:77]
	v_mfma_f32_16x16x128_f8f6f4 v[66:69], v[2:9], v[226:233], v[66:69]
	v_mfma_f32_16x16x128_f8f6f4 v[58:61], v[10:17], v[226:233], v[58:61]
	v_mfma_f32_16x16x128_f8f6f4 v[50:53], v[2:9], v[234:241], v[50:53]
	v_mfma_f32_16x16x128_f8f6f4 v[42:45], v[10:17], v[234:241], v[42:45]
	s_setprio 0
	s_setprio 1
	v_mfma_f32_16x16x128_f8f6f4 v[86:89], v[18:25], v[210:217], v[86:89]
	v_mfma_f32_16x16x128_f8f6f4 v[78:81], v[26:33], v[210:217], v[78:81]
	v_mfma_f32_16x16x128_f8f6f4 v[70:73], v[18:25], v[218:225], v[70:73]
	v_mfma_f32_16x16x128_f8f6f4 v[62:65], v[26:33], v[218:225], v[62:65]
	s_add_i32 s86, s86, 2
	s_add_u32 s84, s84, 0x100
	s_addc_u32 s85, s85, 0
	s_cmp_gt_u32 s86, 53
	s_mov_b64 s[46:47], s[48:49]
	v_mfma_f32_16x16x128_f8f6f4 v[54:57], v[18:25], v[226:233], v[54:57]
	v_mfma_f32_16x16x128_f8f6f4 v[46:49], v[26:33], v[226:233], v[46:49]
	v_mfma_f32_16x16x128_f8f6f4 v[38:41], v[18:25], v[234:241], v[38:41]
	v_mfma_f32_16x16x128_f8f6f4 v[34:37], v[26:33], v[234:241], v[34:37]
	s_setprio 0
	s_barrier
	s_cbranch_scc0 .LBB0_1480
	s_nop 15
	s_nop 15
	s_and_b64 vcc, exec, s[16:17]
	s_cbranch_vccz .LBB0_1483
	s_barrier

; #define PG8_STAGE(bufoff, gbase, voff) do { _Pragma("unroll") for (int _i = 0; _i < 2; ++_i) \
;         __builtin_amdgcn_global_load_lds((const unsigned*)((const char*)(gbase) + (voff)[_i]), (LAS unsigned*)(lds + (bufoff) + ldsw + _i * 8192), 16, 0, 0); } while (0)
; #define PG8_LDA(dst, b, h) do { _Pragma("unroll") for (int m = 0; m < 4; ++m) _Pragma("unroll") for (int k = 0; k < 2; ++k) dst[m][k] = *(const LAS bf16x8*)(lds + PG8_SA(b, h) + aoff + m * 2048 + k * 1024); } while (0)
; #define PG8_LDB(dst, b, h) do { _Pragma("unroll") for (int n = 0; n < 2; ++n) _Pragma("unroll") for (int k = 0; k < 2; ++k) dst[n][k] = *(const LAS bf16x8*)(lds + PG8_SB(b, h) + boff + n * 2048 + k * 1024); } while (0)
; #define PG8_MMA(ai, bj, At, Bt) do { __builtin_amdgcn_s_setprio(1); _Pragma("unroll") for (int m = 0; m < 4; ++m) _Pragma("unroll") for (int n = 0; n < 2; ++n) _Pragma("unroll") for (int k = 0; k < 2; ++k) \
;         acc[ai][bj][m][n] = __builtin_amdgcn_mfma_f32_16x16x32_bf16(Bt[n][k], At[m][k], acc[ai][bj][m][n], 0, 0, 0); __builtin_amdgcn_s_setprio(0); } while (0)
; #define PG8_WAIT_V(n) asm volatile("s_waitcnt vmcnt(" #n ")" ::: "memory")
; #define PG8_WAIT_L(n) asm volatile("s_waitcnt lgkmcnt(" #n ")" ::: "memory")
; #define PG8_BAR __builtin_amdgcn_s_barrier()
; #define PG8_SCHED __builtin_amdgcn_sched_barrier(0)
; #define PG8_LDA(dst, b, h) do { _Pragma("unroll") for (int m = 0; m < 4; ++m) PG8_LD1(dst[m], PG8_SA(b, h) + aoff0 + m * 2048, PG8_SA(b, h) + aoff1 + m * 2048); } while (0)
;     ...
;             const bool last = (t == nt - 2);
;             const char* a1 = cA + (size_t)(t + 1) * kstep;
;             const char* a2 = last ? nA : cA + (size_t)(t + 2) * kstep; const char* b2 = last ? nB : cB + (size_t)(t + 2) * kstep;
;             const char* a3 = a2 + kstep; const char* b3 = b2 + kstep;
;             if (last && has_next) S.a_ready(nxt);
;             PG8_LDB(B0, 0, 0); PG8_LDB(B1, 0, 1); PG8_SCHED; PG8_LDA(At, 0, 0); PG8_STAGE(PG8_SA(1, 1), a1 + hstepA, voffA);
;             PG8_WAIT_V(8); PG8_WAIT_L(0); PG8_BAR; PG8_MMA(0, 0, At, B0); PG8_MMA(0, 1, At, B1); PG8_BAR; PG8_SCHED;
;             PG8_LDA(At, 0, 1); PG8_STAGE(PG8_SB(0, 0), b2, voffB); PG8_STAGE(PG8_SB(0, 1), b2 + hstepB, voffB); PG8_STAGE(PG8_SA(0, 0), a2, voffA);
;             PG8_WAIT_V(8); PG8_WAIT_L(0); PG8_BAR; PG8_MMA(1, 0, At, B0); PG8_MMA(1, 1, At, B1); PG8_BAR; PG8_SCHED;
.LBB0_1497:
	ds_read_b128 v[18:21], v190
	ds_read_b128 v[22:25], v191
	ds_read_b128 v[26:29], v198
	ds_read_b128 v[30:33], v199
	ds_read_b128 v[2:5], v192
	ds_read_b128 v[6:9], v193
	ds_read_b128 v[10:13], v200
	ds_read_b128 v[14:17], v201
	s_add_u32 s48, s46, 0x100
	s_addc_u32 s49, s47, 0
	s_cmp_eq_u32 s88, 10
	s_cselect_b32 s53, s82, s49
	s_cselect_b32 s52, s83, s48
	s_cselect_b32 s51, s84, s87
	s_cselect_b32 s50, s85, s86
	v_lshl_add_u64 v[234:235], s[46:47], 0, v[172:173]
	s_add_i32 m0, s25, 0xc000
	ds_read_b128 v[176:179], v207
	ds_read_b128 v[210:213], v207 offset:2048
	ds_read_b128 v[180:183], v208
	ds_read_b128 v[214:217], v208 offset:2048
	ds_read_b128 v[218:221], v207 offset:4096
	ds_read_b128 v[226:229], v207 offset:6144
	ds_read_b128 v[222:225], v208 offset:4096
	ds_read_b128 v[230:233], v208 offset:6144
	global_load_lds_dwordx4 v[234:235], off
	v_lshl_add_u64 v[234:235], s[46:47], 0, v[174:175]
	s_add_i32 m0, s25, 0xe000
	s_nop 0
	global_load_lds_dwordx4 v[234:235], off
	s_waitcnt vmcnt(8)
	s_waitcnt lgkmcnt(0)
	s_barrier
	s_setprio 1
	s_waitcnt lgkmcnt(0)
	v_mfma_f32_16x16x128_f8f6f4 v[158:161], v[18:25], v[176:183], v[158:161]
	v_mfma_f32_16x16x128_f8f6f4 v[154:157], v[26:33], v[176:183], v[154:157]
	v_mfma_f32_16x16x128_f8f6f4 v[146:149], v[18:25], v[210:217], v[146:149]
	v_mfma_f32_16x16x128_f8f6f4 v[138:141], v[26:33], v[210:217], v[138:141]
	v_mfma_f32_16x16x128_f8f6f4 v[130:133], v[18:25], v[218:225], v[130:133]
	v_mfma_f32_16x16x128_f8f6f4 v[122:125], v[26:33], v[218:225], v[122:125]
	v_mfma_f32_16x16x128_f8f6f4 v[114:117], v[18:25], v[226:233], v[114:117]
	v_mfma_f32_16x16x128_f8f6f4 v[106:109], v[26:33], v[226:233], v[106:109]
	s_setprio 0
	s_setprio 1
	v_mfma_f32_16x16x128_f8f6f4 v[150:153], v[2:9], v[176:183], v[150:153]
	v_mfma_f32_16x16x128_f8f6f4 v[142:145], v[10:17], v[176:183], v[142:145]
	v_mfma_f32_16x16x128_f8f6f4 v[134:137], v[2:9], v[210:217], v[134:137]
	v_mfma_f32_16x16x128_f8f6f4 v[126:129], v[10:17], v[210:217], v[126:129]
	v_mfma_f32_16x16x128_f8f6f4 v[118:121], v[2:9], v[218:225], v[118:121]
	v_mfma_f32_16x16x128_f8f6f4 v[110:113], v[10:17], v[218:225], v[110:113]
	v_mfma_f32_16x16x128_f8f6f4 v[102:105], v[2:9], v[226:233], v[102:105]
	v_mfma_f32_16x16x128_f8f6f4 v[98:101], v[10:17], v[226:233], v[98:101]
	s_setprio 0
	s_barrier
	s_mov_b32 m0, s33
	v_lshl_add_u64 v[176:177], s[50:51], 0, v[166:167]
	s_add_u32 s46, s50, 0xe0000
	ds_read_b128 v[210:213], v207 offset:16384
	ds_read_b128 v[218:221], v207 offset:18432
	ds_read_b128 v[214:217], v208 offset:16384
	ds_read_b128 v[222:225], v208 offset:18432
	ds_read_b128 v[226:229], v207 offset:20480
	ds_read_b128 v[234:237], v207 offset:22528
	ds_read_b128 v[230:233], v208 offset:20480
	ds_read_b128 v[238:241], v208 offset:22528
	global_load_lds_dwordx4 v[176:177], off
	v_lshl_add_u64 v[178:179], s[50:51], 0, v[162:163]
	s_mov_b32 m0, s35
	s_addc_u32 s47, s51, 0
	global_load_lds_dwordx4 v[178:179], off
	v_lshl_add_u64 v[180:181], s[46:47], 0, v[166:167]
	s_mov_b32 m0, s54
	v_lshl_add_u64 v[182:183], s[52:53], 0, v[164:165]
	global_load_lds_dwordx4 v[180:181], off
	v_lshl_add_u64 v[180:181], s[46:47], 0, v[162:163]
	s_mov_b32 m0, s55
	s_nop 0
	global_load_lds_dwordx4 v[180:181], off
	v_lshl_add_u64 v[180:181], s[52:53], 0, v[168:169]
	s_mov_b32 m0, s25
	s_nop 0
	global_load_lds_dwordx4 v[180:181], off
	s_mov_b32 m0, s56
	s_nop 0
	global_load_lds_dwordx4 v[182:183], off
	s_waitcnt vmcnt(8)
	s_waitcnt lgkmcnt(0)
	s_barrier
	s_setprio 1
	s_waitcnt lgkmcnt(0)
	v_mfma_f32_16x16x128_f8f6f4 v[94:97], v[18:25], v[210:217], v[94:97]
	v_mfma_f32_16x16x128_f8f6f4 v[90:93], v[26:33], v[210:217], v[90:93]
	v_mfma_f32_16x16x128_f8f6f4 v[82:85], v[18:25], v[218:225], v[82:85]
	v_mfma_f32_16x16x128_f8f6f4 v[74:77], v[26:33], v[218:225], v[74:77]
	v_mfma_f32_16x16x128_f8f6f4 v[66:69], v[18:25], v[226:233], v[66:69]
	v_mfma_f32_16x16x128_f8f6f4 v[58:61], v[26:33], v[226:233], v[58:61]
	v_mfma_f32_16x16x128_f8f6f4 v[50:53], v[18:25], v[234:241], v[50:53]
	v_mfma_f32_16x16x128_f8f6f4 v[42:45], v[26:33], v[234:241], v[42:45]
	s_setprio 0
	s_setprio 1
	v_mfma_f32_16x16x128_f8f6f4 v[86:89], v[2:9], v[210:217], v[86:89]
	v_mfma_f32_16x16x128_f8f6f4 v[78:81], v[10:17], v[210:217], v[78:81]
	v_mfma_f32_16x16x128_f8f6f4 v[70:73], v[2:9], v[218:225], v[70:73]
	v_mfma_f32_16x16x128_f8f6f4 v[62:65], v[10:17], v[218:225], v[62:65]
	v_mfma_f32_16x16x128_f8f6f4 v[54:57], v[2:9], v[226:233], v[54:57]
	v_mfma_f32_16x16x128_f8f6f4 v[46:49], v[10:17], v[226:233], v[46:49]
	v_mfma_f32_16x16x128_f8f6f4 v[38:41], v[2:9], v[234:241], v[38:41]
	v_mfma_f32_16x16x128_f8f6f4 v[34:37], v[10:17], v[234:241], v[34:37]
	s_setprio 0
	s_barrier
; #define PG8_STAGE(bufoff, gbase, voff) do { _Pragma("unroll") for (int _i = 0; _i < 2; ++_i) \
;         __builtin_amdgcn_global_load_lds((const unsigned*)((const char*)(gbase) + (voff)[_i]), (LAS unsigned*)(lds + (bufoff) + ldsw + _i * 8192), 16, 0, 0); } while (0)
; #define PG8_LDA(dst, b, h) do { _Pragma("unroll") for (int m = 0; m < 4; ++m) _Pragma("unroll") for (int k = 0; k < 2; ++k) dst[m][k] = *(const LAS bf16x8*)(lds + PG8_SA(b, h) + aoff + m * 2048 + k * 1024); } while (0)
; #define PG8_LDB(dst, b, h) do { _Pragma("unroll") for (int n = 0; n < 2; ++n) _Pragma("unroll") for (int k = 0; k < 2; ++k) dst[n][k] = *(const LAS bf16x8*)(lds + PG8_SB(b, h) + boff + n * 2048 + k * 1024); } while (0)
; #define PG8_MMA(ai, bj, At, Bt) do { __builtin_amdgcn_s_setprio(1); _Pragma("unroll") for (int m = 0; m < 4; ++m) _Pragma("unroll") for (int n = 0; n < 2; ++n) _Pragma("unroll") for (int k = 0; k < 2; ++k) \
;         acc[ai][bj][m][n] = __builtin_amdgcn_mfma_f32_16x16x32_bf16(Bt[n][k], At[m][k], acc[ai][bj][m][n], 0, 0, 0); __builtin_amdgcn_s_setprio(0); } while (0)
; #define PG8_WAIT_V(n) asm volatile("s_waitcnt vmcnt(" #n ")" ::: "memory")
; #define PG8_WAIT_L(n) asm volatile("s_waitcnt lgkmcnt(" #n ")" ::: "memory")
; #define PG8_BAR __builtin_amdgcn_s_barrier()
; #define PG8_SCHED __builtin_amdgcn_sched_barrier(0)
; #define PG8_STAGE(bufoff, gbase, voff) do { _Pragma("unroll") for (int _i = 0; _i < 2; ++_i) \
;         __builtin_amdgcn_global_load_lds((const unsigned*)((const char*)(gbase) + (voff)[_i]), (LAS unsigned*)(lds + (bufoff) + ldsw + _i * 8192), 16, 0, 0); } while (0)
; #define PG8_WAIT_V(n) asm volatile("s_waitcnt vmcnt(" #n ")" ::: "memory")
; #define PG8_WAIT_L(n) asm volatile("s_waitcnt lgkmcnt(" #n ")" ::: "memory")
;     ...
;             PG8_LDB(B0, 1, 0); PG8_LDB(B1, 1, 1); PG8_SCHED; PG8_LDA(At, 1, 0); PG8_STAGE(PG8_SA(0, 1), a2 + hstepA, voffA);
;             PG8_WAIT_V(8); PG8_WAIT_L(0); PG8_BAR; PG8_MMA(0, 0, At, B0); PG8_MMA(0, 1, At, B1); PG8_BAR; PG8_SCHED;
;             PG8_LDA(At, 1, 1); PG8_STAGE(PG8_SB(1, 0), b3, voffB); PG8_STAGE(PG8_SB(1, 1), b3 + hstepB, voffB); PG8_STAGE(PG8_SA(1, 0), a3, voffA);
;             PG8_WAIT_V(8); PG8_WAIT_L(0); PG8_BAR; PG8_MMA(1, 0, At, B0); PG8_MMA(1, 1, At, B1); PG8_BAR; PG8_SCHED;
;         }
;         asm volatile("s_nop 15\n\ts_nop 15" ::: "memory");
;         if (wr == 0) PG8_BAR;
	ds_read_b128 v[2:5], v194
	ds_read_b128 v[6:9], v195
	ds_read_b128 v[10:13], v202
	ds_read_b128 v[14:17], v203
	ds_read_b128 v[18:21], v196
	ds_read_b128 v[22:25], v197
	ds_read_b128 v[26:29], v204
	ds_read_b128 v[30:33], v205
	s_add_u32 s46, s52, 0xe0000
	s_addc_u32 s47, s53, 0
	s_mov_b32 m0, s57
	v_lshl_add_u64 v[242:243], s[46:47], 0, v[168:169]
	ds_read_b128 v[210:213], v207 offset:32768
	ds_read_b128 v[218:221], v207 offset:34816
	ds_read_b128 v[214:217], v208 offset:32768
	ds_read_b128 v[222:225], v208 offset:34816
	ds_read_b128 v[226:229], v207 offset:36864
	ds_read_b128 v[234:237], v207 offset:38912
	ds_read_b128 v[230:233], v208 offset:36864
	ds_read_b128 v[238:241], v208 offset:38912
	global_load_lds_dwordx4 v[242:243], off
	v_lshl_add_u64 v[242:243], s[46:47], 0, v[164:165]
	s_mov_b32 m0, s58
	s_nop 0
	global_load_lds_dwordx4 v[242:243], off
	s_waitcnt vmcnt(8)
	s_waitcnt lgkmcnt(0)
	s_barrier
	s_setprio 1
	s_waitcnt lgkmcnt(0)
	v_mfma_f32_16x16x128_f8f6f4 v[158:161], v[2:9], v[210:217], v[158:161]
	v_mfma_f32_16x16x128_f8f6f4 v[154:157], v[10:17], v[210:217], v[154:157]
	v_mfma_f32_16x16x128_f8f6f4 v[146:149], v[2:9], v[218:225], v[146:149]
	v_mfma_f32_16x16x128_f8f6f4 v[138:141], v[10:17], v[218:225], v[138:141]
	v_mfma_f32_16x16x128_f8f6f4 v[130:133], v[2:9], v[226:233], v[130:133]
	v_mfma_f32_16x16x128_f8f6f4 v[122:125], v[10:17], v[226:233], v[122:125]
	v_mfma_f32_16x16x128_f8f6f4 v[114:117], v[2:9], v[234:241], v[114:117]
	v_mfma_f32_16x16x128_f8f6f4 v[106:109], v[10:17], v[234:241], v[106:109]
	s_setprio 0
	s_setprio 1
	v_mfma_f32_16x16x128_f8f6f4 v[150:153], v[18:25], v[210:217], v[150:153]
	v_mfma_f32_16x16x128_f8f6f4 v[142:145], v[26:33], v[210:217], v[142:145]
	v_mfma_f32_16x16x128_f8f6f4 v[134:137], v[18:25], v[218:225], v[134:137]
	v_mfma_f32_16x16x128_f8f6f4 v[126:129], v[26:33], v[218:225], v[126:129]
	v_mfma_f32_16x16x128_f8f6f4 v[118:121], v[18:25], v[226:233], v[118:121]
	v_mfma_f32_16x16x128_f8f6f4 v[110:113], v[26:33], v[226:233], v[110:113]
	v_mfma_f32_16x16x128_f8f6f4 v[102:105], v[18:25], v[234:241], v[102:105]
	v_mfma_f32_16x16x128_f8f6f4 v[98:101], v[26:33], v[234:241], v[98:101]
	s_setprio 0
	s_barrier
	s_mov_b32 m0, s62
	v_lshl_add_u64 v[176:177], v[176:177], 0, s[12:13]
	s_add_u32 s46, s50, 0xe0080
	ds_read_b128 v[210:213], v207 offset:49152
	ds_read_b128 v[218:221], v207 offset:51200
	ds_read_b128 v[214:217], v208 offset:49152
	ds_read_b128 v[222:225], v208 offset:51200
	ds_read_b128 v[226:229], v207 offset:53248
	ds_read_b128 v[234:237], v207 offset:55296
	ds_read_b128 v[230:233], v208 offset:53248
	ds_read_b128 v[238:241], v208 offset:55296
	global_load_lds_dwordx4 v[176:177], off
	v_lshl_add_u64 v[176:177], v[178:179], 0, s[12:13]
	s_mov_b32 m0, s63
	s_addc_u32 s47, s51, 0
	global_load_lds_dwordx4 v[176:177], off
	v_lshl_add_u64 v[176:177], s[46:47], 0, v[166:167]
	s_mov_b32 m0, s66
	s_nop 0
	global_load_lds_dwordx4 v[176:177], off
	v_lshl_add_u64 v[176:177], s[46:47], 0, v[162:163]
	s_mov_b32 m0, s67
	s_nop 0
	global_load_lds_dwordx4 v[176:177], off
	v_lshl_add_u64 v[176:177], v[180:181], 0, s[12:13]
	s_mov_b32 m0, s64
	s_nop 0
	global_load_lds_dwordx4 v[176:177], off
	v_lshl_add_u64 v[176:177], v[182:183], 0, s[12:13]
	s_mov_b32 m0, s65
	s_nop 0
	global_load_lds_dwordx4 v[176:177], off
	s_waitcnt vmcnt(8)
	s_waitcnt lgkmcnt(0)
	s_barrier
	s_setprio 1
	s_waitcnt lgkmcnt(0)
	v_mfma_f32_16x16x128_f8f6f4 v[94:97], v[2:9], v[210:217], v[94:97]
	v_mfma_f32_16x16x128_f8f6f4 v[90:93], v[10:17], v[210:217], v[90:93]
	v_mfma_f32_16x16x128_f8f6f4 v[82:85], v[2:9], v[218:225], v[82:85]
	v_mfma_f32_16x16x128_f8f6f4 v[74:77], v[10:17], v[218:225], v[74:77]
	v_mfma_f32_16x16x128_f8f6f4 v[66:69], v[2:9], v[226:233], v[66:69]
	v_mfma_f32_16x16x128_f8f6f4 v[58:61], v[10:17], v[226:233], v[58:61]
	v_mfma_f32_16x16x128_f8f6f4 v[50:53], v[2:9], v[234:241], v[50:53]
	v_mfma_f32_16x16x128_f8f6f4 v[42:45], v[10:17], v[234:241], v[42:45]
	s_setprio 0
	s_setprio 1
	v_mfma_f32_16x16x128_f8f6f4 v[86:89], v[18:25], v[210:217], v[86:89]
	v_mfma_f32_16x16x128_f8f6f4 v[78:81], v[26:33], v[210:217], v[78:81]
	v_mfma_f32_16x16x128_f8f6f4 v[70:73], v[18:25], v[218:225], v[70:73]
	v_mfma_f32_16x16x128_f8f6f4 v[62:65], v[26:33], v[218:225], v[62:65]
	s_add_i32 s88, s88, 2
	s_add_u32 s86, s86, 0x100
	s_addc_u32 s87, s87, 0
	s_cmp_gt_u32 s88, 11
	s_mov_b64 s[46:47], s[48:49]
	v_mfma_f32_16x16x128_f8f6f4 v[54:57], v[18:25], v[226:233], v[54:57]
	v_mfma_f32_16x16x128_f8f6f4 v[46:49], v[26:33], v[226:233], v[46:49]
	v_mfma_f32_16x16x128_f8f6f4 v[38:41], v[18:25], v[234:241], v[38:41]
	v_mfma_f32_16x16x128_f8f6f4 v[34:37], v[26:33], v[234:241], v[34:37]
	s_setprio 0
	s_barrier
	s_cbranch_scc0 .LBB0_1497
	s_nop 15
	s_nop 15
	s_and_b64 vcc, exec, s[14:15]
	s_cbranch_vccz .LBB0_1500
	s_barrier
